# LDS-DMA: dropped the m0 save/restore SALU pair around all 288 global_load_lds (m0 has no other user)
# baseline (speedup 1.0000x reference)
.LBB0_191:
	v_readlane_b32 s0, v246, 32
	s_waitcnt vmcnt(7)
	v_mov_b32_e32 v2, v0
	v_readlane_b32 s1, v246, 33
	s_andn2_b64 vcc, exec, s[0:1]
	v_readfirstlane_b32 s0, v2
	s_cbranch_vccnz .LBB0_221
	v_ashrrev_i32_e32 v1, 31, v2
	v_lshrrev_b32_e32 v1, 26, v1
	v_add_u32_e32 v1, v2, v1
	v_ashrrev_i32_e32 v4, 6, v1
	v_bfe_i32 v1, v2, 27, 1
	v_lshlrev_b32_e32 v3, 4, v2
	v_lshrrev_b32_e32 v1, 22, v1
	v_add_u32_e32 v1, v3, v1
	v_and_b32_e32 v1, 0xfffffc00, v1
	v_sub_u32_e32 v1, v3, v1
	v_lshrrev_b32_e32 v5, 4, v1
	v_bitop3_b32 v5, v5, v1, 32 bitop3:0x6c
	s_waitcnt vmcnt(6)
	v_ashrrev_i32_e32 v6, 31, v5
	v_lshrrev_b32_e32 v6, 26, v6
	v_add_u32_e32 v6, v5, v6
	v_lshlrev_b32_e32 v1, 3, v4
	v_ashrrev_i32_e32 v7, 6, v6
	v_and_b32_e32 v6, 0xc0, v6
	v_and_b32_e32 v1, -16, v1
	v_lshlrev_b32_e32 v4, 5, v4
	v_sub_u32_e32 v5, v5, v6
	v_add_u32_e32 v1, v7, v1
	v_and_b32_e32 v4, 32, v4
	v_ashrrev_i16_sdwa v5, v203, sext(v5) dst_sel:DWORD dst_unused:UNUSED_PAD src0_sel:DWORD src1_sel:BYTE_0
	v_add_u32_sdwa v194, v4, sext(v5) dst_sel:DWORD dst_unused:UNUSED_PAD src0_sel:DWORD src1_sel:WORD_0
	v_lshlrev_b32_e32 v4, 1, v1
	v_lshrrev_b32_e32 v5, 2, v1
	v_and_b32_e32 v6, 3, v7
	s_mov_b32 s4, 0x7fffe0
	v_and_b32_e32 v4, 24, v4
	v_and_b32_e32 v5, 4, v5
	v_and_or_b32 v6, v1, s4, v6
	v_or3_b32 v4, v6, v5, v4
	v_lshlrev_b32_e32 v5, 1, v194
	v_add_u32_e32 v3, 0x2000, v3
	v_lshl_add_u32 v210, v4, 9, v5
	v_ashrrev_i32_e32 v4, 31, v3
	v_lshrrev_b32_e32 v4, 22, v4
	v_add_u32_e32 v4, v3, v4
	v_ashrrev_i32_e32 v4, 10, v4
	v_mul_i32_i24_e32 v5, 0x400, v4
	v_sub_u32_e32 v3, v3, v5
	v_lshrrev_b32_e32 v5, 4, v3
	v_bitop3_b32 v3, v5, v3, 32 bitop3:0x6c
	v_ashrrev_i32_e32 v6, 31, v3
	v_lshrrev_b32_e32 v6, 26, v6
	v_lshlrev_b32_e32 v5, 3, v4
	v_add_u32_e32 v6, v3, v6
	v_and_b32_e32 v5, -16, v5
	v_ashrrev_i32_e32 v7, 6, v6
	v_add_u32_e32 v211, v7, v5
	v_and_b32_e32 v5, 0xc0, v6
	v_lshlrev_b32_e32 v4, 5, v4
	v_sub_u32_e32 v3, v3, v5
	v_and_b32_e32 v4, 32, v4
	v_ashrrev_i16_sdwa v3, v203, sext(v3) dst_sel:DWORD dst_unused:UNUSED_PAD src0_sel:DWORD src1_sel:BYTE_0
	v_add_u32_sdwa v212, v4, sext(v3) dst_sel:DWORD dst_unused:UNUSED_PAD src0_sel:DWORD src1_sel:WORD_0
	v_lshlrev_b32_e32 v3, 1, v211
	v_lshrrev_b32_e32 v4, 2, v211
	v_and_b32_e32 v5, 3, v7
	s_ashr_i32 s6, s0, 6
	v_and_b32_e32 v3, 24, v3
	v_and_b32_e32 v4, 4, v4
	v_and_or_b32 v5, v211, s4, v5
	s_lshl_b32 s4, s6, 10
	v_or3_b32 v3, v5, v4, v3
	v_lshlrev_b32_e32 v4, 1, v212
	v_readlane_b32 s5, v246, 37
	v_readlane_b32 s7, v246, 36
	s_add_i32 s30, s4, 0
	v_readlane_b32 s8, v246, 41
	v_lshl_add_u32 v213, v3, 9, v4
	v_add_u32_e32 v3, s5, v1
	v_add_lshl_u32 v4, v194, s7, 1
	s_add_i32 s31, s30, 0x10000
	v_readlane_b32 s9, v246, 42
	s_mov_b32 m0, s31
	s_nop 0
	global_load_lds_dwordx4 v210, s[8:9]
	s_ashr_i32 s1, s0, 8
	v_lshl_add_u32 v222, v3, 11, v4
	v_add_u32_e32 v3, s5, v211
	v_add_lshl_u32 v5, v212, s7, 1
	v_readlane_b32 s5, v246, 38
	s_add_i32 s34, s30, 0x12000
	s_mov_b32 m0, s34
	s_nop 0
	global_load_lds_dwordx4 v213, s[8:9]
	v_lshl_add_u32 v223, v3, 11, v5
	v_add_u32_e32 v3, s5, v1
	s_add_u32 s4, s8, 0x10000
	v_lshl_add_u32 v224, v3, 11, v4
	v_add_u32_e32 v3, s5, v211
	s_addc_u32 s5, s9, 0
	s_add_i32 s35, s30, 0x14000
	s_mov_b32 m0, s35
	s_nop 0
	global_load_lds_dwordx4 v210, s[4:5]
	s_add_i32 s36, s30, 0x16000
	s_mov_b32 m0, s36
	s_nop 0
	global_load_lds_dwordx4 v213, s[4:5]
	v_readlane_b32 s8, v246, 34
	v_readlane_b32 s9, v246, 35
	s_mov_b32 m0, s30
	s_nop 0
	global_load_lds_dwordx4 v222, s[8:9]
	s_add_i32 s37, s30, 0x2000
	s_mov_b32 m0, s37
	s_nop 0
	global_load_lds_dwordx4 v223, s[8:9]
	s_add_i32 s38, s30, 0x4000
	s_mov_b32 m0, s38
	s_nop 0
	global_load_lds_dwordx4 v224, s[8:9]
	v_lshl_add_u32 v225, v3, 11, v5
	s_add_i32 s39, s30, 0x6000
	s_mov_b32 m0, s39
	s_nop 0
	global_load_lds_dwordx4 v225, s[8:9]
	s_cmp_eq_u32 s1, 1
	s_cselect_b64 s[4:5], -1, 0
	s_cmp_lg_u32 s1, 1
	s_cbranch_scc1 .LBB0_194
	s_barrier
.LBB0_194:
	v_lshrrev_b32_e32 v4, 1, v2
	v_and_b32_e32 v4, 24, v4
	v_and_b32_e32 v3, 15, v2
	v_lshlrev_b32_e32 v5, 1, v4
	v_lshlrev_b32_e32 v2, 2, v2
	v_lshl_or_b32 v214, s1, 6, v3
	v_lshl_or_b32 v3, v3, 6, v5
	s_lshl_b32 s1, s1, 13
	v_and_b32_e32 v2, 32, v2
	v_bitop3_b32 v5, v3, s1, v2 bitop3:0xde
	s_lshl_b32 s1, s6, 5
	s_and_b32 s1, s1, 0x60
	s_lshl_b32 s6, s1, 7
	v_readlane_b32 s12, v246, 41
	v_bitop3_b32 v2, v3, s6, v2 bitop3:0xde
	v_readlane_b32 s13, v246, 42
	s_add_u32 s6, s12, 0x80
	s_waitcnt vmcnt(2)
	s_barrier
	s_addc_u32 s7, s13, 0
	s_add_i32 s40, s30, 0x18000
	s_mov_b32 m0, s40
	s_nop 0
	global_load_lds_dwordx4 v210, s[6:7]
	s_add_i32 s41, s30, 0x1a000
	s_mov_b32 m0, s41
	s_nop 0
	global_load_lds_dwordx4 v213, s[6:7]
	v_readlane_b32 s6, v246, 34
	v_readlane_b32 s7, v246, 35
	s_add_u32 s6, s6, 0x80
	s_addc_u32 s7, s7, 0
	s_add_i32 s42, s30, 0x8000
	s_mov_b32 m0, s42
	s_nop 0
	global_load_lds_dwordx4 v222, s[6:7]
	s_add_i32 s43, s30, 0xa000
	s_mov_b32 m0, s43
	s_nop 0
	global_load_lds_dwordx4 v223, s[6:7]
	s_add_u32 s8, s12, 0x10080
	s_addc_u32 s9, s13, 0
	s_add_i32 s44, s30, 0x1c000
	s_mov_b32 m0, s44
	s_nop 0
	global_load_lds_dwordx4 v210, s[8:9]
	s_add_i32 s45, s30, 0x1e000
	s_mov_b32 m0, s45
	s_nop 0
	global_load_lds_dwordx4 v213, s[8:9]
	s_add_i32 s47, s30, 0xc000
	s_waitcnt vmcnt(6)
	s_cmpk_lt_u32 s0, 0x100
	v_or_b32_e32 v215, s1, v4
	v_readlane_b32 s0, v243, 32
	v_readlane_b32 s1, v243, 33
	s_cselect_b64 s[8:9], -1, 0
	s_add_i32 s48, s30, 0xe000
	s_mov_b32 s16, 0
	v_add_u32_e32 v216, 0, v2
	v_add_u32_e32 v217, 0, v5
	v_readlane_b32 s51, v243, 20
	s_mov_b32 s52, s0
	s_mov_b64 s[0:1], s[12:13]
	v_mov_b32_e32 v218, v222
	v_mov_b32_e32 v219, v223
	v_mov_b32_e32 v220, v224
	v_mov_b32_e32 v221, v225
	s_mov_b64 s[10:11], s[12:13]
	s_barrier
	s_waitcnt vmcnt(0)
	s_branch .LBB0_197

.LBB0_200:
	s_xor_b64 s[24:25], s[18:19], -1
	s_add_u32 s18, s26, 0x80
	s_addc_u32 s19, s27, 0
	s_waitcnt lgkmcnt(0)
	s_add_u32 s20, s22, 0x80
	s_addc_u32 s21, s23, 0
	s_barrier
	s_setprio 1
	s_waitcnt lgkmcnt(7)
	v_mfma_f32_16x16x32_bf16 v[126:129], v[146:149], v[186:189], v[126:129]
	v_mfma_f32_16x16x32_bf16 v[122:125], v[154:157], v[186:189], v[122:125]
	s_waitcnt lgkmcnt(5)
	v_mfma_f32_16x16x32_bf16 v[118:121], v[146:149], v[178:181], v[118:121]
	v_mfma_f32_16x16x32_bf16 v[110:113], v[154:157], v[178:181], v[110:113]
	s_waitcnt lgkmcnt(3)
	v_mfma_f32_16x16x32_bf16 v[102:105], v[146:149], v[170:173], v[102:105]
	v_mfma_f32_16x16x32_bf16 v[94:97], v[154:157], v[170:173], v[94:97]
	s_waitcnt lgkmcnt(1)
	v_mfma_f32_16x16x32_bf16 v[82:85], v[146:149], v[162:165], v[82:85]
	v_mfma_f32_16x16x32_bf16 v[74:77], v[154:157], v[162:165], v[74:77]
	v_mfma_f32_16x16x32_bf16 v[126:129], v[150:153], v[190:193], v[126:129]
	v_mfma_f32_16x16x32_bf16 v[122:125], v[158:161], v[190:193], v[122:125]
	v_mfma_f32_16x16x32_bf16 v[118:121], v[150:153], v[182:185], v[118:121]
	v_mfma_f32_16x16x32_bf16 v[110:113], v[158:161], v[182:185], v[110:113]
	v_mfma_f32_16x16x32_bf16 v[102:105], v[150:153], v[174:177], v[102:105]
	v_mfma_f32_16x16x32_bf16 v[94:97], v[158:161], v[174:177], v[94:97]
	s_waitcnt lgkmcnt(0)
	v_mfma_f32_16x16x32_bf16 v[82:85], v[150:153], v[166:169], v[82:85]
	v_mfma_f32_16x16x32_bf16 v[74:77], v[158:161], v[166:169], v[74:77]
	s_setprio 0
	s_setprio 1
	v_mfma_f32_16x16x32_bf16 v[114:117], v[130:133], v[186:189], v[114:117]
	v_mfma_f32_16x16x32_bf16 v[106:109], v[138:141], v[186:189], v[106:109]
	v_mfma_f32_16x16x32_bf16 v[98:101], v[130:133], v[178:181], v[98:101]
	v_mfma_f32_16x16x32_bf16 v[90:93], v[138:141], v[178:181], v[90:93]
	v_mfma_f32_16x16x32_bf16 v[86:89], v[130:133], v[170:173], v[86:89]
	v_mfma_f32_16x16x32_bf16 v[78:81], v[138:141], v[170:173], v[78:81]
	v_mfma_f32_16x16x32_bf16 v[70:73], v[130:133], v[162:165], v[70:73]
	v_mfma_f32_16x16x32_bf16 v[66:69], v[138:141], v[162:165], v[66:69]
	v_mfma_f32_16x16x32_bf16 v[114:117], v[134:137], v[190:193], v[114:117]
	v_mfma_f32_16x16x32_bf16 v[106:109], v[142:145], v[190:193], v[106:109]
	v_mfma_f32_16x16x32_bf16 v[98:101], v[134:137], v[182:185], v[98:101]
	v_mfma_f32_16x16x32_bf16 v[90:93], v[142:145], v[182:185], v[90:93]
	v_mfma_f32_16x16x32_bf16 v[86:89], v[134:137], v[174:177], v[86:89]
	v_mfma_f32_16x16x32_bf16 v[78:81], v[142:145], v[174:177], v[78:81]
	v_mfma_f32_16x16x32_bf16 v[70:73], v[134:137], v[166:169], v[70:73]
	v_mfma_f32_16x16x32_bf16 v[66:69], v[142:145], v[166:169], v[66:69]
	s_setprio 0
	s_barrier
	ds_read_b128 v[162:165], v217 offset:49152
	ds_read_b128 v[166:169], v217 offset:50176
	ds_read_b128 v[170:173], v217 offset:51200
	ds_read_b128 v[174:177], v217 offset:52224
	ds_read_b128 v[178:181], v217 offset:53248
	ds_read_b128 v[182:185], v217 offset:54272
	ds_read_b128 v[186:189], v217 offset:55296
	ds_read_b128 v[190:193], v217 offset:56320
	s_mov_b32 m0, s40
	s_nop 0
	global_load_lds_dwordx4 v210, s[20:21]
	s_nop 0
	s_mov_b32 m0, s41
	s_nop 0
	global_load_lds_dwordx4 v213, s[20:21]
	s_add_u32 s20, s22, 0x10080
	s_addc_u32 s21, s23, 0
	s_mov_b32 m0, s44
	s_nop 0
	global_load_lds_dwordx4 v210, s[20:21]
	s_nop 0
	s_mov_b32 m0, s45
	s_nop 0
	global_load_lds_dwordx4 v213, s[20:21]
	s_nop 0
	s_mov_b32 m0, s42
	s_nop 0
	global_load_lds_dwordx4 v227, s[18:19]
	s_nop 0
	s_mov_b32 m0, s43
	s_nop 0
	global_load_lds_dwordx4 v226, s[18:19]
	s_waitcnt vmcnt(8)
	s_waitcnt lgkmcnt(0)
	s_barrier
	s_setprio 1
	s_waitcnt lgkmcnt(7)
	v_mfma_f32_16x16x32_bf16 v[62:65], v[146:149], v[162:165], v[62:65]
	v_mfma_f32_16x16x32_bf16 v[58:61], v[154:157], v[162:165], v[58:61]
	s_waitcnt lgkmcnt(5)
	v_mfma_f32_16x16x32_bf16 v[46:49], v[146:149], v[170:173], v[46:49]
	v_mfma_f32_16x16x32_bf16 v[38:41], v[154:157], v[170:173], v[38:41]
	s_waitcnt lgkmcnt(3)
	v_mfma_f32_16x16x32_bf16 v[22:25], v[146:149], v[178:181], v[22:25]
	v_mfma_f32_16x16x32_bf16 v[14:17], v[154:157], v[178:181], v[14:17]
	s_waitcnt lgkmcnt(1)
	v_mfma_f32_16x16x32_bf16 v[6:9], v[146:149], v[186:189], v[6:9]
	v_mfma_f32_16x16x32_bf16 v[2:5], v[154:157], v[186:189], v[2:5]
	v_mfma_f32_16x16x32_bf16 v[62:65], v[150:153], v[166:169], v[62:65]
	v_mfma_f32_16x16x32_bf16 v[58:61], v[158:161], v[166:169], v[58:61]
	v_mfma_f32_16x16x32_bf16 v[46:49], v[150:153], v[174:177], v[46:49]
	v_mfma_f32_16x16x32_bf16 v[38:41], v[158:161], v[174:177], v[38:41]
	v_mfma_f32_16x16x32_bf16 v[22:25], v[150:153], v[182:185], v[22:25]
	v_mfma_f32_16x16x32_bf16 v[14:17], v[158:161], v[182:185], v[14:17]
	s_waitcnt lgkmcnt(0)
	v_mfma_f32_16x16x32_bf16 v[6:9], v[150:153], v[190:193], v[6:9]
	v_mfma_f32_16x16x32_bf16 v[2:5], v[158:161], v[190:193], v[2:5]
	s_setprio 0
	s_setprio 1
	v_mfma_f32_16x16x32_bf16 v[42:45], v[130:133], v[162:165], v[42:45]
	v_mfma_f32_16x16x32_bf16 v[34:37], v[138:141], v[162:165], v[34:37]
	v_mfma_f32_16x16x32_bf16 v[18:21], v[130:133], v[170:173], v[18:21]
	v_mfma_f32_16x16x32_bf16 v[10:13], v[138:141], v[170:173], v[10:13]
	v_mfma_f32_16x16x32_bf16 v[54:57], v[130:133], v[178:181], v[54:57]
	v_mfma_f32_16x16x32_bf16 v[50:53], v[138:141], v[178:181], v[50:53]
	v_mfma_f32_16x16x32_bf16 v[30:33], v[130:133], v[186:189], v[30:33]
	v_mfma_f32_16x16x32_bf16 v[26:29], v[138:141], v[186:189], v[26:29]
	v_mfma_f32_16x16x32_bf16 v[42:45], v[134:137], v[166:169], v[42:45]
	v_mfma_f32_16x16x32_bf16 v[34:37], v[142:145], v[166:169], v[34:37]
	v_mfma_f32_16x16x32_bf16 v[18:21], v[134:137], v[174:177], v[18:21]
	v_mfma_f32_16x16x32_bf16 v[10:13], v[142:145], v[174:177], v[10:13]
	v_mfma_f32_16x16x32_bf16 v[54:57], v[134:137], v[182:185], v[54:57]
	v_mfma_f32_16x16x32_bf16 v[50:53], v[142:145], v[182:185], v[50:53]
	v_mfma_f32_16x16x32_bf16 v[30:33], v[134:137], v[190:193], v[30:33]
	v_mfma_f32_16x16x32_bf16 v[26:29], v[142:145], v[190:193], v[26:29]
	s_setprio 0
	s_barrier
	s_mov_b64 s[22:23], 0x100
	s_mov_b64 s[18:19], 0
	s_mov_b64 s[20:21], -1
	s_and_b64 vcc, exec, s[24:25]
	s_cbranch_vccnz .LBB0_213
.LBB0_201:
	v_add_u32_e32 v130, 0x10000, v216
	v_add_u32_e32 v142, 0x14000, v216
	ds_read_b128 v[146:149], v130
	ds_read_b128 v[150:153], v130 offset:1024
	ds_read_b128 v[154:157], v130 offset:2048
	ds_read_b128 v[158:161], v130 offset:3072
	ds_read_b128 v[130:133], v142
	ds_read_b128 v[134:137], v142 offset:1024
	ds_read_b128 v[138:141], v142 offset:2048
	ds_read_b128 v[142:145], v142 offset:3072
	v_readlane_b32 s24, v246, 34
	v_readlane_b32 s25, v246, 35
	s_add_u32 s13, s24, s22
	s_addc_u32 s28, s25, s23
	ds_read_b128 v[186:189], v217
	ds_read_b128 v[190:193], v217 offset:1024
	ds_read_b128 v[178:181], v217 offset:2048
	ds_read_b128 v[182:185], v217 offset:3072
	ds_read_b128 v[170:173], v217 offset:4096
	ds_read_b128 v[174:177], v217 offset:5120
	ds_read_b128 v[162:165], v217 offset:6144
	ds_read_b128 v[166:169], v217 offset:7168
	s_and_b64 s[24:25], s[16:17], s[18:19]
	s_and_b64 vcc, exec, s[24:25]
	s_mov_b64 s[26:27], -1
	s_cbranch_vccnz .LBB0_203
	s_add_u32 s26, s13, 0x80
	s_addc_u32 s27, s28, 0
	s_mov_b32 m0, s47
	s_nop 0
	global_load_lds_dwordx4 v224, s[26:27]
	s_nop 0
	s_mov_b32 m0, s48
	s_nop 0
	global_load_lds_dwordx4 v225, s[26:27]
	s_waitcnt vmcnt(8)
	s_mov_b64 s[26:27], 0

.LBB0_205:
	s_xor_b64 s[24:25], s[24:25], -1
	s_add_u32 s13, s13, 0x100
	s_addc_u32 s28, s28, 0
	s_and_b64 s[26:27], s[20:21], exec
	v_readlane_b32 s26, v246, 34
	v_readlane_b32 s27, v246, 35
	s_cselect_b32 s27, s27, s28
	s_cselect_b32 s26, s26, s13
	s_add_u32 s13, s0, s22
	s_addc_u32 s22, s1, s23
	s_add_u32 s13, s13, 0x100
	s_addc_u32 s28, s22, 0
	s_waitcnt lgkmcnt(0)
	s_and_b64 s[22:23], s[20:21], exec
	v_cndmask_b32_e64 v227, v222, v218, s[20:21]
	v_cndmask_b32_e64 v226, v223, v219, s[20:21]
	s_cselect_b32 s23, s11, s28
	s_cselect_b32 s22, s10, s13
	s_barrier
	s_setprio 1
	s_waitcnt lgkmcnt(7)
	v_mfma_f32_16x16x32_bf16 v[126:129], v[146:149], v[186:189], v[126:129]
	v_mfma_f32_16x16x32_bf16 v[122:125], v[154:157], v[186:189], v[122:125]
	s_waitcnt lgkmcnt(5)
	v_mfma_f32_16x16x32_bf16 v[118:121], v[146:149], v[178:181], v[118:121]
	v_mfma_f32_16x16x32_bf16 v[110:113], v[154:157], v[178:181], v[110:113]
	s_waitcnt lgkmcnt(3)
	v_mfma_f32_16x16x32_bf16 v[102:105], v[146:149], v[170:173], v[102:105]
	v_mfma_f32_16x16x32_bf16 v[94:97], v[154:157], v[170:173], v[94:97]
	s_waitcnt lgkmcnt(1)
	v_mfma_f32_16x16x32_bf16 v[82:85], v[146:149], v[162:165], v[82:85]
	v_mfma_f32_16x16x32_bf16 v[74:77], v[154:157], v[162:165], v[74:77]
	v_mfma_f32_16x16x32_bf16 v[126:129], v[150:153], v[190:193], v[126:129]
	v_mfma_f32_16x16x32_bf16 v[122:125], v[158:161], v[190:193], v[122:125]
	v_mfma_f32_16x16x32_bf16 v[118:121], v[150:153], v[182:185], v[118:121]
	v_mfma_f32_16x16x32_bf16 v[110:113], v[158:161], v[182:185], v[110:113]
	v_mfma_f32_16x16x32_bf16 v[102:105], v[150:153], v[174:177], v[102:105]
	v_mfma_f32_16x16x32_bf16 v[94:97], v[158:161], v[174:177], v[94:97]
	s_waitcnt lgkmcnt(0)
	v_mfma_f32_16x16x32_bf16 v[82:85], v[150:153], v[166:169], v[82:85]
	v_mfma_f32_16x16x32_bf16 v[74:77], v[158:161], v[166:169], v[74:77]
	s_setprio 0
	s_setprio 1
	v_mfma_f32_16x16x32_bf16 v[114:117], v[130:133], v[186:189], v[114:117]
	v_mfma_f32_16x16x32_bf16 v[106:109], v[138:141], v[186:189], v[106:109]
	v_mfma_f32_16x16x32_bf16 v[98:101], v[130:133], v[178:181], v[98:101]
	v_mfma_f32_16x16x32_bf16 v[90:93], v[138:141], v[178:181], v[90:93]
	v_mfma_f32_16x16x32_bf16 v[86:89], v[130:133], v[170:173], v[86:89]
	v_mfma_f32_16x16x32_bf16 v[78:81], v[138:141], v[170:173], v[78:81]
	v_mfma_f32_16x16x32_bf16 v[70:73], v[130:133], v[162:165], v[70:73]
	v_mfma_f32_16x16x32_bf16 v[66:69], v[138:141], v[162:165], v[66:69]
	v_mfma_f32_16x16x32_bf16 v[114:117], v[134:137], v[190:193], v[114:117]
	v_mfma_f32_16x16x32_bf16 v[106:109], v[142:145], v[190:193], v[106:109]
	v_mfma_f32_16x16x32_bf16 v[98:101], v[134:137], v[182:185], v[98:101]
	v_mfma_f32_16x16x32_bf16 v[90:93], v[142:145], v[182:185], v[90:93]
	v_mfma_f32_16x16x32_bf16 v[86:89], v[134:137], v[174:177], v[86:89]
	v_mfma_f32_16x16x32_bf16 v[78:81], v[142:145], v[174:177], v[78:81]
	v_mfma_f32_16x16x32_bf16 v[70:73], v[134:137], v[166:169], v[70:73]
	v_mfma_f32_16x16x32_bf16 v[66:69], v[142:145], v[166:169], v[66:69]
	s_setprio 0
	s_barrier
	ds_read_b128 v[186:189], v217 offset:16384
	ds_read_b128 v[190:193], v217 offset:17408
	ds_read_b128 v[178:181], v217 offset:18432
	ds_read_b128 v[182:185], v217 offset:19456
	ds_read_b128 v[170:173], v217 offset:20480
	ds_read_b128 v[174:177], v217 offset:21504
	ds_read_b128 v[162:165], v217 offset:22528
	ds_read_b128 v[166:169], v217 offset:23552
	s_mov_b32 m0, s31
	s_nop 0
	global_load_lds_dwordx4 v210, s[22:23]
	s_add_u32 s28, s22, 0x10000
	s_mov_b32 m0, s34
	s_nop 0
	global_load_lds_dwordx4 v213, s[22:23]
	s_addc_u32 s29, s23, 0
	s_mov_b32 m0, s35
	s_nop 0
	global_load_lds_dwordx4 v210, s[28:29]
	s_and_b64 vcc, exec, s[24:25]
	s_mov_b32 m0, s36
	s_nop 0
	global_load_lds_dwordx4 v213, s[28:29]
	s_mov_b64 s[28:29], -1
	s_mov_b32 m0, s30
	s_nop 0
	global_load_lds_dwordx4 v227, s[26:27]
	s_nop 0
	s_mov_b32 m0, s37
	s_nop 0
	global_load_lds_dwordx4 v226, s[26:27]
	s_cbranch_vccz .LBB0_207
	s_waitcnt vmcnt(8)
	s_mov_b64 s[28:29], 0

.LBB0_209:
	s_waitcnt lgkmcnt(0)
	v_cndmask_b32_e64 v228, v224, v220, s[20:21]
	v_cndmask_b32_e64 v229, v225, v221, s[20:21]
	s_barrier
	s_setprio 1
	s_waitcnt lgkmcnt(7)
	v_mfma_f32_16x16x32_bf16 v[62:65], v[146:149], v[186:189], v[62:65]
	v_mfma_f32_16x16x32_bf16 v[58:61], v[154:157], v[186:189], v[58:61]
	s_waitcnt lgkmcnt(5)
	v_mfma_f32_16x16x32_bf16 v[46:49], v[146:149], v[178:181], v[46:49]
	v_mfma_f32_16x16x32_bf16 v[38:41], v[154:157], v[178:181], v[38:41]
	s_waitcnt lgkmcnt(3)
	v_mfma_f32_16x16x32_bf16 v[22:25], v[146:149], v[170:173], v[22:25]
	v_mfma_f32_16x16x32_bf16 v[14:17], v[154:157], v[170:173], v[14:17]
	s_waitcnt lgkmcnt(1)
	v_mfma_f32_16x16x32_bf16 v[6:9], v[146:149], v[162:165], v[6:9]
	v_mfma_f32_16x16x32_bf16 v[2:5], v[154:157], v[162:165], v[2:5]
	v_mfma_f32_16x16x32_bf16 v[62:65], v[150:153], v[190:193], v[62:65]
	v_mfma_f32_16x16x32_bf16 v[58:61], v[158:161], v[190:193], v[58:61]
	v_mfma_f32_16x16x32_bf16 v[46:49], v[150:153], v[182:185], v[46:49]
	v_mfma_f32_16x16x32_bf16 v[38:41], v[158:161], v[182:185], v[38:41]
	v_mfma_f32_16x16x32_bf16 v[22:25], v[150:153], v[174:177], v[22:25]
	v_mfma_f32_16x16x32_bf16 v[14:17], v[158:161], v[174:177], v[14:17]
	s_waitcnt lgkmcnt(0)
	v_mfma_f32_16x16x32_bf16 v[6:9], v[150:153], v[166:169], v[6:9]
	v_mfma_f32_16x16x32_bf16 v[2:5], v[158:161], v[166:169], v[2:5]
	s_setprio 0
	s_setprio 1
	v_mfma_f32_16x16x32_bf16 v[42:45], v[130:133], v[186:189], v[42:45]
	v_mfma_f32_16x16x32_bf16 v[34:37], v[138:141], v[186:189], v[34:37]
	v_mfma_f32_16x16x32_bf16 v[18:21], v[130:133], v[178:181], v[18:21]
	v_mfma_f32_16x16x32_bf16 v[10:13], v[138:141], v[178:181], v[10:13]
	v_mfma_f32_16x16x32_bf16 v[54:57], v[130:133], v[170:173], v[54:57]
	v_mfma_f32_16x16x32_bf16 v[50:53], v[138:141], v[170:173], v[50:53]
	v_mfma_f32_16x16x32_bf16 v[30:33], v[130:133], v[162:165], v[30:33]
	v_mfma_f32_16x16x32_bf16 v[26:29], v[138:141], v[162:165], v[26:29]
	v_mfma_f32_16x16x32_bf16 v[42:45], v[134:137], v[190:193], v[42:45]
	v_mfma_f32_16x16x32_bf16 v[34:37], v[142:145], v[190:193], v[34:37]
	v_mfma_f32_16x16x32_bf16 v[18:21], v[134:137], v[182:185], v[18:21]
	v_mfma_f32_16x16x32_bf16 v[10:13], v[142:145], v[182:185], v[10:13]
	v_mfma_f32_16x16x32_bf16 v[54:57], v[134:137], v[174:177], v[54:57]
	v_mfma_f32_16x16x32_bf16 v[50:53], v[142:145], v[174:177], v[50:53]
	v_mfma_f32_16x16x32_bf16 v[30:33], v[134:137], v[166:169], v[30:33]
	v_mfma_f32_16x16x32_bf16 v[26:29], v[142:145], v[166:169], v[26:29]
	s_setprio 0
	s_barrier
	v_add_u32_e32 v130, 0x18000, v216
	v_add_u32_e32 v142, 0x1c000, v216
	ds_read_b128 v[146:149], v130
	ds_read_b128 v[150:153], v130 offset:1024
	ds_read_b128 v[154:157], v130 offset:2048
	ds_read_b128 v[158:161], v130 offset:3072
	ds_read_b128 v[130:133], v142
	ds_read_b128 v[134:137], v142 offset:1024
	ds_read_b128 v[138:141], v142 offset:2048
	ds_read_b128 v[142:145], v142 offset:3072
	ds_read_b128 v[186:189], v217 offset:32768
	ds_read_b128 v[190:193], v217 offset:33792
	ds_read_b128 v[178:181], v217 offset:34816
	ds_read_b128 v[182:185], v217 offset:35840
	ds_read_b128 v[170:173], v217 offset:36864
	ds_read_b128 v[174:177], v217 offset:37888
	ds_read_b128 v[162:165], v217 offset:38912
	ds_read_b128 v[166:169], v217 offset:39936
	s_mov_b32 m0, s38
	s_nop 0
	global_load_lds_dwordx4 v228, s[26:27]
	s_mov_b64 s[20:21], -1
	s_mov_b32 m0, s39
	s_nop 0
	global_load_lds_dwordx4 v229, s[26:27]
	s_and_b64 vcc, exec, s[24:25]
	s_cbranch_vccz .LBB0_211
	s_waitcnt vmcnt(8)
	s_mov_b64 s[20:21], 0

.LBB0_213:
	v_cndmask_b32_e64 v130, 0, 1, s[14:15]
	v_cmp_ne_u32_e64 s[0:1], 1, v130
	s_andn2_b64 vcc, exec, s[14:15]
	s_cbranch_vccnz .LBB0_215
	s_mov_b32 m0, s47
	s_nop 0
	global_load_lds_dwordx4 v220, s[6:7]
	s_nop 0
	s_mov_b32 m0, s48
	s_nop 0
	global_load_lds_dwordx4 v221, s[6:7]

.LBB0_278:
	s_andn2_b64 vcc, exec, s[0:1]
	s_cbranch_vccnz .LBB0_366
	v_readlane_b32 s0, v243, 1
	s_waitcnt vmcnt(7)
	v_mov_b32_e32 v2, v0
	v_readlane_b32 s1, v243, 2
	s_andn2_b64 vcc, exec, s[0:1]
	v_readfirstlane_b32 s0, v2
	s_cbranch_vccnz .LBB0_314
	v_ashrrev_i32_e32 v1, 31, v2
	v_lshrrev_b32_e32 v1, 26, v1
	v_add_u32_e32 v1, v2, v1
	v_ashrrev_i32_e32 v4, 6, v1
	v_bfe_i32 v1, v2, 27, 1
	v_lshlrev_b32_e32 v3, 4, v2
	v_lshrrev_b32_e32 v1, 22, v1
	v_add_u32_e32 v1, v3, v1
	v_and_b32_e32 v1, 0xfffffc00, v1
	v_sub_u32_e32 v1, v3, v1
	v_lshrrev_b32_e32 v5, 4, v1
	v_bitop3_b32 v5, v5, v1, 32 bitop3:0x6c
	s_waitcnt vmcnt(6)
	v_ashrrev_i32_e32 v6, 31, v5
	v_lshrrev_b32_e32 v6, 26, v6
	v_add_u32_e32 v6, v5, v6
	v_ashrrev_i32_e32 v7, 6, v6
	v_and_b32_e32 v6, 0xc0, v6
	v_sub_u32_e32 v5, v5, v6
	v_lshlrev_b32_e32 v1, 3, v4
	v_lshlrev_b32_e32 v4, 5, v4
	v_ashrrev_i16_sdwa v5, v203, sext(v5) dst_sel:DWORD dst_unused:UNUSED_PAD src0_sel:DWORD src1_sel:BYTE_0
	v_and_b32_e32 v4, 32, v4
	v_bfe_i32 v5, v5, 0, 16
	v_add_u32_e32 v3, 0x2000, v3
	v_add_lshl_u32 v210, v4, v5, 1
	v_ashrrev_i32_e32 v4, 31, v3
	v_lshrrev_b32_e32 v4, 22, v4
	v_add_u32_e32 v4, v3, v4
	v_and_b32_e32 v1, -16, v1
	v_ashrrev_i32_e32 v4, 10, v4
	v_add_u32_e32 v1, v7, v1
	v_mul_i32_i24_e32 v5, 0x400, v4
	v_lshlrev_b32_e32 v6, 1, v1
	v_lshrrev_b32_e32 v8, 2, v1
	v_and_b32_e32 v7, 3, v7
	s_mov_b32 s4, 0x3fffe0
	v_sub_u32_e32 v3, v3, v5
	v_and_b32_e32 v6, 24, v6
	v_and_b32_e32 v8, 4, v8
	v_and_or_b32 v7, v1, s4, v7
	v_lshrrev_b32_e32 v5, 4, v3
	v_or3_b32 v6, v7, v8, v6
	v_bitop3_b32 v3, v5, v3, 32 bitop3:0x6c
	v_lshl_add_u32 v211, v6, 10, v210
	v_ashrrev_i32_e32 v6, 31, v3
	v_lshrrev_b32_e32 v6, 26, v6
	v_lshlrev_b32_e32 v5, 3, v4
	v_add_u32_e32 v6, v3, v6
	v_and_b32_e32 v5, -16, v5
	v_ashrrev_i32_e32 v7, 6, v6
	v_add_u32_e32 v212, v7, v5
	v_and_b32_e32 v5, 0xc0, v6
	v_sub_u32_e32 v3, v3, v5
	v_and_b32_e32 v7, 3, v7
	s_ashr_i32 s6, s0, 6
	v_lshlrev_b32_e32 v4, 5, v4
	v_ashrrev_i16_sdwa v3, v203, sext(v3) dst_sel:DWORD dst_unused:UNUSED_PAD src0_sel:DWORD src1_sel:BYTE_0
	v_lshlrev_b32_e32 v5, 1, v212
	v_lshrrev_b32_e32 v6, 2, v212
	v_and_or_b32 v7, v212, s4, v7
	s_lshl_b32 s4, s6, 10
	v_and_b32_e32 v4, 32, v4
	v_bfe_i32 v3, v3, 0, 16
	v_and_b32_e32 v5, 24, v5
	v_and_b32_e32 v6, 4, v6
	v_readlane_b32 s5, v243, 4
	s_add_i32 s28, s4, 0
	v_readlane_b32 s8, v243, 10
	v_or3_b32 v5, v7, v6, v5
	v_add_lshl_u32 v213, v4, v3, 1
	v_add_u32_e32 v3, s5, v1
	s_add_i32 s29, s28, 0x10000
	v_readlane_b32 s9, v243, 11
	s_mov_b32 m0, s29
	s_nop 0
	global_load_lds_dwordx4 v211, s[8:9]
	s_ashr_i32 s1, s0, 8
	v_lshl_add_u32 v214, v5, 10, v213
	v_lshl_add_u32 v194, v3, 10, v210
	v_add_u32_e32 v3, s5, v212
	v_readlane_b32 s5, v243, 5
	s_add_i32 s30, s28, 0x12000
	s_mov_b32 m0, s30
	s_nop 0
	global_load_lds_dwordx4 v214, s[8:9]
	v_lshl_add_u32 v224, v3, 10, v213
	v_add_u32_e32 v3, s5, v1
	s_add_u32 s4, s8, 0x20000
	v_lshl_add_u32 v225, v3, 10, v210
	v_add_u32_e32 v3, s5, v212
	s_addc_u32 s5, s9, 0
	s_add_i32 s31, s28, 0x14000
	s_mov_b32 m0, s31
	s_nop 0
	global_load_lds_dwordx4 v211, s[4:5]
	s_add_i32 s34, s28, 0x16000
	s_mov_b32 m0, s34
	s_nop 0
	global_load_lds_dwordx4 v214, s[4:5]
	s_mov_b32 m0, s28
	s_nop 0
	global_load_lds_dwordx4 v194, s[2:3]
	s_add_i32 s35, s28, 0x2000
	s_mov_b32 m0, s35
	s_nop 0
	global_load_lds_dwordx4 v224, s[2:3]
	s_add_i32 s36, s28, 0x4000
	s_mov_b32 m0, s36
	s_nop 0
	global_load_lds_dwordx4 v225, s[2:3]
	v_lshl_add_u32 v226, v3, 10, v213
	s_add_i32 s37, s28, 0x6000
	s_mov_b32 m0, s37
	s_nop 0
	global_load_lds_dwordx4 v226, s[2:3]
	s_cmp_eq_u32 s1, 1
	s_cselect_b64 s[4:5], -1, 0
	s_cmp_lg_u32 s1, 1
	s_cbranch_scc1 .LBB0_282
	s_barrier
.LBB0_282:
	v_lshrrev_b32_e32 v4, 1, v2
	v_and_b32_e32 v4, 24, v4
	v_and_b32_e32 v3, 15, v2
	v_lshlrev_b32_e32 v5, 1, v4
	v_lshlrev_b32_e32 v2, 2, v2
	v_lshl_or_b32 v215, s1, 6, v3
	v_lshl_or_b32 v3, v3, 6, v5
	s_lshl_b32 s1, s1, 13
	v_and_b32_e32 v2, 32, v2
	v_bitop3_b32 v5, v3, s1, v2 bitop3:0xde
	s_lshl_b32 s1, s6, 5
	s_and_b32 s1, s1, 0x60
	s_lshl_b32 s6, s1, 7
	v_readlane_b32 s12, v243, 10
	v_bitop3_b32 v2, v3, s6, v2 bitop3:0xde
	v_readlane_b32 s13, v243, 11
	s_add_u32 s6, s12, 0x80
	s_waitcnt vmcnt(2)
	s_barrier
	s_addc_u32 s7, s13, 0
	s_add_i32 s38, s28, 0x18000
	s_mov_b32 m0, s38
	s_nop 0
	global_load_lds_dwordx4 v211, s[6:7]
	s_add_i32 s39, s28, 0x1a000
	s_mov_b32 m0, s39
	s_nop 0
	global_load_lds_dwordx4 v214, s[6:7]
	s_add_u32 s6, s2, 0x80
	s_addc_u32 s7, s3, 0
	s_add_i32 s40, s28, 0x8000
	s_mov_b32 m0, s40
	s_nop 0
	global_load_lds_dwordx4 v194, s[6:7]
	s_add_i32 s41, s28, 0xa000
	s_mov_b32 m0, s41
	s_nop 0
	global_load_lds_dwordx4 v224, s[6:7]
	s_add_u32 s8, s12, 0x20080
	s_addc_u32 s9, s13, 0
	s_add_i32 s42, s28, 0x1c000
	s_mov_b32 m0, s42
	s_nop 0
	global_load_lds_dwordx4 v211, s[8:9]
	s_add_i32 s43, s28, 0x1e000
	s_mov_b32 m0, s43
	s_nop 0
	global_load_lds_dwordx4 v214, s[8:9]
	s_add_i32 s44, s28, 0xc000
	s_waitcnt vmcnt(6)
	v_or_b32_e32 v216, s1, v4
	s_cmpk_lt_u32 s0, 0x100
	v_readlane_b32 s0, v243, 6
	v_readlane_b32 s1, v243, 7
	v_or_b32_e32 v217, 0xfffffe00, v216
	s_cselect_b64 s[8:9], -1, 0
	s_add_i32 s45, s28, 0xe000
	s_mov_b32 s16, 0
	v_add_u32_e32 v218, 0, v2
	v_add_u32_e32 v219, 0, v5
	v_readlane_b32 s52, v243, 3
	s_mov_b32 s51, s0
	s_mov_b64 s[0:1], s[12:13]
	v_mov_b32_e32 v220, v194
	v_mov_b32_e32 v221, v224
	v_mov_b32_e32 v222, v225
	v_mov_b32_e32 v223, v226
	s_mov_b64 s[10:11], s[12:13]
	s_barrier
	s_waitcnt vmcnt(0)
	s_branch .LBB0_285

.LBB0_288:
	s_add_u32 s0, s22, 0x80
	s_waitcnt lgkmcnt(0)
	s_addc_u32 s1, s23, 0
	s_add_u32 s22, s20, 0x80
	s_addc_u32 s23, s21, 0
	s_barrier
	s_setprio 1
	s_waitcnt lgkmcnt(6)
	v_mfma_f32_16x16x128_f8f6f4 v[190:193], v[26:33], v[58:65], v[190:193]
	v_mfma_f32_16x16x128_f8f6f4 v[186:189], v[18:25], v[58:65], v[186:189]
	s_waitcnt lgkmcnt(4)
	v_mfma_f32_16x16x128_f8f6f4 v[178:181], v[26:33], v[50:57], v[178:181]
	v_mfma_f32_16x16x128_f8f6f4 v[170:173], v[18:25], v[50:57], v[170:173]
	s_waitcnt lgkmcnt(2)
	v_mfma_f32_16x16x128_f8f6f4 v[162:165], v[26:33], v[42:49], v[162:165]
	v_mfma_f32_16x16x128_f8f6f4 v[154:157], v[18:25], v[42:49], v[154:157]
	s_waitcnt lgkmcnt(0)
	v_mfma_f32_16x16x128_f8f6f4 v[146:149], v[26:33], v[34:41], v[146:149]
	v_mfma_f32_16x16x128_f8f6f4 v[138:141], v[18:25], v[34:41], v[138:141]
	s_setprio 0
	s_setprio 1
	v_mfma_f32_16x16x128_f8f6f4 v[182:185], v[10:17], v[58:65], v[182:185]
	v_mfma_f32_16x16x128_f8f6f4 v[174:177], v[2:9], v[58:65], v[174:177]
	v_mfma_f32_16x16x128_f8f6f4 v[166:169], v[10:17], v[50:57], v[166:169]
	v_mfma_f32_16x16x128_f8f6f4 v[158:161], v[2:9], v[50:57], v[158:161]
	v_mfma_f32_16x16x128_f8f6f4 v[150:153], v[10:17], v[42:49], v[150:153]
	v_mfma_f32_16x16x128_f8f6f4 v[142:145], v[2:9], v[42:49], v[142:145]
	v_mfma_f32_16x16x128_f8f6f4 v[134:137], v[10:17], v[34:41], v[134:137]
	v_mfma_f32_16x16x128_f8f6f4 v[130:133], v[2:9], v[34:41], v[130:133]
	s_setprio 0
	s_barrier
	ds_read_b128 v[34:37], v219 offset:49152
	ds_read_b128 v[38:41], v219 offset:50176
	ds_read_b128 v[42:45], v219 offset:51200
	ds_read_b128 v[46:49], v219 offset:52224
	ds_read_b128 v[50:53], v219 offset:53248
	ds_read_b128 v[54:57], v219 offset:54272
	ds_read_b128 v[58:61], v219 offset:55296
	ds_read_b128 v[62:65], v219 offset:56320
	s_mov_b32 m0, s38
	s_nop 0
	global_load_lds_dwordx4 v211, s[22:23]
	s_add_u32 s20, s20, 0x20080
	s_mov_b32 m0, s39
	s_nop 0
	global_load_lds_dwordx4 v214, s[22:23]
	s_addc_u32 s21, s21, 0
	s_mov_b32 m0, s42
	s_nop 0
	global_load_lds_dwordx4 v211, s[20:21]
	s_nop 0
	s_mov_b32 m0, s43
	s_nop 0
	global_load_lds_dwordx4 v214, s[20:21]
	s_mov_b32 m0, s40
	s_nop 0
	global_load_lds_dwordx4 v227, s[0:1]
	s_nop 0
	s_mov_b32 m0, s41
	s_nop 0
	global_load_lds_dwordx4 v228, s[0:1]
	s_waitcnt vmcnt(8)
	s_waitcnt lgkmcnt(0)
	s_barrier
	s_setprio 1
	s_waitcnt lgkmcnt(6)
	v_mfma_f32_16x16x128_f8f6f4 v[126:129], v[26:33], v[34:41], v[126:129]
	v_mfma_f32_16x16x128_f8f6f4 v[122:125], v[18:25], v[34:41], v[122:125]
	s_waitcnt lgkmcnt(4)
	v_mfma_f32_16x16x128_f8f6f4 v[114:117], v[26:33], v[42:49], v[114:117]
	v_mfma_f32_16x16x128_f8f6f4 v[106:109], v[18:25], v[42:49], v[106:109]
	s_waitcnt lgkmcnt(2)
	v_mfma_f32_16x16x128_f8f6f4 v[82:85], v[26:33], v[50:57], v[82:85]
	v_mfma_f32_16x16x128_f8f6f4 v[78:81], v[18:25], v[50:57], v[78:81]
	s_waitcnt lgkmcnt(0)
	v_mfma_f32_16x16x128_f8f6f4 v[70:73], v[26:33], v[58:65], v[70:73]
	v_mfma_f32_16x16x128_f8f6f4 v[66:69], v[18:25], v[58:65], v[66:69]
	s_setprio 0
	s_setprio 1
	v_mfma_f32_16x16x128_f8f6f4 v[118:121], v[10:17], v[34:41], v[118:121]
	v_mfma_f32_16x16x128_f8f6f4 v[110:113], v[2:9], v[34:41], v[110:113]
	v_mfma_f32_16x16x128_f8f6f4 v[86:89], v[10:17], v[42:49], v[86:89]
	v_mfma_f32_16x16x128_f8f6f4 v[74:77], v[2:9], v[42:49], v[74:77]
	v_mfma_f32_16x16x128_f8f6f4 v[102:105], v[10:17], v[50:57], v[102:105]
	v_mfma_f32_16x16x128_f8f6f4 v[98:101], v[2:9], v[50:57], v[98:101]
	v_mfma_f32_16x16x128_f8f6f4 v[94:97], v[10:17], v[58:65], v[94:97]
	v_mfma_f32_16x16x128_f8f6f4 v[90:93], v[2:9], v[58:65], v[90:93]
	s_setprio 0
	s_barrier
	s_add_i32 s54, s54, 2
	s_add_u32 s18, s18, 0x100
	s_addc_u32 s19, s19, 0
	s_cmp_gt_u32 s54, 5
	s_cbranch_scc1 .LBB0_301
.LBB0_289:
	v_add_u32_e32 v2, 0x10000, v218
	v_add_u32_e32 v6, 0x14000, v218
	ds_read_b128 v[26:29], v2
	ds_read_b128 v[30:33], v2 offset:1024
	ds_read_b128 v[18:21], v2 offset:2048
	ds_read_b128 v[22:25], v2 offset:3072
	ds_read_b128 v[10:13], v6
	ds_read_b128 v[14:17], v6 offset:1024
	ds_read_b128 v[2:5], v6 offset:2048
	ds_read_b128 v[6:9], v6 offset:3072
	s_add_u32 s22, s2, s18
	s_addc_u32 s23, s3, s19
	s_cmp_eq_u32 s18, 0
	s_cselect_b64 s[0:1], -1, 0
	ds_read_b128 v[58:61], v219
	ds_read_b128 v[62:65], v219 offset:1024
	ds_read_b128 v[50:53], v219 offset:2048
	ds_read_b128 v[54:57], v219 offset:3072
	ds_read_b128 v[42:45], v219 offset:4096
	ds_read_b128 v[46:49], v219 offset:5120
	ds_read_b128 v[34:37], v219 offset:6144
	ds_read_b128 v[38:41], v219 offset:7168
	s_and_b64 s[0:1], s[16:17], s[0:1]
	s_mov_b64 s[20:21], -1
	s_and_b64 vcc, exec, s[0:1]
	s_cbranch_vccnz .LBB0_291
	s_add_u32 s20, s22, 0x80
	s_addc_u32 s21, s23, 0
	s_mov_b32 m0, s44
	s_nop 0
	global_load_lds_dwordx4 v225, s[20:21]
	s_nop 0
	s_mov_b32 m0, s45
	s_nop 0
	global_load_lds_dwordx4 v226, s[20:21]
	s_waitcnt vmcnt(8)
	s_mov_b64 s[20:21], 0

.LBB0_293:
	s_xor_b64 s[24:25], s[0:1], -1
	s_add_u32 s22, s22, 0x100
	s_addc_u32 s23, s23, 0
	s_add_u32 s26, s13, s18
	s_addc_u32 s27, s53, s19
	s_cmpk_eq_i32 s18, 0x300
	s_cselect_b64 s[0:1], -1, 0
	s_waitcnt lgkmcnt(0)
	s_and_b64 s[20:21], s[0:1], exec
	v_cndmask_b32_e64 v227, v194, v220, s[0:1]
	s_cselect_b32 s23, s3, s23
	s_cselect_b32 s22, s2, s22
	v_cndmask_b32_e64 v228, v224, v221, s[0:1]
	s_cselect_b32 s21, s11, s27
	s_cselect_b32 s20, s10, s26
	s_barrier
	s_setprio 1
	s_waitcnt lgkmcnt(6)
	v_mfma_f32_16x16x128_f8f6f4 v[190:193], v[26:33], v[58:65], v[190:193]
	v_mfma_f32_16x16x128_f8f6f4 v[186:189], v[18:25], v[58:65], v[186:189]
	s_waitcnt lgkmcnt(4)
	v_mfma_f32_16x16x128_f8f6f4 v[178:181], v[26:33], v[50:57], v[178:181]
	v_mfma_f32_16x16x128_f8f6f4 v[170:173], v[18:25], v[50:57], v[170:173]
	s_waitcnt lgkmcnt(2)
	v_mfma_f32_16x16x128_f8f6f4 v[162:165], v[26:33], v[42:49], v[162:165]
	v_mfma_f32_16x16x128_f8f6f4 v[154:157], v[18:25], v[42:49], v[154:157]
	s_waitcnt lgkmcnt(0)
	v_mfma_f32_16x16x128_f8f6f4 v[146:149], v[26:33], v[34:41], v[146:149]
	v_mfma_f32_16x16x128_f8f6f4 v[138:141], v[18:25], v[34:41], v[138:141]
	s_setprio 0
	s_setprio 1
	v_mfma_f32_16x16x128_f8f6f4 v[182:185], v[10:17], v[58:65], v[182:185]
	v_mfma_f32_16x16x128_f8f6f4 v[174:177], v[2:9], v[58:65], v[174:177]
	v_mfma_f32_16x16x128_f8f6f4 v[166:169], v[10:17], v[50:57], v[166:169]
	v_mfma_f32_16x16x128_f8f6f4 v[158:161], v[2:9], v[50:57], v[158:161]
	v_mfma_f32_16x16x128_f8f6f4 v[150:153], v[10:17], v[42:49], v[150:153]
	v_mfma_f32_16x16x128_f8f6f4 v[142:145], v[2:9], v[42:49], v[142:145]
	v_mfma_f32_16x16x128_f8f6f4 v[134:137], v[10:17], v[34:41], v[134:137]
	v_mfma_f32_16x16x128_f8f6f4 v[130:133], v[2:9], v[34:41], v[130:133]
	s_setprio 0
	s_barrier
	ds_read_b128 v[58:61], v219 offset:16384
	ds_read_b128 v[62:65], v219 offset:17408
	ds_read_b128 v[50:53], v219 offset:18432
	ds_read_b128 v[54:57], v219 offset:19456
	ds_read_b128 v[42:45], v219 offset:20480
	ds_read_b128 v[46:49], v219 offset:21504
	ds_read_b128 v[34:37], v219 offset:22528
	ds_read_b128 v[38:41], v219 offset:23552
	s_mov_b32 m0, s29
	s_nop 0
	global_load_lds_dwordx4 v211, s[20:21]
	s_nop 0
	s_mov_b32 m0, s30
	s_nop 0
	global_load_lds_dwordx4 v214, s[20:21]
	s_add_u32 s26, s20, 0x20000
	s_addc_u32 s27, s21, 0
	s_mov_b32 m0, s31
	s_nop 0
	global_load_lds_dwordx4 v211, s[26:27]
	s_and_b64 vcc, exec, s[24:25]
	s_mov_b32 m0, s34
	s_nop 0
	global_load_lds_dwordx4 v214, s[26:27]
	s_mov_b32 m0, s28
	s_nop 0
	global_load_lds_dwordx4 v227, s[22:23]
	s_nop 0
	s_mov_b32 m0, s35
	s_nop 0
	global_load_lds_dwordx4 v228, s[22:23]
	s_mov_b64 s[26:27], -1
	s_cbranch_vccz .LBB0_295
	s_waitcnt vmcnt(8)
	s_mov_b64 s[26:27], 0

.LBB0_297:
	s_waitcnt lgkmcnt(0)
	v_cndmask_b32_e64 v229, v225, v222, s[0:1]
	v_cndmask_b32_e64 v230, v226, v223, s[0:1]
	s_barrier
	s_setprio 1
	s_waitcnt lgkmcnt(6)
	v_mfma_f32_16x16x128_f8f6f4 v[126:129], v[26:33], v[58:65], v[126:129]
	v_mfma_f32_16x16x128_f8f6f4 v[122:125], v[18:25], v[58:65], v[122:125]
	s_waitcnt lgkmcnt(4)
	v_mfma_f32_16x16x128_f8f6f4 v[114:117], v[26:33], v[50:57], v[114:117]
	v_mfma_f32_16x16x128_f8f6f4 v[106:109], v[18:25], v[50:57], v[106:109]
	s_waitcnt lgkmcnt(2)
	v_mfma_f32_16x16x128_f8f6f4 v[82:85], v[26:33], v[42:49], v[82:85]
	v_mfma_f32_16x16x128_f8f6f4 v[78:81], v[18:25], v[42:49], v[78:81]
	s_waitcnt lgkmcnt(0)
	v_mfma_f32_16x16x128_f8f6f4 v[70:73], v[26:33], v[34:41], v[70:73]
	v_mfma_f32_16x16x128_f8f6f4 v[66:69], v[18:25], v[34:41], v[66:69]
	s_setprio 0
	s_setprio 1
	v_mfma_f32_16x16x128_f8f6f4 v[118:121], v[10:17], v[58:65], v[118:121]
	v_mfma_f32_16x16x128_f8f6f4 v[110:113], v[2:9], v[58:65], v[110:113]
	v_mfma_f32_16x16x128_f8f6f4 v[86:89], v[10:17], v[50:57], v[86:89]
	v_mfma_f32_16x16x128_f8f6f4 v[74:77], v[2:9], v[50:57], v[74:77]
	v_mfma_f32_16x16x128_f8f6f4 v[102:105], v[10:17], v[42:49], v[102:105]
	v_mfma_f32_16x16x128_f8f6f4 v[98:101], v[2:9], v[42:49], v[98:101]
	v_mfma_f32_16x16x128_f8f6f4 v[94:97], v[10:17], v[34:41], v[94:97]
	v_mfma_f32_16x16x128_f8f6f4 v[90:93], v[2:9], v[34:41], v[90:93]
	s_setprio 0
	s_barrier
	v_add_u32_e32 v2, 0x18000, v218
	v_add_u32_e32 v6, 0x1c000, v218
	ds_read_b128 v[26:29], v2
	ds_read_b128 v[30:33], v2 offset:1024
	ds_read_b128 v[18:21], v2 offset:2048
	ds_read_b128 v[22:25], v2 offset:3072
	ds_read_b128 v[10:13], v6
	ds_read_b128 v[14:17], v6 offset:1024
	ds_read_b128 v[2:5], v6 offset:2048
	ds_read_b128 v[6:9], v6 offset:3072
	ds_read_b128 v[58:61], v219 offset:32768
	ds_read_b128 v[62:65], v219 offset:33792
	ds_read_b128 v[50:53], v219 offset:34816
	ds_read_b128 v[54:57], v219 offset:35840
	ds_read_b128 v[42:45], v219 offset:36864
	ds_read_b128 v[46:49], v219 offset:37888
	ds_read_b128 v[34:37], v219 offset:38912
	ds_read_b128 v[38:41], v219 offset:39936
	s_mov_b32 m0, s36
	s_nop 0
	global_load_lds_dwordx4 v229, s[22:23]
	s_and_b64 vcc, exec, s[24:25]
	s_mov_b32 m0, s37
	s_nop 0
	global_load_lds_dwordx4 v230, s[22:23]
	s_mov_b64 s[0:1], -1
	s_cbranch_vccz .LBB0_299
	s_waitcnt vmcnt(8)
	s_mov_b64 s[0:1], 0

.LBB0_301:
	v_cndmask_b32_e64 v2, 0, 1, s[14:15]
	v_cmp_ne_u32_e64 s[0:1], 1, v2
	s_andn2_b64 vcc, exec, s[14:15]
	s_cbranch_vccnz .LBB0_303
	s_mov_b32 m0, s44
	s_nop 0
	global_load_lds_dwordx4 v222, s[6:7]
	s_nop 0
	s_mov_b32 m0, s45
	s_nop 0
	global_load_lds_dwordx4 v223, s[6:7]

.LBB0_556:
	v_readlane_b32 s0, v245, 30
	s_waitcnt vmcnt(7)
	v_mov_b32_e32 v2, v0
	v_readlane_b32 s1, v245, 31
	s_andn2_b64 vcc, exec, s[0:1]
	v_readfirstlane_b32 s0, v2
	s_cbranch_vccnz .LBB0_739
	v_ashrrev_i32_e32 v1, 31, v2
	v_lshrrev_b32_e32 v1, 26, v1
	v_add_u32_e32 v1, v2, v1
	v_ashrrev_i32_e32 v4, 6, v1
	v_bfe_i32 v1, v2, 27, 1
	v_lshlrev_b32_e32 v3, 4, v2
	v_lshrrev_b32_e32 v1, 22, v1
	v_add_u32_e32 v1, v3, v1
	v_and_b32_e32 v1, 0xfffffc00, v1
	v_sub_u32_e32 v1, v3, v1
	v_lshrrev_b32_e32 v5, 4, v1
	v_bitop3_b32 v5, v5, v1, 32 bitop3:0x6c
	s_waitcnt vmcnt(6)
	v_ashrrev_i32_e32 v6, 31, v5
	v_lshrrev_b32_e32 v6, 26, v6
	v_add_u32_e32 v6, v5, v6
	v_ashrrev_i32_e32 v7, 6, v6
	v_and_b32_e32 v6, 0xc0, v6
	v_sub_u32_e32 v5, v5, v6
	v_lshlrev_b32_e32 v1, 3, v4
	v_lshlrev_b32_e32 v4, 5, v4
	v_ashrrev_i16_sdwa v5, v203, sext(v5) dst_sel:DWORD dst_unused:UNUSED_PAD src0_sel:DWORD src1_sel:BYTE_0
	v_and_b32_e32 v4, 32, v4
	v_bfe_i32 v5, v5, 0, 16
	v_add_u32_e32 v3, 0x2000, v3
	v_add_lshl_u32 v194, v4, v5, 1
	v_ashrrev_i32_e32 v4, 31, v3
	v_lshrrev_b32_e32 v4, 22, v4
	v_add_u32_e32 v4, v3, v4
	v_and_b32_e32 v1, -16, v1
	v_ashrrev_i32_e32 v4, 10, v4
	v_add_u32_e32 v1, v7, v1
	v_mul_i32_i24_e32 v5, 0x400, v4
	v_lshlrev_b32_e32 v6, 1, v1
	v_lshrrev_b32_e32 v8, 2, v1
	v_and_b32_e32 v7, 3, v7
	s_mov_b32 s4, 0x3fffe0
	v_sub_u32_e32 v3, v3, v5
	v_and_b32_e32 v6, 24, v6
	v_and_b32_e32 v8, 4, v8
	v_and_or_b32 v7, v1, s4, v7
	v_lshrrev_b32_e32 v5, 4, v3
	v_or3_b32 v6, v7, v8, v6
	v_bitop3_b32 v3, v5, v3, 32 bitop3:0x6c
	v_lshl_add_u32 v210, v6, 10, v194
	v_ashrrev_i32_e32 v6, 31, v3
	v_lshrrev_b32_e32 v6, 26, v6
	v_lshlrev_b32_e32 v5, 3, v4
	v_add_u32_e32 v6, v3, v6
	v_and_b32_e32 v5, -16, v5
	v_ashrrev_i32_e32 v7, 6, v6
	v_add_u32_e32 v211, v7, v5
	v_and_b32_e32 v5, 0xc0, v6
	v_sub_u32_e32 v3, v3, v5
	v_and_b32_e32 v7, 3, v7
	s_ashr_i32 s6, s0, 6
	v_lshlrev_b32_e32 v4, 5, v4
	v_ashrrev_i16_sdwa v3, v203, sext(v3) dst_sel:DWORD dst_unused:UNUSED_PAD src0_sel:DWORD src1_sel:BYTE_0
	v_lshlrev_b32_e32 v5, 1, v211
	v_lshrrev_b32_e32 v6, 2, v211
	v_and_or_b32 v7, v211, s4, v7
	s_lshl_b32 s4, s6, 10
	v_and_b32_e32 v4, 32, v4
	v_bfe_i32 v3, v3, 0, 16
	v_and_b32_e32 v5, 24, v5
	v_and_b32_e32 v6, 4, v6
	v_readlane_b32 s5, v245, 33
	s_add_i32 s28, s4, 0
	v_readlane_b32 s8, v245, 39
	v_or3_b32 v5, v7, v6, v5
	v_add_lshl_u32 v212, v4, v3, 1
	v_add_u32_e32 v3, s5, v1
	s_add_i32 s29, s28, 0x10000
	v_readlane_b32 s9, v245, 40
	s_mov_b32 m0, s29
	s_nop 0
	global_load_lds_dwordx4 v210, s[8:9]
	s_ashr_i32 s1, s0, 8
	v_lshl_add_u32 v213, v5, 10, v212
	v_lshl_add_u32 v222, v3, 10, v194
	v_add_u32_e32 v3, s5, v211
	v_readlane_b32 s5, v245, 34
	s_add_i32 s30, s28, 0x12000
	s_mov_b32 m0, s30
	s_nop 0
	global_load_lds_dwordx4 v213, s[8:9]
	v_lshl_add_u32 v223, v3, 10, v212
	v_add_u32_e32 v3, s5, v1
	s_add_u32 s4, s8, 0x20000
	v_lshl_add_u32 v224, v3, 10, v194
	v_add_u32_e32 v3, s5, v211
	s_addc_u32 s5, s9, 0
	s_add_i32 s31, s28, 0x14000
	s_mov_b32 m0, s31
	s_nop 0
	global_load_lds_dwordx4 v210, s[4:5]
	s_add_i32 s34, s28, 0x16000
	s_mov_b32 m0, s34
	s_nop 0
	global_load_lds_dwordx4 v213, s[4:5]
	s_mov_b32 m0, s28
	s_nop 0
	global_load_lds_dwordx4 v222, s[2:3]
	s_add_i32 s35, s28, 0x2000
	s_mov_b32 m0, s35
	s_nop 0
	global_load_lds_dwordx4 v223, s[2:3]
	s_add_i32 s36, s28, 0x4000
	s_mov_b32 m0, s36
	s_nop 0
	global_load_lds_dwordx4 v224, s[2:3]
	v_lshl_add_u32 v225, v3, 10, v212
	s_add_i32 s37, s28, 0x6000
	s_mov_b32 m0, s37
	s_nop 0
	global_load_lds_dwordx4 v225, s[2:3]
	s_cmp_eq_u32 s1, 1
	s_cselect_b64 s[4:5], -1, 0
	s_cmp_lg_u32 s1, 1
	s_cbranch_scc1 .LBB0_559
	s_barrier
.LBB0_559:
	v_lshrrev_b32_e32 v4, 1, v2
	v_and_b32_e32 v4, 24, v4
	v_and_b32_e32 v3, 15, v2
	v_lshlrev_b32_e32 v5, 1, v4
	v_lshlrev_b32_e32 v2, 2, v2
	v_lshl_or_b32 v214, s1, 6, v3
	v_lshl_or_b32 v3, v3, 6, v5
	s_lshl_b32 s1, s1, 13
	v_and_b32_e32 v2, 32, v2
	v_bitop3_b32 v5, v3, s1, v2 bitop3:0xde
	s_lshl_b32 s1, s6, 5
	s_and_b32 s1, s1, 0x60
	s_lshl_b32 s6, s1, 7
	v_readlane_b32 s12, v245, 39
	v_bitop3_b32 v2, v3, s6, v2 bitop3:0xde
	v_readlane_b32 s13, v245, 40
	s_add_u32 s6, s12, 0x80
	s_waitcnt vmcnt(2)
	s_barrier
	s_addc_u32 s7, s13, 0
	s_add_i32 s38, s28, 0x18000
	s_mov_b32 m0, s38
	s_nop 0
	global_load_lds_dwordx4 v210, s[6:7]
	s_add_i32 s39, s28, 0x1a000
	s_mov_b32 m0, s39
	s_nop 0
	global_load_lds_dwordx4 v213, s[6:7]
	s_add_u32 s6, s2, 0x80
	s_addc_u32 s7, s3, 0
	s_add_i32 s40, s28, 0x8000
	s_mov_b32 m0, s40
	s_nop 0
	global_load_lds_dwordx4 v222, s[6:7]
	s_add_i32 s41, s28, 0xa000
	s_mov_b32 m0, s41
	s_nop 0
	global_load_lds_dwordx4 v223, s[6:7]
	s_add_u32 s8, s12, 0x20080
	s_addc_u32 s9, s13, 0
	s_add_i32 s42, s28, 0x1c000
	s_mov_b32 m0, s42
	s_nop 0
	global_load_lds_dwordx4 v210, s[8:9]
	s_add_i32 s43, s28, 0x1e000
	s_mov_b32 m0, s43
	s_nop 0
	global_load_lds_dwordx4 v213, s[8:9]
	s_add_i32 s44, s28, 0xc000
	s_waitcnt vmcnt(6)
	s_cmpk_lt_u32 s0, 0x100
	v_or_b32_e32 v215, s1, v4
	v_readlane_b32 s0, v245, 35
	v_readlane_b32 s1, v245, 36
	s_cselect_b64 s[8:9], -1, 0
	s_add_i32 s45, s28, 0xe000
	s_mov_b32 s16, 0
	v_add_u32_e32 v216, 0, v2
	v_add_u32_e32 v217, 0, v5
	v_readlane_b32 s51, v245, 32
	s_mov_b32 s52, s0
	s_mov_b64 s[0:1], s[12:13]
	v_mov_b32_e32 v218, v222
	v_mov_b32_e32 v219, v223
	v_mov_b32_e32 v220, v224
	v_mov_b32_e32 v221, v225
	s_mov_b64 s[10:11], s[12:13]
	s_barrier
	s_waitcnt vmcnt(0)
	s_branch .LBB0_562

.LBB0_565:
	s_add_u32 s0, s22, 0x80
	s_waitcnt lgkmcnt(0)
	s_addc_u32 s1, s23, 0
	s_add_u32 s22, s20, 0x80
	s_addc_u32 s23, s21, 0
	s_barrier
	s_setprio 1
	s_waitcnt lgkmcnt(6)
	v_mfma_f32_16x16x128_f8f6f4 v[190:193], v[26:33], v[58:65], v[190:193]
	v_mfma_f32_16x16x128_f8f6f4 v[186:189], v[18:25], v[58:65], v[186:189]
	s_waitcnt lgkmcnt(4)
	v_mfma_f32_16x16x128_f8f6f4 v[178:181], v[26:33], v[50:57], v[178:181]
	v_mfma_f32_16x16x128_f8f6f4 v[170:173], v[18:25], v[50:57], v[170:173]
	s_waitcnt lgkmcnt(2)
	v_mfma_f32_16x16x128_f8f6f4 v[162:165], v[26:33], v[42:49], v[162:165]
	v_mfma_f32_16x16x128_f8f6f4 v[154:157], v[18:25], v[42:49], v[154:157]
	s_waitcnt lgkmcnt(0)
	v_mfma_f32_16x16x128_f8f6f4 v[146:149], v[26:33], v[34:41], v[146:149]
	v_mfma_f32_16x16x128_f8f6f4 v[138:141], v[18:25], v[34:41], v[138:141]
	s_setprio 0
	s_setprio 1
	v_mfma_f32_16x16x128_f8f6f4 v[182:185], v[10:17], v[58:65], v[182:185]
	v_mfma_f32_16x16x128_f8f6f4 v[174:177], v[2:9], v[58:65], v[174:177]
	v_mfma_f32_16x16x128_f8f6f4 v[166:169], v[10:17], v[50:57], v[166:169]
	v_mfma_f32_16x16x128_f8f6f4 v[158:161], v[2:9], v[50:57], v[158:161]
	v_mfma_f32_16x16x128_f8f6f4 v[150:153], v[10:17], v[42:49], v[150:153]
	v_mfma_f32_16x16x128_f8f6f4 v[142:145], v[2:9], v[42:49], v[142:145]
	v_mfma_f32_16x16x128_f8f6f4 v[134:137], v[10:17], v[34:41], v[134:137]
	v_mfma_f32_16x16x128_f8f6f4 v[130:133], v[2:9], v[34:41], v[130:133]
	s_setprio 0
	s_barrier
	ds_read_b128 v[34:37], v217 offset:49152
	ds_read_b128 v[38:41], v217 offset:50176
	ds_read_b128 v[42:45], v217 offset:51200
	ds_read_b128 v[46:49], v217 offset:52224
	ds_read_b128 v[50:53], v217 offset:53248
	ds_read_b128 v[54:57], v217 offset:54272
	ds_read_b128 v[58:61], v217 offset:55296
	ds_read_b128 v[62:65], v217 offset:56320
	s_mov_b32 m0, s38
	s_nop 0
	global_load_lds_dwordx4 v210, s[22:23]
	s_add_u32 s20, s20, 0x20080
	s_mov_b32 m0, s39
	s_nop 0
	global_load_lds_dwordx4 v213, s[22:23]
	s_addc_u32 s21, s21, 0
	s_mov_b32 m0, s42
	s_nop 0
	global_load_lds_dwordx4 v210, s[20:21]
	s_nop 0
	s_mov_b32 m0, s43
	s_nop 0
	global_load_lds_dwordx4 v213, s[20:21]
	s_mov_b32 m0, s40
	s_nop 0
	global_load_lds_dwordx4 v226, s[0:1]
	s_nop 0
	s_mov_b32 m0, s41
	s_nop 0
	global_load_lds_dwordx4 v227, s[0:1]
	s_waitcnt vmcnt(8)
	s_waitcnt lgkmcnt(0)
	s_barrier
	s_setprio 1
	s_waitcnt lgkmcnt(6)
	v_mfma_f32_16x16x128_f8f6f4 v[126:129], v[26:33], v[34:41], v[126:129]
	v_mfma_f32_16x16x128_f8f6f4 v[122:125], v[18:25], v[34:41], v[122:125]
	s_waitcnt lgkmcnt(4)
	v_mfma_f32_16x16x128_f8f6f4 v[114:117], v[26:33], v[42:49], v[114:117]
	v_mfma_f32_16x16x128_f8f6f4 v[98:101], v[18:25], v[42:49], v[98:101]
	s_waitcnt lgkmcnt(2)
	v_mfma_f32_16x16x128_f8f6f4 v[82:85], v[26:33], v[50:57], v[82:85]
	v_mfma_f32_16x16x128_f8f6f4 v[78:81], v[18:25], v[50:57], v[78:81]
	s_waitcnt lgkmcnt(0)
	v_mfma_f32_16x16x128_f8f6f4 v[70:73], v[26:33], v[58:65], v[70:73]
	v_mfma_f32_16x16x128_f8f6f4 v[66:69], v[18:25], v[58:65], v[66:69]
	s_setprio 0
	s_setprio 1
	v_mfma_f32_16x16x128_f8f6f4 v[118:121], v[10:17], v[34:41], v[118:121]
	v_mfma_f32_16x16x128_f8f6f4 v[102:105], v[2:9], v[34:41], v[102:105]
	v_mfma_f32_16x16x128_f8f6f4 v[86:89], v[10:17], v[42:49], v[86:89]
	v_mfma_f32_16x16x128_f8f6f4 v[74:77], v[2:9], v[42:49], v[74:77]
	v_mfma_f32_16x16x128_f8f6f4 v[110:113], v[10:17], v[50:57], v[110:113]
	v_mfma_f32_16x16x128_f8f6f4 v[106:109], v[2:9], v[50:57], v[106:109]
	v_mfma_f32_16x16x128_f8f6f4 v[94:97], v[10:17], v[58:65], v[94:97]
	v_mfma_f32_16x16x128_f8f6f4 v[90:93], v[2:9], v[58:65], v[90:93]
	s_setprio 0
	s_barrier
	s_add_i32 s54, s54, 2
	s_add_u32 s18, s18, 0x100
	s_addc_u32 s19, s19, 0
	s_cmp_gt_u32 s54, 5
	s_cbranch_scc1 .LBB0_578
.LBB0_566:
	v_add_u32_e32 v2, 0x10000, v216
	v_add_u32_e32 v6, 0x14000, v216
	ds_read_b128 v[26:29], v2
	ds_read_b128 v[30:33], v2 offset:1024
	ds_read_b128 v[18:21], v2 offset:2048
	ds_read_b128 v[22:25], v2 offset:3072
	ds_read_b128 v[10:13], v6
	ds_read_b128 v[14:17], v6 offset:1024
	ds_read_b128 v[2:5], v6 offset:2048
	ds_read_b128 v[6:9], v6 offset:3072
	s_add_u32 s22, s2, s18
	s_addc_u32 s23, s3, s19
	s_cmp_eq_u32 s18, 0
	s_cselect_b64 s[0:1], -1, 0
	ds_read_b128 v[58:61], v217
	ds_read_b128 v[62:65], v217 offset:1024
	ds_read_b128 v[50:53], v217 offset:2048
	ds_read_b128 v[54:57], v217 offset:3072
	ds_read_b128 v[42:45], v217 offset:4096
	ds_read_b128 v[46:49], v217 offset:5120
	ds_read_b128 v[34:37], v217 offset:6144
	ds_read_b128 v[38:41], v217 offset:7168
	s_and_b64 s[0:1], s[16:17], s[0:1]
	s_mov_b64 s[20:21], -1
	s_and_b64 vcc, exec, s[0:1]
	s_cbranch_vccnz .LBB0_568
	s_add_u32 s20, s22, 0x80
	s_addc_u32 s21, s23, 0
	s_mov_b32 m0, s44
	s_nop 0
	global_load_lds_dwordx4 v224, s[20:21]
	s_nop 0
	s_mov_b32 m0, s45
	s_nop 0
	global_load_lds_dwordx4 v225, s[20:21]
	s_waitcnt vmcnt(8)
	s_mov_b64 s[20:21], 0

.LBB0_570:
	s_xor_b64 s[24:25], s[0:1], -1
	s_add_u32 s22, s22, 0x100
	s_addc_u32 s23, s23, 0
	s_add_u32 s26, s13, s18
	s_addc_u32 s27, s53, s19
	s_cmpk_eq_i32 s18, 0x300
	s_cselect_b64 s[0:1], -1, 0
	s_waitcnt lgkmcnt(0)
	s_and_b64 s[20:21], s[0:1], exec
	v_cndmask_b32_e64 v226, v222, v218, s[0:1]
	s_cselect_b32 s23, s3, s23
	s_cselect_b32 s22, s2, s22
	v_cndmask_b32_e64 v227, v223, v219, s[0:1]
	s_cselect_b32 s21, s11, s27
	s_cselect_b32 s20, s10, s26
	s_barrier
	s_setprio 1
	s_waitcnt lgkmcnt(6)
	v_mfma_f32_16x16x128_f8f6f4 v[190:193], v[26:33], v[58:65], v[190:193]
	v_mfma_f32_16x16x128_f8f6f4 v[186:189], v[18:25], v[58:65], v[186:189]
	s_waitcnt lgkmcnt(4)
	v_mfma_f32_16x16x128_f8f6f4 v[178:181], v[26:33], v[50:57], v[178:181]
	v_mfma_f32_16x16x128_f8f6f4 v[170:173], v[18:25], v[50:57], v[170:173]
	s_waitcnt lgkmcnt(2)
	v_mfma_f32_16x16x128_f8f6f4 v[162:165], v[26:33], v[42:49], v[162:165]
	v_mfma_f32_16x16x128_f8f6f4 v[154:157], v[18:25], v[42:49], v[154:157]
	s_waitcnt lgkmcnt(0)
	v_mfma_f32_16x16x128_f8f6f4 v[146:149], v[26:33], v[34:41], v[146:149]
	v_mfma_f32_16x16x128_f8f6f4 v[138:141], v[18:25], v[34:41], v[138:141]
	s_setprio 0
	s_setprio 1
	v_mfma_f32_16x16x128_f8f6f4 v[182:185], v[10:17], v[58:65], v[182:185]
	v_mfma_f32_16x16x128_f8f6f4 v[174:177], v[2:9], v[58:65], v[174:177]
	v_mfma_f32_16x16x128_f8f6f4 v[166:169], v[10:17], v[50:57], v[166:169]
	v_mfma_f32_16x16x128_f8f6f4 v[158:161], v[2:9], v[50:57], v[158:161]
	v_mfma_f32_16x16x128_f8f6f4 v[150:153], v[10:17], v[42:49], v[150:153]
	v_mfma_f32_16x16x128_f8f6f4 v[142:145], v[2:9], v[42:49], v[142:145]
	v_mfma_f32_16x16x128_f8f6f4 v[134:137], v[10:17], v[34:41], v[134:137]
	v_mfma_f32_16x16x128_f8f6f4 v[130:133], v[2:9], v[34:41], v[130:133]
	s_setprio 0
	s_barrier
	ds_read_b128 v[58:61], v217 offset:16384
	ds_read_b128 v[62:65], v217 offset:17408
	ds_read_b128 v[50:53], v217 offset:18432
	ds_read_b128 v[54:57], v217 offset:19456
	ds_read_b128 v[42:45], v217 offset:20480
	ds_read_b128 v[46:49], v217 offset:21504
	ds_read_b128 v[34:37], v217 offset:22528
	ds_read_b128 v[38:41], v217 offset:23552
	s_mov_b32 m0, s29
	s_nop 0
	global_load_lds_dwordx4 v210, s[20:21]
	s_nop 0
	s_mov_b32 m0, s30
	s_nop 0
	global_load_lds_dwordx4 v213, s[20:21]
	s_add_u32 s26, s20, 0x20000
	s_addc_u32 s27, s21, 0
	s_mov_b32 m0, s31
	s_nop 0
	global_load_lds_dwordx4 v210, s[26:27]
	s_and_b64 vcc, exec, s[24:25]
	s_mov_b32 m0, s34
	s_nop 0
	global_load_lds_dwordx4 v213, s[26:27]
	s_mov_b32 m0, s28
	s_nop 0
	global_load_lds_dwordx4 v226, s[22:23]
	s_nop 0
	s_mov_b32 m0, s35
	s_nop 0
	global_load_lds_dwordx4 v227, s[22:23]
	s_mov_b64 s[26:27], -1
	s_cbranch_vccz .LBB0_572
	s_waitcnt vmcnt(8)
	s_mov_b64 s[26:27], 0

.LBB0_574:
	s_waitcnt lgkmcnt(0)
	v_cndmask_b32_e64 v228, v224, v220, s[0:1]
	v_cndmask_b32_e64 v229, v225, v221, s[0:1]
	s_barrier
	s_setprio 1
	s_waitcnt lgkmcnt(6)
	v_mfma_f32_16x16x128_f8f6f4 v[126:129], v[26:33], v[58:65], v[126:129]
	v_mfma_f32_16x16x128_f8f6f4 v[122:125], v[18:25], v[58:65], v[122:125]
	s_waitcnt lgkmcnt(4)
	v_mfma_f32_16x16x128_f8f6f4 v[114:117], v[26:33], v[50:57], v[114:117]
	v_mfma_f32_16x16x128_f8f6f4 v[98:101], v[18:25], v[50:57], v[98:101]
	s_waitcnt lgkmcnt(2)
	v_mfma_f32_16x16x128_f8f6f4 v[82:85], v[26:33], v[42:49], v[82:85]
	v_mfma_f32_16x16x128_f8f6f4 v[78:81], v[18:25], v[42:49], v[78:81]
	s_waitcnt lgkmcnt(0)
	v_mfma_f32_16x16x128_f8f6f4 v[70:73], v[26:33], v[34:41], v[70:73]
	v_mfma_f32_16x16x128_f8f6f4 v[66:69], v[18:25], v[34:41], v[66:69]
	s_setprio 0
	s_setprio 1
	v_mfma_f32_16x16x128_f8f6f4 v[118:121], v[10:17], v[58:65], v[118:121]
	v_mfma_f32_16x16x128_f8f6f4 v[102:105], v[2:9], v[58:65], v[102:105]
	v_mfma_f32_16x16x128_f8f6f4 v[86:89], v[10:17], v[50:57], v[86:89]
	v_mfma_f32_16x16x128_f8f6f4 v[74:77], v[2:9], v[50:57], v[74:77]
	v_mfma_f32_16x16x128_f8f6f4 v[110:113], v[10:17], v[42:49], v[110:113]
	v_mfma_f32_16x16x128_f8f6f4 v[106:109], v[2:9], v[42:49], v[106:109]
	v_mfma_f32_16x16x128_f8f6f4 v[94:97], v[10:17], v[34:41], v[94:97]
	v_mfma_f32_16x16x128_f8f6f4 v[90:93], v[2:9], v[34:41], v[90:93]
	s_setprio 0
	s_barrier
	v_add_u32_e32 v2, 0x18000, v216
	v_add_u32_e32 v6, 0x1c000, v216
	ds_read_b128 v[26:29], v2
	ds_read_b128 v[30:33], v2 offset:1024
	ds_read_b128 v[18:21], v2 offset:2048
	ds_read_b128 v[22:25], v2 offset:3072
	ds_read_b128 v[10:13], v6
	ds_read_b128 v[14:17], v6 offset:1024
	ds_read_b128 v[2:5], v6 offset:2048
	ds_read_b128 v[6:9], v6 offset:3072
	ds_read_b128 v[58:61], v217 offset:32768
	ds_read_b128 v[62:65], v217 offset:33792
	ds_read_b128 v[50:53], v217 offset:34816
	ds_read_b128 v[54:57], v217 offset:35840
	ds_read_b128 v[42:45], v217 offset:36864
	ds_read_b128 v[46:49], v217 offset:37888
	ds_read_b128 v[34:37], v217 offset:38912
	ds_read_b128 v[38:41], v217 offset:39936
	s_mov_b32 m0, s36
	s_nop 0
	global_load_lds_dwordx4 v228, s[22:23]
	s_and_b64 vcc, exec, s[24:25]
	s_mov_b32 m0, s37
	s_nop 0
	global_load_lds_dwordx4 v229, s[22:23]
	s_mov_b64 s[0:1], -1
	s_cbranch_vccz .LBB0_576
	s_waitcnt vmcnt(8)
	s_mov_b64 s[0:1], 0

.LBB0_578:
	v_cndmask_b32_e64 v2, 0, 1, s[14:15]
	v_cmp_ne_u32_e64 s[0:1], 1, v2
	s_andn2_b64 vcc, exec, s[14:15]
	s_cbranch_vccnz .LBB0_580
	s_mov_b32 m0, s44
	s_nop 0
	global_load_lds_dwordx4 v220, s[6:7]
	s_nop 0
	s_mov_b32 m0, s45
	s_nop 0
	global_load_lds_dwordx4 v221, s[6:7]

.LBB0_589:
	s_andn2_b64 vcc, exec, s[0:1]
	s_cbranch_vccnz .LBB0_806
	v_readlane_b32 s0, v245, 47
	s_waitcnt vmcnt(7)
	v_mov_b32_e32 v2, v0
	v_readlane_b32 s1, v245, 48
	s_andn2_b64 vcc, exec, s[0:1]
	v_readfirstlane_b32 s0, v2
	s_cbranch_vccnz .LBB0_724
	v_ashrrev_i32_e32 v1, 31, v2
	v_lshrrev_b32_e32 v1, 26, v1
	v_add_u32_e32 v1, v2, v1
	v_ashrrev_i32_e32 v4, 6, v1
	v_bfe_i32 v1, v2, 27, 1
	v_lshlrev_b32_e32 v3, 4, v2
	v_lshrrev_b32_e32 v1, 22, v1
	v_add_u32_e32 v1, v3, v1
	v_and_b32_e32 v1, 0xfffffc00, v1
	v_sub_u32_e32 v1, v3, v1
	v_lshrrev_b32_e32 v5, 4, v1
	v_bitop3_b32 v5, v5, v1, 32 bitop3:0x6c
	s_waitcnt vmcnt(6)
	v_ashrrev_i32_e32 v6, 31, v5
	v_lshrrev_b32_e32 v6, 26, v6
	v_add_u32_e32 v6, v5, v6
	v_ashrrev_i32_e32 v7, 6, v6
	v_and_b32_e32 v6, 0xc0, v6
	v_sub_u32_e32 v5, v5, v6
	v_lshlrev_b32_e32 v1, 3, v4
	v_lshlrev_b32_e32 v4, 5, v4
	v_ashrrev_i16_sdwa v5, v203, sext(v5) dst_sel:DWORD dst_unused:UNUSED_PAD src0_sel:DWORD src1_sel:BYTE_0
	v_and_b32_e32 v4, 32, v4
	v_bfe_i32 v5, v5, 0, 16
	v_add_u32_e32 v3, 0x2000, v3
	v_add_lshl_u32 v194, v4, v5, 1
	v_ashrrev_i32_e32 v4, 31, v3
	v_lshrrev_b32_e32 v4, 22, v4
	v_add_u32_e32 v4, v3, v4
	v_and_b32_e32 v1, -16, v1
	v_ashrrev_i32_e32 v4, 10, v4
	v_add_u32_e32 v1, v7, v1
	v_mul_i32_i24_e32 v5, 0x400, v4
	v_lshlrev_b32_e32 v6, 1, v1
	v_lshrrev_b32_e32 v8, 2, v1
	v_and_b32_e32 v7, 3, v7
	s_mov_b32 s4, 0x3fffe0
	v_sub_u32_e32 v3, v3, v5
	v_and_b32_e32 v6, 24, v6
	v_and_b32_e32 v8, 4, v8
	v_and_or_b32 v7, v1, s4, v7
	v_lshrrev_b32_e32 v5, 4, v3
	v_or3_b32 v6, v7, v8, v6
	v_bitop3_b32 v3, v5, v3, 32 bitop3:0x6c
	v_lshl_add_u32 v210, v6, 10, v194
	v_ashrrev_i32_e32 v6, 31, v3
	v_lshrrev_b32_e32 v6, 26, v6
	v_lshlrev_b32_e32 v5, 3, v4
	v_add_u32_e32 v6, v3, v6
	v_and_b32_e32 v5, -16, v5
	v_ashrrev_i32_e32 v7, 6, v6
	v_add_u32_e32 v211, v7, v5
	v_and_b32_e32 v5, 0xc0, v6
	v_sub_u32_e32 v3, v3, v5
	v_and_b32_e32 v7, 3, v7
	s_ashr_i32 s6, s0, 6
	v_lshlrev_b32_e32 v4, 5, v4
	v_ashrrev_i16_sdwa v3, v203, sext(v3) dst_sel:DWORD dst_unused:UNUSED_PAD src0_sel:DWORD src1_sel:BYTE_0
	v_lshlrev_b32_e32 v5, 1, v211
	v_lshrrev_b32_e32 v6, 2, v211
	v_and_or_b32 v7, v211, s4, v7
	s_lshl_b32 s4, s6, 10
	v_and_b32_e32 v4, 32, v4
	v_bfe_i32 v3, v3, 0, 16
	v_and_b32_e32 v5, 24, v5
	v_and_b32_e32 v6, 4, v6
	v_readlane_b32 s5, v245, 50
	s_add_i32 s28, s4, 0
	v_readlane_b32 s8, v245, 56
	v_or3_b32 v5, v7, v6, v5
	v_add_lshl_u32 v212, v4, v3, 1
	v_add_u32_e32 v3, s5, v1
	s_add_i32 s29, s28, 0x10000
	v_readlane_b32 s9, v245, 57
	s_mov_b32 m0, s29
	s_nop 0
	global_load_lds_dwordx4 v210, s[8:9]
	s_ashr_i32 s1, s0, 8
	v_lshl_add_u32 v213, v5, 10, v212
	v_lshl_add_u32 v222, v3, 10, v194
	v_add_u32_e32 v3, s5, v211
	v_readlane_b32 s5, v245, 51
	s_add_i32 s30, s28, 0x12000
	s_mov_b32 m0, s30
	s_nop 0
	global_load_lds_dwordx4 v213, s[8:9]
	v_lshl_add_u32 v223, v3, 10, v212
	v_add_u32_e32 v3, s5, v1
	s_add_u32 s4, s8, 0x20000
	v_lshl_add_u32 v224, v3, 10, v194
	v_add_u32_e32 v3, s5, v211
	s_addc_u32 s5, s9, 0
	s_add_i32 s31, s28, 0x14000
	s_mov_b32 m0, s31
	s_nop 0
	global_load_lds_dwordx4 v210, s[4:5]
	s_add_i32 s34, s28, 0x16000
	s_mov_b32 m0, s34
	s_nop 0
	global_load_lds_dwordx4 v213, s[4:5]
	s_mov_b32 m0, s28
	s_nop 0
	global_load_lds_dwordx4 v222, s[2:3]
	s_add_i32 s35, s28, 0x2000
	s_mov_b32 m0, s35
	s_nop 0
	global_load_lds_dwordx4 v223, s[2:3]
	s_add_i32 s36, s28, 0x4000
	s_mov_b32 m0, s36
	s_nop 0
	global_load_lds_dwordx4 v224, s[2:3]
	v_lshl_add_u32 v225, v3, 10, v212
	s_add_i32 s37, s28, 0x6000
	s_mov_b32 m0, s37
	s_nop 0
	global_load_lds_dwordx4 v225, s[2:3]
	s_cmp_eq_u32 s1, 1
	s_cselect_b64 s[4:5], -1, 0
	s_cmp_lg_u32 s1, 1
	s_cbranch_scc1 .LBB0_593
	s_barrier
.LBB0_593:
	v_lshrrev_b32_e32 v4, 1, v2
	v_and_b32_e32 v4, 24, v4
	v_and_b32_e32 v3, 15, v2
	v_lshlrev_b32_e32 v5, 1, v4
	v_lshlrev_b32_e32 v2, 2, v2
	v_lshl_or_b32 v214, s1, 6, v3
	v_lshl_or_b32 v3, v3, 6, v5
	s_lshl_b32 s1, s1, 13
	v_and_b32_e32 v2, 32, v2
	v_bitop3_b32 v5, v3, s1, v2 bitop3:0xde
	s_lshl_b32 s1, s6, 5
	s_and_b32 s1, s1, 0x60
	s_lshl_b32 s6, s1, 7
	v_readlane_b32 s12, v245, 56
	v_bitop3_b32 v2, v3, s6, v2 bitop3:0xde
	v_readlane_b32 s13, v245, 57
	s_add_u32 s6, s12, 0x80
	s_waitcnt vmcnt(2)
	s_barrier
	s_addc_u32 s7, s13, 0
	s_add_i32 s38, s28, 0x18000
	s_mov_b32 m0, s38
	s_nop 0
	global_load_lds_dwordx4 v210, s[6:7]
	s_add_i32 s39, s28, 0x1a000
	s_mov_b32 m0, s39
	s_nop 0
	global_load_lds_dwordx4 v213, s[6:7]
	s_add_u32 s6, s2, 0x80
	s_addc_u32 s7, s3, 0
	s_add_i32 s40, s28, 0x8000
	s_mov_b32 m0, s40
	s_nop 0
	global_load_lds_dwordx4 v222, s[6:7]
	s_add_i32 s41, s28, 0xa000
	s_mov_b32 m0, s41
	s_nop 0
	global_load_lds_dwordx4 v223, s[6:7]
	s_add_u32 s8, s12, 0x20080
	s_addc_u32 s9, s13, 0
	s_add_i32 s42, s28, 0x1c000
	s_mov_b32 m0, s42
	s_nop 0
	global_load_lds_dwordx4 v210, s[8:9]
	s_add_i32 s43, s28, 0x1e000
	s_mov_b32 m0, s43
	s_nop 0
	global_load_lds_dwordx4 v213, s[8:9]
	s_add_i32 s44, s28, 0xc000
	s_waitcnt vmcnt(6)
	s_cmpk_lt_u32 s0, 0x100
	v_or_b32_e32 v215, s1, v4
	v_readlane_b32 s0, v245, 52
	v_readlane_b32 s1, v245, 53
	s_cselect_b64 s[8:9], -1, 0
	s_add_i32 s45, s28, 0xe000
	s_mov_b32 s16, 0
	v_add_u32_e32 v216, 0, v2
	v_add_u32_e32 v217, 0, v5
	v_readlane_b32 s51, v245, 49
	s_mov_b32 s56, s0
	s_mov_b64 s[0:1], s[12:13]
	v_mov_b32_e32 v218, v222
	v_mov_b32_e32 v219, v223
	v_mov_b32_e32 v220, v224
	v_mov_b32_e32 v221, v225
	s_mov_b64 s[10:11], s[12:13]
	s_barrier
	s_branch .LBB0_596

.LBB0_599:
	s_add_u32 s0, s22, 0x80
	s_waitcnt lgkmcnt(0)
	s_addc_u32 s1, s23, 0
	s_add_u32 s22, s20, 0x80
	s_addc_u32 s23, s21, 0
	s_barrier
	s_setprio 1
	s_waitcnt lgkmcnt(6)
	v_mfma_f32_16x16x128_f8f6f4 v[190:193], v[26:33], v[58:65], v[190:193]
	v_mfma_f32_16x16x128_f8f6f4 v[186:189], v[18:25], v[58:65], v[186:189]
	s_waitcnt lgkmcnt(4)
	v_mfma_f32_16x16x128_f8f6f4 v[174:177], v[26:33], v[50:57], v[174:177]
	v_mfma_f32_16x16x128_f8f6f4 v[170:173], v[18:25], v[50:57], v[170:173]
	s_waitcnt lgkmcnt(2)
	v_mfma_f32_16x16x128_f8f6f4 v[158:161], v[26:33], v[42:49], v[158:161]
	v_mfma_f32_16x16x128_f8f6f4 v[154:157], v[18:25], v[42:49], v[154:157]
	s_waitcnt lgkmcnt(0)
	v_mfma_f32_16x16x128_f8f6f4 v[142:145], v[26:33], v[34:41], v[142:145]
	v_mfma_f32_16x16x128_f8f6f4 v[138:141], v[18:25], v[34:41], v[138:141]
	s_setprio 0
	s_setprio 1
	v_mfma_f32_16x16x128_f8f6f4 v[182:185], v[10:17], v[58:65], v[182:185]
	v_mfma_f32_16x16x128_f8f6f4 v[178:181], v[2:9], v[58:65], v[178:181]
	v_mfma_f32_16x16x128_f8f6f4 v[166:169], v[10:17], v[50:57], v[166:169]
	v_mfma_f32_16x16x128_f8f6f4 v[162:165], v[2:9], v[50:57], v[162:165]
	v_mfma_f32_16x16x128_f8f6f4 v[150:153], v[10:17], v[42:49], v[150:153]
	v_mfma_f32_16x16x128_f8f6f4 v[146:149], v[2:9], v[42:49], v[146:149]
	v_mfma_f32_16x16x128_f8f6f4 v[134:137], v[10:17], v[34:41], v[134:137]
	v_mfma_f32_16x16x128_f8f6f4 v[130:133], v[2:9], v[34:41], v[130:133]
	s_setprio 0
	s_barrier
	ds_read_b128 v[34:37], v217 offset:49152
	ds_read_b128 v[38:41], v217 offset:50176
	ds_read_b128 v[42:45], v217 offset:51200
	ds_read_b128 v[46:49], v217 offset:52224
	ds_read_b128 v[50:53], v217 offset:53248
	ds_read_b128 v[54:57], v217 offset:54272
	ds_read_b128 v[58:61], v217 offset:55296
	ds_read_b128 v[62:65], v217 offset:56320
	s_mov_b32 m0, s38
	s_nop 0
	global_load_lds_dwordx4 v210, s[22:23]
	s_add_u32 s20, s20, 0x20080
	s_mov_b32 m0, s39
	s_nop 0
	global_load_lds_dwordx4 v213, s[22:23]
	s_addc_u32 s21, s21, 0
	s_mov_b32 m0, s42
	s_nop 0
	global_load_lds_dwordx4 v210, s[20:21]
	s_nop 0
	s_mov_b32 m0, s43
	s_nop 0
	global_load_lds_dwordx4 v213, s[20:21]
	s_mov_b32 m0, s40
	s_nop 0
	global_load_lds_dwordx4 v226, s[0:1]
	s_nop 0
	s_mov_b32 m0, s41
	s_nop 0
	global_load_lds_dwordx4 v227, s[0:1]
	s_waitcnt vmcnt(8)
	s_waitcnt lgkmcnt(0)
	s_barrier
	s_setprio 1
	s_waitcnt lgkmcnt(6)
	v_mfma_f32_16x16x128_f8f6f4 v[126:129], v[26:33], v[34:41], v[126:129]
	v_mfma_f32_16x16x128_f8f6f4 v[122:125], v[18:25], v[34:41], v[122:125]
	s_waitcnt lgkmcnt(4)
	v_mfma_f32_16x16x128_f8f6f4 v[110:113], v[26:33], v[42:49], v[110:113]
	v_mfma_f32_16x16x128_f8f6f4 v[106:109], v[18:25], v[42:49], v[106:109]
	s_waitcnt lgkmcnt(2)
	v_mfma_f32_16x16x128_f8f6f4 v[94:97], v[26:33], v[50:57], v[94:97]
	v_mfma_f32_16x16x128_f8f6f4 v[90:93], v[18:25], v[50:57], v[90:93]
	s_waitcnt lgkmcnt(0)
	v_mfma_f32_16x16x128_f8f6f4 v[78:81], v[26:33], v[58:65], v[78:81]
	v_mfma_f32_16x16x128_f8f6f4 v[74:77], v[18:25], v[58:65], v[74:77]
	s_setprio 0
	s_setprio 1
	v_mfma_f32_16x16x128_f8f6f4 v[118:121], v[10:17], v[34:41], v[118:121]
	v_mfma_f32_16x16x128_f8f6f4 v[114:117], v[2:9], v[34:41], v[114:117]
	v_mfma_f32_16x16x128_f8f6f4 v[102:105], v[10:17], v[42:49], v[102:105]
	v_mfma_f32_16x16x128_f8f6f4 v[98:101], v[2:9], v[42:49], v[98:101]
	v_mfma_f32_16x16x128_f8f6f4 v[86:89], v[10:17], v[50:57], v[86:89]
	v_mfma_f32_16x16x128_f8f6f4 v[82:85], v[2:9], v[50:57], v[82:85]
	v_mfma_f32_16x16x128_f8f6f4 v[70:73], v[10:17], v[58:65], v[70:73]
	v_mfma_f32_16x16x128_f8f6f4 v[66:69], v[2:9], v[58:65], v[66:69]
	s_setprio 0
	s_barrier
	s_add_i32 s53, s53, 2
	s_add_u32 s18, s18, 0x100
	s_addc_u32 s19, s19, 0
	s_cmp_gt_u32 s53, 5
	s_cbranch_scc1 .LBB0_612

.LBB0_604:
	s_xor_b64 s[24:25], s[0:1], -1
	s_add_u32 s22, s22, 0x100
	s_addc_u32 s23, s23, 0
	s_add_u32 s26, s13, s18
	s_addc_u32 s27, s52, s19
	s_cmpk_eq_i32 s18, 0x300
	s_cselect_b64 s[0:1], -1, 0
	s_waitcnt lgkmcnt(0)
	s_and_b64 s[20:21], s[0:1], exec
	v_cndmask_b32_e64 v226, v222, v218, s[0:1]
	s_cselect_b32 s23, s3, s23
	s_cselect_b32 s22, s2, s22
	v_cndmask_b32_e64 v227, v223, v219, s[0:1]
	s_cselect_b32 s21, s11, s27
	s_cselect_b32 s20, s10, s26
	s_barrier
	s_setprio 1
	s_waitcnt lgkmcnt(6)
	v_mfma_f32_16x16x128_f8f6f4 v[190:193], v[26:33], v[58:65], v[190:193]
	v_mfma_f32_16x16x128_f8f6f4 v[186:189], v[18:25], v[58:65], v[186:189]
	s_waitcnt lgkmcnt(4)
	v_mfma_f32_16x16x128_f8f6f4 v[174:177], v[26:33], v[50:57], v[174:177]
	v_mfma_f32_16x16x128_f8f6f4 v[170:173], v[18:25], v[50:57], v[170:173]
	s_waitcnt lgkmcnt(2)
	v_mfma_f32_16x16x128_f8f6f4 v[158:161], v[26:33], v[42:49], v[158:161]
	v_mfma_f32_16x16x128_f8f6f4 v[154:157], v[18:25], v[42:49], v[154:157]
	s_waitcnt lgkmcnt(0)
	v_mfma_f32_16x16x128_f8f6f4 v[142:145], v[26:33], v[34:41], v[142:145]
	v_mfma_f32_16x16x128_f8f6f4 v[138:141], v[18:25], v[34:41], v[138:141]
	s_setprio 0
	s_setprio 1
	v_mfma_f32_16x16x128_f8f6f4 v[182:185], v[10:17], v[58:65], v[182:185]
	v_mfma_f32_16x16x128_f8f6f4 v[178:181], v[2:9], v[58:65], v[178:181]
	v_mfma_f32_16x16x128_f8f6f4 v[166:169], v[10:17], v[50:57], v[166:169]
	v_mfma_f32_16x16x128_f8f6f4 v[162:165], v[2:9], v[50:57], v[162:165]
	v_mfma_f32_16x16x128_f8f6f4 v[150:153], v[10:17], v[42:49], v[150:153]
	v_mfma_f32_16x16x128_f8f6f4 v[146:149], v[2:9], v[42:49], v[146:149]
	v_mfma_f32_16x16x128_f8f6f4 v[134:137], v[10:17], v[34:41], v[134:137]
	v_mfma_f32_16x16x128_f8f6f4 v[130:133], v[2:9], v[34:41], v[130:133]
	s_setprio 0
	s_barrier
	ds_read_b128 v[58:61], v217 offset:16384
	ds_read_b128 v[62:65], v217 offset:17408
	ds_read_b128 v[50:53], v217 offset:18432
	ds_read_b128 v[54:57], v217 offset:19456
	ds_read_b128 v[42:45], v217 offset:20480
	ds_read_b128 v[46:49], v217 offset:21504
	ds_read_b128 v[34:37], v217 offset:22528
	ds_read_b128 v[38:41], v217 offset:23552
	s_mov_b32 m0, s29
	s_nop 0
	global_load_lds_dwordx4 v210, s[20:21]
	s_nop 0
	s_mov_b32 m0, s30
	s_nop 0
	global_load_lds_dwordx4 v213, s[20:21]
	s_add_u32 s26, s20, 0x20000
	s_addc_u32 s27, s21, 0
	s_mov_b32 m0, s31
	s_nop 0
	global_load_lds_dwordx4 v210, s[26:27]
	s_and_b64 vcc, exec, s[24:25]
	s_mov_b32 m0, s34
	s_nop 0
	global_load_lds_dwordx4 v213, s[26:27]
	s_mov_b32 m0, s28
	s_nop 0
	global_load_lds_dwordx4 v226, s[22:23]
	s_nop 0
	s_mov_b32 m0, s35
	s_nop 0
	global_load_lds_dwordx4 v227, s[22:23]
	s_mov_b64 s[26:27], -1
	s_cbranch_vccz .LBB0_606
	s_waitcnt vmcnt(8)
	s_mov_b64 s[26:27], 0

.LBB0_608:
	s_waitcnt lgkmcnt(0)
	v_cndmask_b32_e64 v228, v224, v220, s[0:1]
	v_cndmask_b32_e64 v229, v225, v221, s[0:1]
	s_barrier
	s_setprio 1
	s_waitcnt lgkmcnt(6)
	v_mfma_f32_16x16x128_f8f6f4 v[126:129], v[26:33], v[58:65], v[126:129]
	v_mfma_f32_16x16x128_f8f6f4 v[122:125], v[18:25], v[58:65], v[122:125]
	s_waitcnt lgkmcnt(4)
	v_mfma_f32_16x16x128_f8f6f4 v[110:113], v[26:33], v[50:57], v[110:113]
	v_mfma_f32_16x16x128_f8f6f4 v[106:109], v[18:25], v[50:57], v[106:109]
	s_waitcnt lgkmcnt(2)
	v_mfma_f32_16x16x128_f8f6f4 v[94:97], v[26:33], v[42:49], v[94:97]
	v_mfma_f32_16x16x128_f8f6f4 v[90:93], v[18:25], v[42:49], v[90:93]
	s_waitcnt lgkmcnt(0)
	v_mfma_f32_16x16x128_f8f6f4 v[78:81], v[26:33], v[34:41], v[78:81]
	v_mfma_f32_16x16x128_f8f6f4 v[74:77], v[18:25], v[34:41], v[74:77]
	s_setprio 0
	s_setprio 1
	v_mfma_f32_16x16x128_f8f6f4 v[118:121], v[10:17], v[58:65], v[118:121]
	v_mfma_f32_16x16x128_f8f6f4 v[114:117], v[2:9], v[58:65], v[114:117]
	v_mfma_f32_16x16x128_f8f6f4 v[102:105], v[10:17], v[50:57], v[102:105]
	v_mfma_f32_16x16x128_f8f6f4 v[98:101], v[2:9], v[50:57], v[98:101]
	v_mfma_f32_16x16x128_f8f6f4 v[86:89], v[10:17], v[42:49], v[86:89]
	v_mfma_f32_16x16x128_f8f6f4 v[82:85], v[2:9], v[42:49], v[82:85]
	v_mfma_f32_16x16x128_f8f6f4 v[70:73], v[10:17], v[34:41], v[70:73]
	v_mfma_f32_16x16x128_f8f6f4 v[66:69], v[2:9], v[34:41], v[66:69]
	s_setprio 0
	s_barrier
	v_add_u32_e32 v2, 0x18000, v216
	v_add_u32_e32 v6, 0x1c000, v216
	ds_read_b128 v[26:29], v2
	ds_read_b128 v[30:33], v2 offset:1024
	ds_read_b128 v[18:21], v2 offset:2048
	ds_read_b128 v[22:25], v2 offset:3072
	ds_read_b128 v[10:13], v6
	ds_read_b128 v[14:17], v6 offset:1024
	ds_read_b128 v[2:5], v6 offset:2048
	ds_read_b128 v[6:9], v6 offset:3072
	ds_read_b128 v[58:61], v217 offset:32768
	ds_read_b128 v[62:65], v217 offset:33792
	ds_read_b128 v[50:53], v217 offset:34816
	ds_read_b128 v[54:57], v217 offset:35840
	ds_read_b128 v[42:45], v217 offset:36864
	ds_read_b128 v[46:49], v217 offset:37888
	ds_read_b128 v[34:37], v217 offset:38912
	ds_read_b128 v[38:41], v217 offset:39936
	s_mov_b32 m0, s36
	s_nop 0
	global_load_lds_dwordx4 v228, s[22:23]
	s_and_b64 vcc, exec, s[24:25]
	s_mov_b32 m0, s37
	s_nop 0
	global_load_lds_dwordx4 v229, s[22:23]
	s_mov_b64 s[0:1], -1
	s_cbranch_vccz .LBB0_610
	s_waitcnt vmcnt(8)
	s_mov_b64 s[0:1], 0

.LBB0_612:
	v_cndmask_b32_e64 v2, 0, 1, s[14:15]
	v_cmp_ne_u32_e64 s[52:53], 1, v2
	s_andn2_b64 vcc, exec, s[14:15]
	s_cbranch_vccnz .LBB0_614
	s_mov_b32 m0, s44
	s_nop 0
	global_load_lds_dwordx4 v220, s[6:7]
	s_nop 0
	s_mov_b32 m0, s45
	s_nop 0
	global_load_lds_dwordx4 v221, s[6:7]

.LBB0_955:
	s_andn2_b64 vcc, exec, s[0:1]
	s_cbranch_vccnz .LBB0_1038
	v_readlane_b32 s0, v243, 21
	s_waitcnt vmcnt(7)
	v_mov_b32_e32 v2, v0
	v_readlane_b32 s1, v243, 22
	s_andn2_b64 vcc, exec, s[0:1]
	v_readfirstlane_b32 s0, v2
	s_cbranch_vccnz .LBB0_986
	v_ashrrev_i32_e32 v1, 31, v2
	v_lshrrev_b32_e32 v1, 26, v1
	v_add_u32_e32 v1, v2, v1
	v_ashrrev_i32_e32 v4, 6, v1
	v_bfe_i32 v1, v2, 27, 1
	v_lshlrev_b32_e32 v3, 4, v2
	v_lshrrev_b32_e32 v1, 22, v1
	v_add_u32_e32 v1, v3, v1
	v_and_b32_e32 v1, 0xfffffc00, v1
	v_sub_u32_e32 v1, v3, v1
	v_lshrrev_b32_e32 v5, 4, v1
	v_bitop3_b32 v5, v5, v1, 32 bitop3:0x6c
	s_waitcnt vmcnt(6)
	v_ashrrev_i32_e32 v6, 31, v5
	v_lshrrev_b32_e32 v6, 26, v6
	v_add_u32_e32 v6, v5, v6
	v_ashrrev_i32_e32 v7, 6, v6
	v_and_b32_e32 v6, 0xc0, v6
	v_sub_u32_e32 v5, v5, v6
	v_lshlrev_b32_e32 v1, 3, v4
	v_lshlrev_b32_e32 v4, 5, v4
	v_ashrrev_i16_sdwa v5, v203, sext(v5) dst_sel:DWORD dst_unused:UNUSED_PAD src0_sel:DWORD src1_sel:BYTE_0
	v_and_b32_e32 v4, 32, v4
	v_bfe_i32 v5, v5, 0, 16
	v_add_u32_e32 v3, 0x2000, v3
	v_add_lshl_u32 v194, v4, v5, 1
	v_ashrrev_i32_e32 v4, 31, v3
	v_lshrrev_b32_e32 v4, 22, v4
	v_add_u32_e32 v4, v3, v4
	v_and_b32_e32 v1, -16, v1
	v_ashrrev_i32_e32 v4, 10, v4
	v_add_u32_e32 v1, v7, v1
	v_mul_i32_i24_e32 v5, 0x400, v4
	v_lshlrev_b32_e32 v6, 1, v1
	v_lshrrev_b32_e32 v8, 2, v1
	v_and_b32_e32 v7, 3, v7
	s_mov_b32 s4, 0x3fffe0
	v_sub_u32_e32 v3, v3, v5
	v_and_b32_e32 v6, 24, v6
	v_and_b32_e32 v8, 4, v8
	v_and_or_b32 v7, v1, s4, v7
	v_lshrrev_b32_e32 v5, 4, v3
	v_or3_b32 v6, v7, v8, v6
	v_bitop3_b32 v3, v5, v3, 32 bitop3:0x6c
	v_lshl_add_u32 v210, v6, 10, v194
	v_ashrrev_i32_e32 v6, 31, v3
	v_lshrrev_b32_e32 v6, 26, v6
	v_lshlrev_b32_e32 v5, 3, v4
	v_add_u32_e32 v6, v3, v6
	v_and_b32_e32 v5, -16, v5
	v_ashrrev_i32_e32 v7, 6, v6
	v_add_u32_e32 v211, v7, v5
	v_and_b32_e32 v5, 0xc0, v6
	v_sub_u32_e32 v3, v3, v5
	v_and_b32_e32 v7, 3, v7
	s_ashr_i32 s6, s0, 6
	v_lshlrev_b32_e32 v4, 5, v4
	v_ashrrev_i16_sdwa v3, v203, sext(v3) dst_sel:DWORD dst_unused:UNUSED_PAD src0_sel:DWORD src1_sel:BYTE_0
	v_lshlrev_b32_e32 v5, 1, v211
	v_lshrrev_b32_e32 v6, 2, v211
	v_and_or_b32 v7, v211, s4, v7
	s_lshl_b32 s4, s6, 10
	v_and_b32_e32 v4, 32, v4
	v_bfe_i32 v3, v3, 0, 16
	v_and_b32_e32 v5, 24, v5
	v_and_b32_e32 v6, 4, v6
	v_readlane_b32 s5, v246, 37
	s_add_i32 s28, s4, 0
	v_readlane_b32 s8, v243, 27
	v_or3_b32 v5, v7, v6, v5
	v_add_lshl_u32 v212, v4, v3, 1
	v_add_u32_e32 v3, s5, v1
	s_add_i32 s29, s28, 0x10000
	v_readlane_b32 s9, v243, 28
	s_mov_b32 m0, s29
	s_nop 0
	global_load_lds_dwordx4 v210, s[8:9]
	s_ashr_i32 s1, s0, 8
	v_lshl_add_u32 v213, v5, 10, v212
	v_lshl_add_u32 v222, v3, 10, v194
	v_add_u32_e32 v3, s5, v211
	v_readlane_b32 s5, v246, 38
	s_add_i32 s30, s28, 0x12000
	s_mov_b32 m0, s30
	s_nop 0
	global_load_lds_dwordx4 v213, s[8:9]
	v_lshl_add_u32 v223, v3, 10, v212
	v_add_u32_e32 v3, s5, v1
	s_add_u32 s4, s8, 0x20000
	v_lshl_add_u32 v224, v3, 10, v194
	v_add_u32_e32 v3, s5, v211
	s_addc_u32 s5, s9, 0
	s_add_i32 s31, s28, 0x14000
	s_mov_b32 m0, s31
	s_nop 0
	global_load_lds_dwordx4 v210, s[4:5]
	s_add_i32 s34, s28, 0x16000
	s_mov_b32 m0, s34
	s_nop 0
	global_load_lds_dwordx4 v213, s[4:5]
	s_mov_b32 m0, s28
	s_nop 0
	global_load_lds_dwordx4 v222, s[2:3]
	s_add_i32 s35, s28, 0x2000
	s_mov_b32 m0, s35
	s_nop 0
	global_load_lds_dwordx4 v223, s[2:3]
	s_add_i32 s36, s28, 0x4000
	s_mov_b32 m0, s36
	s_nop 0
	global_load_lds_dwordx4 v224, s[2:3]
	v_lshl_add_u32 v225, v3, 10, v212
	s_add_i32 s37, s28, 0x6000
	s_mov_b32 m0, s37
	s_nop 0
	global_load_lds_dwordx4 v225, s[2:3]
	s_cmp_eq_u32 s1, 1
	s_cselect_b64 s[4:5], -1, 0
	s_cmp_lg_u32 s1, 1
	s_cbranch_scc1 .LBB0_959
	s_barrier
.LBB0_959:
	v_lshrrev_b32_e32 v4, 1, v2
	v_and_b32_e32 v4, 24, v4
	v_and_b32_e32 v3, 15, v2
	v_lshlrev_b32_e32 v5, 1, v4
	v_lshlrev_b32_e32 v2, 2, v2
	v_lshl_or_b32 v214, s1, 6, v3
	v_lshl_or_b32 v3, v3, 6, v5
	s_lshl_b32 s1, s1, 13
	v_and_b32_e32 v2, 32, v2
	v_bitop3_b32 v5, v3, s1, v2 bitop3:0xde
	s_lshl_b32 s1, s6, 5
	s_and_b32 s1, s1, 0x60
	s_lshl_b32 s6, s1, 7
	v_readlane_b32 s12, v243, 27
	v_bitop3_b32 v2, v3, s6, v2 bitop3:0xde
	v_readlane_b32 s13, v243, 28
	s_add_u32 s6, s12, 0x80
	s_waitcnt vmcnt(2)
	s_barrier
	s_addc_u32 s7, s13, 0
	s_add_i32 s38, s28, 0x18000
	s_mov_b32 m0, s38
	s_nop 0
	global_load_lds_dwordx4 v210, s[6:7]
	s_add_i32 s39, s28, 0x1a000
	s_mov_b32 m0, s39
	s_nop 0
	global_load_lds_dwordx4 v213, s[6:7]
	s_add_u32 s6, s2, 0x80
	s_addc_u32 s7, s3, 0
	s_add_i32 s40, s28, 0x8000
	s_mov_b32 m0, s40
	s_nop 0
	global_load_lds_dwordx4 v222, s[6:7]
	s_add_i32 s41, s28, 0xa000
	s_mov_b32 m0, s41
	s_nop 0
	global_load_lds_dwordx4 v223, s[6:7]
	s_add_u32 s8, s12, 0x20080
	s_addc_u32 s9, s13, 0
	s_add_i32 s42, s28, 0x1c000
	s_mov_b32 m0, s42
	s_nop 0
	global_load_lds_dwordx4 v210, s[8:9]
	s_add_i32 s43, s28, 0x1e000
	s_mov_b32 m0, s43
	s_nop 0
	global_load_lds_dwordx4 v213, s[8:9]
	s_add_i32 s44, s28, 0xc000
	s_waitcnt vmcnt(6)
	s_cmpk_lt_u32 s0, 0x100
	v_or_b32_e32 v215, s1, v4
	v_readlane_b32 s0, v243, 32
	v_readlane_b32 s1, v243, 33
	s_cselect_b64 s[8:9], -1, 0
	s_add_i32 s45, s28, 0xe000
	s_mov_b32 s16, 0
	v_add_u32_e32 v216, 0, v2
	v_add_u32_e32 v217, 0, v5
	v_readlane_b32 s49, v243, 20
	s_mov_b32 s50, s0
	s_mov_b64 s[0:1], s[12:13]
	v_mov_b32_e32 v218, v222
	v_mov_b32_e32 v219, v223
	v_mov_b32_e32 v220, v224
	v_mov_b32_e32 v221, v225
	s_mov_b64 s[10:11], s[12:13]
	s_barrier
	s_waitcnt vmcnt(0)
	s_branch .LBB0_962

.LBB0_965:
	s_add_u32 s0, s22, 0x80
	s_waitcnt lgkmcnt(0)
	s_addc_u32 s1, s23, 0
	s_add_u32 s22, s20, 0x80
	s_addc_u32 s23, s21, 0
	s_barrier
	s_setprio 1
	s_waitcnt lgkmcnt(6)
	v_mfma_f32_16x16x128_f8f6f4 v[190:193], v[26:33], v[58:65], v[190:193]
	v_mfma_f32_16x16x128_f8f6f4 v[186:189], v[18:25], v[58:65], v[186:189]
	s_waitcnt lgkmcnt(4)
	v_mfma_f32_16x16x128_f8f6f4 v[178:181], v[26:33], v[50:57], v[178:181]
	v_mfma_f32_16x16x128_f8f6f4 v[170:173], v[18:25], v[50:57], v[170:173]
	s_waitcnt lgkmcnt(2)
	v_mfma_f32_16x16x128_f8f6f4 v[162:165], v[26:33], v[42:49], v[162:165]
	v_mfma_f32_16x16x128_f8f6f4 v[154:157], v[18:25], v[42:49], v[154:157]
	s_waitcnt lgkmcnt(0)
	v_mfma_f32_16x16x128_f8f6f4 v[142:145], v[26:33], v[34:41], v[142:145]
	v_mfma_f32_16x16x128_f8f6f4 v[138:141], v[18:25], v[34:41], v[138:141]
	s_setprio 0
	s_setprio 1
	v_mfma_f32_16x16x128_f8f6f4 v[182:185], v[10:17], v[58:65], v[182:185]
	v_mfma_f32_16x16x128_f8f6f4 v[174:177], v[2:9], v[58:65], v[174:177]
	v_mfma_f32_16x16x128_f8f6f4 v[166:169], v[10:17], v[50:57], v[166:169]
	v_mfma_f32_16x16x128_f8f6f4 v[158:161], v[2:9], v[50:57], v[158:161]
	v_mfma_f32_16x16x128_f8f6f4 v[150:153], v[10:17], v[42:49], v[150:153]
	v_mfma_f32_16x16x128_f8f6f4 v[146:149], v[2:9], v[42:49], v[146:149]
	v_mfma_f32_16x16x128_f8f6f4 v[134:137], v[10:17], v[34:41], v[134:137]
	v_mfma_f32_16x16x128_f8f6f4 v[130:133], v[2:9], v[34:41], v[130:133]
	s_setprio 0
	s_barrier
	ds_read_b128 v[34:37], v217 offset:49152
	ds_read_b128 v[38:41], v217 offset:50176
	ds_read_b128 v[42:45], v217 offset:51200
	ds_read_b128 v[46:49], v217 offset:52224
	ds_read_b128 v[50:53], v217 offset:53248
	ds_read_b128 v[54:57], v217 offset:54272
	ds_read_b128 v[58:61], v217 offset:55296
	ds_read_b128 v[62:65], v217 offset:56320
	s_mov_b32 m0, s38
	s_nop 0
	global_load_lds_dwordx4 v210, s[22:23]
	s_add_u32 s20, s20, 0x20080
	s_mov_b32 m0, s39
	s_nop 0
	global_load_lds_dwordx4 v213, s[22:23]
	s_addc_u32 s21, s21, 0
	s_mov_b32 m0, s42
	s_nop 0
	global_load_lds_dwordx4 v210, s[20:21]
	s_nop 0
	s_mov_b32 m0, s43
	s_nop 0
	global_load_lds_dwordx4 v213, s[20:21]
	s_mov_b32 m0, s40
	s_nop 0
	global_load_lds_dwordx4 v226, s[0:1]
	s_nop 0
	s_mov_b32 m0, s41
	s_nop 0
	global_load_lds_dwordx4 v227, s[0:1]
	s_waitcnt vmcnt(8)
	s_waitcnt lgkmcnt(0)
	s_barrier
	s_setprio 1
	s_waitcnt lgkmcnt(6)
	v_mfma_f32_16x16x128_f8f6f4 v[126:129], v[26:33], v[34:41], v[126:129]
	v_mfma_f32_16x16x128_f8f6f4 v[122:125], v[18:25], v[34:41], v[122:125]
	s_waitcnt lgkmcnt(4)
	v_mfma_f32_16x16x128_f8f6f4 v[114:117], v[26:33], v[42:49], v[114:117]
	v_mfma_f32_16x16x128_f8f6f4 v[106:109], v[18:25], v[42:49], v[106:109]
	s_waitcnt lgkmcnt(2)
	v_mfma_f32_16x16x128_f8f6f4 v[82:85], v[26:33], v[50:57], v[82:85]
	v_mfma_f32_16x16x128_f8f6f4 v[78:81], v[18:25], v[50:57], v[78:81]
	s_waitcnt lgkmcnt(0)
	v_mfma_f32_16x16x128_f8f6f4 v[70:73], v[26:33], v[58:65], v[70:73]
	v_mfma_f32_16x16x128_f8f6f4 v[66:69], v[18:25], v[58:65], v[66:69]
	s_setprio 0
	s_setprio 1
	v_mfma_f32_16x16x128_f8f6f4 v[118:121], v[10:17], v[34:41], v[118:121]
	v_mfma_f32_16x16x128_f8f6f4 v[110:113], v[2:9], v[34:41], v[110:113]
	v_mfma_f32_16x16x128_f8f6f4 v[86:89], v[10:17], v[42:49], v[86:89]
	v_mfma_f32_16x16x128_f8f6f4 v[74:77], v[2:9], v[42:49], v[74:77]
	v_mfma_f32_16x16x128_f8f6f4 v[102:105], v[10:17], v[50:57], v[102:105]
	v_mfma_f32_16x16x128_f8f6f4 v[98:101], v[2:9], v[50:57], v[98:101]
	v_mfma_f32_16x16x128_f8f6f4 v[94:97], v[10:17], v[58:65], v[94:97]
	v_mfma_f32_16x16x128_f8f6f4 v[90:93], v[2:9], v[58:65], v[90:93]
	s_setprio 0
	s_barrier
	s_add_i32 s52, s52, 2
	s_add_u32 s18, s18, 0x100
	s_addc_u32 s19, s19, 0
	s_cmp_gt_u32 s52, 5
	s_cbranch_scc1 .LBB0_978

.LBB0_970:
	s_xor_b64 s[24:25], s[0:1], -1
	s_add_u32 s22, s22, 0x100
	s_addc_u32 s23, s23, 0
	s_add_u32 s26, s13, s18
	s_addc_u32 s27, s51, s19
	s_cmpk_eq_i32 s18, 0x300
	s_cselect_b64 s[0:1], -1, 0
	s_waitcnt lgkmcnt(0)
	s_and_b64 s[20:21], s[0:1], exec
	v_cndmask_b32_e64 v226, v222, v218, s[0:1]
	s_cselect_b32 s23, s3, s23
	s_cselect_b32 s22, s2, s22
	v_cndmask_b32_e64 v227, v223, v219, s[0:1]
	s_cselect_b32 s21, s11, s27
	s_cselect_b32 s20, s10, s26
	s_barrier
	s_setprio 1
	s_waitcnt lgkmcnt(6)
	v_mfma_f32_16x16x128_f8f6f4 v[190:193], v[26:33], v[58:65], v[190:193]
	v_mfma_f32_16x16x128_f8f6f4 v[186:189], v[18:25], v[58:65], v[186:189]
	s_waitcnt lgkmcnt(4)
	v_mfma_f32_16x16x128_f8f6f4 v[178:181], v[26:33], v[50:57], v[178:181]
	v_mfma_f32_16x16x128_f8f6f4 v[170:173], v[18:25], v[50:57], v[170:173]
	s_waitcnt lgkmcnt(2)
	v_mfma_f32_16x16x128_f8f6f4 v[162:165], v[26:33], v[42:49], v[162:165]
	v_mfma_f32_16x16x128_f8f6f4 v[154:157], v[18:25], v[42:49], v[154:157]
	s_waitcnt lgkmcnt(0)
	v_mfma_f32_16x16x128_f8f6f4 v[142:145], v[26:33], v[34:41], v[142:145]
	v_mfma_f32_16x16x128_f8f6f4 v[138:141], v[18:25], v[34:41], v[138:141]
	s_setprio 0
	s_setprio 1
	v_mfma_f32_16x16x128_f8f6f4 v[182:185], v[10:17], v[58:65], v[182:185]
	v_mfma_f32_16x16x128_f8f6f4 v[174:177], v[2:9], v[58:65], v[174:177]
	v_mfma_f32_16x16x128_f8f6f4 v[166:169], v[10:17], v[50:57], v[166:169]
	v_mfma_f32_16x16x128_f8f6f4 v[158:161], v[2:9], v[50:57], v[158:161]
	v_mfma_f32_16x16x128_f8f6f4 v[150:153], v[10:17], v[42:49], v[150:153]
	v_mfma_f32_16x16x128_f8f6f4 v[146:149], v[2:9], v[42:49], v[146:149]
	v_mfma_f32_16x16x128_f8f6f4 v[134:137], v[10:17], v[34:41], v[134:137]
	v_mfma_f32_16x16x128_f8f6f4 v[130:133], v[2:9], v[34:41], v[130:133]
	s_setprio 0
	s_barrier
	ds_read_b128 v[58:61], v217 offset:16384
	ds_read_b128 v[62:65], v217 offset:17408
	ds_read_b128 v[50:53], v217 offset:18432
	ds_read_b128 v[54:57], v217 offset:19456
	ds_read_b128 v[42:45], v217 offset:20480
	ds_read_b128 v[46:49], v217 offset:21504
	ds_read_b128 v[34:37], v217 offset:22528
	ds_read_b128 v[38:41], v217 offset:23552
	s_mov_b32 m0, s29
	s_nop 0
	global_load_lds_dwordx4 v210, s[20:21]
	s_nop 0
	s_mov_b32 m0, s30
	s_nop 0
	global_load_lds_dwordx4 v213, s[20:21]
	s_add_u32 s26, s20, 0x20000
	s_addc_u32 s27, s21, 0
	s_mov_b32 m0, s31
	s_nop 0
	global_load_lds_dwordx4 v210, s[26:27]
	s_and_b64 vcc, exec, s[24:25]
	s_mov_b32 m0, s34
	s_nop 0
	global_load_lds_dwordx4 v213, s[26:27]
	s_mov_b32 m0, s28
	s_nop 0
	global_load_lds_dwordx4 v226, s[22:23]
	s_nop 0
	s_mov_b32 m0, s35
	s_nop 0
	global_load_lds_dwordx4 v227, s[22:23]
	s_mov_b64 s[26:27], -1
	s_cbranch_vccz .LBB0_972
	s_waitcnt vmcnt(8)
	s_mov_b64 s[26:27], 0

.LBB0_974:
	s_waitcnt lgkmcnt(0)
	v_cndmask_b32_e64 v228, v224, v220, s[0:1]
	v_cndmask_b32_e64 v229, v225, v221, s[0:1]
	s_barrier
	s_setprio 1
	s_waitcnt lgkmcnt(6)
	v_mfma_f32_16x16x128_f8f6f4 v[126:129], v[26:33], v[58:65], v[126:129]
	v_mfma_f32_16x16x128_f8f6f4 v[122:125], v[18:25], v[58:65], v[122:125]
	s_waitcnt lgkmcnt(4)
	v_mfma_f32_16x16x128_f8f6f4 v[114:117], v[26:33], v[50:57], v[114:117]
	v_mfma_f32_16x16x128_f8f6f4 v[106:109], v[18:25], v[50:57], v[106:109]
	s_waitcnt lgkmcnt(2)
	v_mfma_f32_16x16x128_f8f6f4 v[82:85], v[26:33], v[42:49], v[82:85]
	v_mfma_f32_16x16x128_f8f6f4 v[78:81], v[18:25], v[42:49], v[78:81]
	s_waitcnt lgkmcnt(0)
	v_mfma_f32_16x16x128_f8f6f4 v[70:73], v[26:33], v[34:41], v[70:73]
	v_mfma_f32_16x16x128_f8f6f4 v[66:69], v[18:25], v[34:41], v[66:69]
	s_setprio 0
	s_setprio 1
	v_mfma_f32_16x16x128_f8f6f4 v[118:121], v[10:17], v[58:65], v[118:121]
	v_mfma_f32_16x16x128_f8f6f4 v[110:113], v[2:9], v[58:65], v[110:113]
	v_mfma_f32_16x16x128_f8f6f4 v[86:89], v[10:17], v[50:57], v[86:89]
	v_mfma_f32_16x16x128_f8f6f4 v[74:77], v[2:9], v[50:57], v[74:77]
	v_mfma_f32_16x16x128_f8f6f4 v[102:105], v[10:17], v[42:49], v[102:105]
	v_mfma_f32_16x16x128_f8f6f4 v[98:101], v[2:9], v[42:49], v[98:101]
	v_mfma_f32_16x16x128_f8f6f4 v[94:97], v[10:17], v[34:41], v[94:97]
	v_mfma_f32_16x16x128_f8f6f4 v[90:93], v[2:9], v[34:41], v[90:93]
	s_setprio 0
	s_barrier
	v_add_u32_e32 v2, 0x18000, v216
	v_add_u32_e32 v6, 0x1c000, v216
	ds_read_b128 v[26:29], v2
	ds_read_b128 v[30:33], v2 offset:1024
	ds_read_b128 v[18:21], v2 offset:2048
	ds_read_b128 v[22:25], v2 offset:3072
	ds_read_b128 v[10:13], v6
	ds_read_b128 v[14:17], v6 offset:1024
	ds_read_b128 v[2:5], v6 offset:2048
	ds_read_b128 v[6:9], v6 offset:3072
	ds_read_b128 v[58:61], v217 offset:32768
	ds_read_b128 v[62:65], v217 offset:33792
	ds_read_b128 v[50:53], v217 offset:34816
	ds_read_b128 v[54:57], v217 offset:35840
	ds_read_b128 v[42:45], v217 offset:36864
	ds_read_b128 v[46:49], v217 offset:37888
	ds_read_b128 v[34:37], v217 offset:38912
	ds_read_b128 v[38:41], v217 offset:39936
	s_mov_b32 m0, s36
	s_nop 0
	global_load_lds_dwordx4 v228, s[22:23]
	s_and_b64 vcc, exec, s[24:25]
	s_mov_b32 m0, s37
	s_nop 0
	global_load_lds_dwordx4 v229, s[22:23]
	s_mov_b64 s[0:1], -1
	s_cbranch_vccz .LBB0_976
	s_waitcnt vmcnt(8)
	s_mov_b64 s[0:1], 0

.LBB0_1133:
	s_andn2_b64 vcc, exec, s[0:1]
	s_cbranch_vccnz .LBB0_1249
	v_readlane_b32 s0, v243, 21
	v_readlane_b32 s1, v243, 22
	s_and_b64 vcc, exec, s[64:65]
	s_nop 0
	v_cndmask_b32_e64 v1, 0, 1, s[0:1]
	v_cmp_ne_u32_e64 s[0:1], 1, v1
	s_cbranch_vccz .LBB0_1164
	s_waitcnt vmcnt(7)
	v_mov_b32_e32 v2, v0
	s_and_b64 vcc, exec, s[0:1]
	v_readfirstlane_b32 s14, v2
	s_cbranch_vccnz .LBB0_1166
	v_ashrrev_i32_e32 v1, 31, v2
	v_lshrrev_b32_e32 v1, 26, v1
	v_add_u32_e32 v1, v2, v1
	v_ashrrev_i32_e32 v4, 6, v1
	v_bfe_i32 v1, v2, 27, 1
	v_lshlrev_b32_e32 v3, 4, v2
	v_lshrrev_b32_e32 v1, 22, v1
	v_add_u32_e32 v1, v3, v1
	v_and_b32_e32 v1, 0xfffffc00, v1
	v_sub_u32_e32 v1, v3, v1
	v_lshrrev_b32_e32 v5, 4, v1
	v_bitop3_b32 v5, v5, v1, 32 bitop3:0x6c
	s_waitcnt vmcnt(6)
	v_ashrrev_i32_e32 v6, 31, v5
	v_lshrrev_b32_e32 v6, 26, v6
	v_add_u32_e32 v6, v5, v6
	v_ashrrev_i32_e32 v7, 6, v6
	v_and_b32_e32 v6, 0xc0, v6
	v_sub_u32_e32 v5, v5, v6
	v_lshlrev_b32_e32 v1, 3, v4
	v_lshlrev_b32_e32 v4, 5, v4
	v_ashrrev_i16_sdwa v5, v203, sext(v5) dst_sel:DWORD dst_unused:UNUSED_PAD src0_sel:DWORD src1_sel:BYTE_0
	v_and_b32_e32 v4, 32, v4
	v_bfe_i32 v5, v5, 0, 16
	v_add_u32_e32 v3, 0x2000, v3
	v_add_lshl_u32 v194, v4, v5, 1
	v_ashrrev_i32_e32 v4, 31, v3
	v_lshrrev_b32_e32 v4, 22, v4
	v_add_u32_e32 v4, v3, v4
	v_and_b32_e32 v1, -16, v1
	v_ashrrev_i32_e32 v4, 10, v4
	v_add_u32_e32 v1, v7, v1
	v_mul_i32_i24_e32 v5, 0x400, v4
	v_lshlrev_b32_e32 v6, 1, v1
	v_lshrrev_b32_e32 v8, 2, v1
	v_and_b32_e32 v7, 3, v7
	s_mov_b32 s4, 0x3fffe0
	v_sub_u32_e32 v3, v3, v5
	v_and_b32_e32 v6, 24, v6
	v_and_b32_e32 v8, 4, v8
	v_and_or_b32 v7, v1, s4, v7
	v_lshrrev_b32_e32 v5, 4, v3
	v_or3_b32 v6, v7, v8, v6
	v_bitop3_b32 v3, v5, v3, 32 bitop3:0x6c
	v_lshl_add_u32 v210, v6, 10, v194
	v_ashrrev_i32_e32 v6, 31, v3
	v_lshrrev_b32_e32 v6, 26, v6
	v_lshlrev_b32_e32 v5, 3, v4
	v_add_u32_e32 v6, v3, v6
	v_and_b32_e32 v5, -16, v5
	v_ashrrev_i32_e32 v7, 6, v6
	v_add_u32_e32 v211, v7, v5
	v_and_b32_e32 v5, 0xc0, v6
	v_sub_u32_e32 v3, v3, v5
	v_lshlrev_b32_e32 v4, 5, v4
	v_ashrrev_i16_sdwa v3, v203, sext(v3) dst_sel:DWORD dst_unused:UNUSED_PAD src0_sel:DWORD src1_sel:BYTE_0
	v_and_b32_e32 v7, 3, v7
	v_and_b32_e32 v4, 32, v4
	v_bfe_i32 v3, v3, 0, 16
	v_and_or_b32 v7, v211, s4, v7
	v_readlane_b32 s4, v246, 37
	v_add_lshl_u32 v212, v4, v3, 1
	s_ashr_i32 s13, s14, 6
	v_add_u32_e32 v3, s4, v1
	v_lshl_add_u32 v222, v3, 10, v194
	v_add_u32_e32 v3, s4, v211
	v_readlane_b32 s4, v246, 38
	v_lshl_add_u32 v223, v3, 10, v212
	s_ashr_i32 s12, s14, 8
	v_add_u32_e32 v3, s4, v1
	s_lshl_b32 s36, s13, 10
	v_lshl_add_u32 v224, v3, 10, v194
	v_add_u32_e32 v3, s4, v211
	v_readlane_b32 s4, v243, 25
	v_lshlrev_b32_e32 v5, 1, v211
	v_lshrrev_b32_e32 v6, 2, v211
	v_readlane_b32 s5, v243, 26
	s_add_u32 s4, s6, s4
	v_and_b32_e32 v5, 24, v5
	v_and_b32_e32 v6, 4, v6
	s_addc_u32 s5, s7, s5
	s_add_i32 s36, s36, 0
	v_or3_b32 v5, v7, v6, v5
	s_add_i32 s37, s36, 0x10000
	s_mov_b32 m0, s37
	s_nop 0
	global_load_lds_dwordx4 v210, s[4:5]
	v_lshl_add_u32 v213, v5, 10, v212
	s_add_i32 s38, s36, 0x12000
	s_mov_b32 m0, s38
	s_nop 0
	global_load_lds_dwordx4 v213, s[4:5]
	s_add_u32 s10, s4, 0x20000
	s_addc_u32 s11, s5, 0
	s_add_i32 s39, s36, 0x14000
	s_mov_b32 m0, s39
	s_nop 0
	global_load_lds_dwordx4 v210, s[10:11]
	s_add_i32 s40, s36, 0x16000
	s_mov_b32 m0, s40
	s_nop 0
	global_load_lds_dwordx4 v213, s[10:11]
	s_mov_b32 m0, s36
	s_nop 0
	global_load_lds_dwordx4 v222, s[8:9]
	s_add_i32 s41, s36, 0x2000
	s_mov_b32 m0, s41
	s_nop 0
	global_load_lds_dwordx4 v223, s[8:9]
	s_add_i32 s42, s36, 0x4000
	s_mov_b32 m0, s42
	s_nop 0
	global_load_lds_dwordx4 v224, s[8:9]
	v_lshl_add_u32 v225, v3, 10, v212
	s_add_i32 s43, s36, 0x6000
	s_mov_b32 m0, s43
	s_nop 0
	global_load_lds_dwordx4 v225, s[8:9]
	s_cmp_eq_u32 s12, 1
	s_cselect_b64 s[10:11], -1, 0
	s_cmp_lg_u32 s12, 1
	s_cbranch_scc1 .LBB0_1138
	s_barrier
.LBB0_1138:
	v_readlane_b32 s16, v244, 23
	v_readlane_b32 s15, v244, 22
	v_readlane_b32 s17, v244, 24
	s_mul_i32 s16, s15, 0xc000
	s_mov_b32 s15, s17
	v_writelane_b32 v244, s14, 23
	s_lshl_b64 s[16:17], s[16:17], 2
	v_lshrrev_b32_e32 v4, 1, v2
	v_writelane_b32 v244, s15, 24
	s_add_u32 s15, s58, s16
	s_addc_u32 s16, s59, s17
	v_and_b32_e32 v4, 24, v4
	s_add_u32 s44, s15, 0x12000
	v_and_b32_e32 v3, 15, v2
	v_lshlrev_b32_e32 v5, 1, v4
	v_lshlrev_b32_e32 v2, 2, v2
	s_addc_u32 s45, s16, 0
	v_lshl_or_b32 v214, s12, 6, v3
	v_lshl_or_b32 v3, v3, 6, v5
	s_lshl_b32 s12, s12, 13
	v_and_b32_e32 v2, 32, v2
	v_bitop3_b32 v5, v3, s12, v2 bitop3:0xde
	s_lshl_b32 s12, s13, 5
	s_and_b32 s18, s12, 0x60
	s_lshl_b32 s12, s18, 7
	v_bitop3_b32 v2, v3, s12, v2 bitop3:0xde
	s_add_u32 s12, s4, 0x80
	s_waitcnt vmcnt(2)
	s_barrier
	s_addc_u32 s13, s5, 0
	s_add_i32 s47, s36, 0x18000
	s_mov_b32 m0, s47
	s_nop 0
	global_load_lds_dwordx4 v210, s[12:13]
	s_add_i32 s48, s36, 0x1a000
	s_mov_b32 m0, s48
	s_nop 0
	global_load_lds_dwordx4 v213, s[12:13]
	s_add_u32 s12, s8, 0x80
	s_addc_u32 s13, s9, 0
	s_add_i32 s49, s36, 0x8000
	s_mov_b32 m0, s49
	s_nop 0
	global_load_lds_dwordx4 v222, s[12:13]
	s_add_i32 s50, s36, 0xa000
	s_mov_b32 m0, s50
	s_nop 0
	global_load_lds_dwordx4 v223, s[12:13]
	s_add_u32 s16, s4, 0x20080
	s_addc_u32 s17, s5, 0
	s_add_i32 s51, s36, 0x1c000
	s_mov_b32 m0, s51
	s_nop 0
	global_load_lds_dwordx4 v210, s[16:17]
	s_add_i32 s52, s36, 0x1e000
	s_mov_b32 m0, s52
	s_nop 0
	global_load_lds_dwordx4 v213, s[16:17]
	s_waitcnt vmcnt(6)
	s_add_i32 s53, s36, 0xc000
	v_readlane_b32 s16, v243, 32
	s_cmpk_lt_u32 s14, 0x100
	v_readlane_b32 s17, v243, 33
	s_cselect_b64 s[14:15], -1, 0
	s_add_i32 s54, s36, 0xe000
	v_or_b32_e32 v215, s18, v4
	s_mov_b32 s22, 0
	v_add_u32_e32 v216, 0, v2
	v_add_u32_e32 v217, 0, v5
	v_readlane_b32 s57, v243, 20
	s_mov_b32 s58, s16
	v_mov_b32_e32 v218, v222
	v_mov_b32_e32 v219, v223
	v_mov_b32_e32 v220, v224
	v_mov_b32_e32 v221, v225
	s_mov_b64 s[16:17], s[4:5]
	s_barrier
	s_branch .LBB0_1141

.LBB0_1144:
	s_add_u32 s4, s28, 0x80
	s_waitcnt lgkmcnt(0)
	s_addc_u32 s5, s29, 0
	s_add_u32 s28, s26, 0x80
	s_addc_u32 s29, s27, 0
	s_barrier
	s_setprio 1
	s_waitcnt lgkmcnt(6)
	v_mfma_f32_16x16x128_f8f6f4 v[190:193], v[26:33], v[58:65], v[190:193]
	v_mfma_f32_16x16x128_f8f6f4 v[186:189], v[18:25], v[58:65], v[186:189]
	s_waitcnt lgkmcnt(4)
	v_mfma_f32_16x16x128_f8f6f4 v[178:181], v[26:33], v[50:57], v[178:181]
	v_mfma_f32_16x16x128_f8f6f4 v[170:173], v[18:25], v[50:57], v[170:173]
	s_waitcnt lgkmcnt(2)
	v_mfma_f32_16x16x128_f8f6f4 v[158:161], v[26:33], v[42:49], v[158:161]
	v_mfma_f32_16x16x128_f8f6f4 v[154:157], v[18:25], v[42:49], v[154:157]
	s_waitcnt lgkmcnt(0)
	v_mfma_f32_16x16x128_f8f6f4 v[142:145], v[26:33], v[34:41], v[142:145]
	v_mfma_f32_16x16x128_f8f6f4 v[138:141], v[18:25], v[34:41], v[138:141]
	s_setprio 0
	s_setprio 1
	v_mfma_f32_16x16x128_f8f6f4 v[182:185], v[10:17], v[58:65], v[182:185]
	v_mfma_f32_16x16x128_f8f6f4 v[174:177], v[2:9], v[58:65], v[174:177]
	v_mfma_f32_16x16x128_f8f6f4 v[166:169], v[10:17], v[50:57], v[166:169]
	v_mfma_f32_16x16x128_f8f6f4 v[162:165], v[2:9], v[50:57], v[162:165]
	v_mfma_f32_16x16x128_f8f6f4 v[150:153], v[10:17], v[42:49], v[150:153]
	v_mfma_f32_16x16x128_f8f6f4 v[146:149], v[2:9], v[42:49], v[146:149]
	v_mfma_f32_16x16x128_f8f6f4 v[134:137], v[10:17], v[34:41], v[134:137]
	v_mfma_f32_16x16x128_f8f6f4 v[130:133], v[2:9], v[34:41], v[130:133]
	s_setprio 0
	s_barrier
	ds_read_b128 v[34:37], v217 offset:49152
	ds_read_b128 v[38:41], v217 offset:50176
	ds_read_b128 v[42:45], v217 offset:51200
	ds_read_b128 v[46:49], v217 offset:52224
	ds_read_b128 v[50:53], v217 offset:53248
	ds_read_b128 v[54:57], v217 offset:54272
	ds_read_b128 v[58:61], v217 offset:55296
	ds_read_b128 v[62:65], v217 offset:56320
	s_mov_b32 m0, s47
	s_nop 0
	global_load_lds_dwordx4 v210, s[28:29]
	s_add_u32 s26, s26, 0x20080
	s_mov_b32 m0, s48
	s_nop 0
	global_load_lds_dwordx4 v213, s[28:29]
	s_addc_u32 s27, s27, 0
	s_mov_b32 m0, s51
	s_nop 0
	global_load_lds_dwordx4 v210, s[26:27]
	s_nop 0
	s_mov_b32 m0, s52
	s_nop 0
	global_load_lds_dwordx4 v213, s[26:27]
	s_mov_b32 m0, s49
	s_nop 0
	global_load_lds_dwordx4 v226, s[4:5]
	s_nop 0
	s_mov_b32 m0, s50
	s_nop 0
	global_load_lds_dwordx4 v227, s[4:5]
	s_waitcnt vmcnt(8)
	s_waitcnt lgkmcnt(0)
	s_barrier
	s_setprio 1
	s_waitcnt lgkmcnt(6)
	v_mfma_f32_16x16x128_f8f6f4 v[126:129], v[26:33], v[34:41], v[126:129]
	v_mfma_f32_16x16x128_f8f6f4 v[122:125], v[18:25], v[34:41], v[122:125]
	s_waitcnt lgkmcnt(4)
	v_mfma_f32_16x16x128_f8f6f4 v[110:113], v[26:33], v[42:49], v[110:113]
	v_mfma_f32_16x16x128_f8f6f4 v[106:109], v[18:25], v[42:49], v[106:109]
	s_waitcnt lgkmcnt(2)
	v_mfma_f32_16x16x128_f8f6f4 v[86:89], v[26:33], v[50:57], v[86:89]
	v_mfma_f32_16x16x128_f8f6f4 v[82:85], v[18:25], v[50:57], v[82:85]
	s_waitcnt lgkmcnt(0)
	v_mfma_f32_16x16x128_f8f6f4 v[70:73], v[26:33], v[58:65], v[70:73]
	v_mfma_f32_16x16x128_f8f6f4 v[66:69], v[18:25], v[58:65], v[66:69]
	s_setprio 0
	s_setprio 1
	v_mfma_f32_16x16x128_f8f6f4 v[118:121], v[10:17], v[34:41], v[118:121]
	v_mfma_f32_16x16x128_f8f6f4 v[114:117], v[2:9], v[34:41], v[114:117]
	v_mfma_f32_16x16x128_f8f6f4 v[94:97], v[10:17], v[42:49], v[94:97]
	v_mfma_f32_16x16x128_f8f6f4 v[90:93], v[2:9], v[42:49], v[90:93]
	v_mfma_f32_16x16x128_f8f6f4 v[102:105], v[10:17], v[50:57], v[102:105]
	v_mfma_f32_16x16x128_f8f6f4 v[98:101], v[2:9], v[50:57], v[98:101]
	v_mfma_f32_16x16x128_f8f6f4 v[78:81], v[10:17], v[58:65], v[78:81]
	v_mfma_f32_16x16x128_f8f6f4 v[74:77], v[2:9], v[58:65], v[74:77]
	s_setprio 0
	s_barrier
	s_add_i32 s60, s60, 2
	s_add_u32 s24, s24, 0x100
	s_addc_u32 s25, s25, 0
	s_cmp_gt_u32 s60, 5
	s_cbranch_scc1 .LBB0_1157
.LBB0_1145:
	v_add_u32_e32 v2, 0x10000, v216
	v_add_u32_e32 v6, 0x14000, v216
	ds_read_b128 v[26:29], v2
	ds_read_b128 v[30:33], v2 offset:1024
	ds_read_b128 v[18:21], v2 offset:2048
	ds_read_b128 v[22:25], v2 offset:3072
	ds_read_b128 v[10:13], v6
	ds_read_b128 v[14:17], v6 offset:1024
	ds_read_b128 v[2:5], v6 offset:2048
	ds_read_b128 v[6:9], v6 offset:3072
	s_add_u32 s28, s8, s24
	s_addc_u32 s29, s9, s25
	s_cmp_eq_u32 s24, 0
	s_cselect_b64 s[4:5], -1, 0
	ds_read_b128 v[58:61], v217
	ds_read_b128 v[62:65], v217 offset:1024
	ds_read_b128 v[50:53], v217 offset:2048
	ds_read_b128 v[54:57], v217 offset:3072
	ds_read_b128 v[42:45], v217 offset:4096
	ds_read_b128 v[46:49], v217 offset:5120
	ds_read_b128 v[34:37], v217 offset:6144
	ds_read_b128 v[38:41], v217 offset:7168
	s_and_b64 s[4:5], s[22:23], s[4:5]
	s_mov_b64 s[26:27], -1
	s_and_b64 vcc, exec, s[4:5]
	s_cbranch_vccnz .LBB0_1147
	s_add_u32 s26, s28, 0x80
	s_addc_u32 s27, s29, 0
	s_mov_b32 m0, s53
	s_nop 0
	global_load_lds_dwordx4 v224, s[26:27]
	s_nop 0
	s_mov_b32 m0, s54
	s_nop 0
	global_load_lds_dwordx4 v225, s[26:27]
	s_waitcnt vmcnt(8)
	s_mov_b64 s[26:27], 0

.LBB0_1149:
	s_xor_b64 s[30:31], s[4:5], -1
	s_add_u32 s28, s28, 0x100
	s_addc_u32 s29, s29, 0
	s_add_u32 s34, s19, s24
	s_addc_u32 s35, s59, s25
	s_cmpk_eq_i32 s24, 0x300
	s_cselect_b64 s[4:5], -1, 0
	s_waitcnt lgkmcnt(0)
	s_and_b64 s[26:27], s[4:5], exec
	v_cndmask_b32_e64 v226, v222, v218, s[4:5]
	s_cselect_b32 s29, s9, s29
	s_cselect_b32 s28, s8, s28
	v_cndmask_b32_e64 v227, v223, v219, s[4:5]
	s_cselect_b32 s27, s17, s35
	s_cselect_b32 s26, s16, s34
	s_barrier
	s_setprio 1
	s_waitcnt lgkmcnt(6)
	v_mfma_f32_16x16x128_f8f6f4 v[190:193], v[26:33], v[58:65], v[190:193]
	v_mfma_f32_16x16x128_f8f6f4 v[186:189], v[18:25], v[58:65], v[186:189]
	s_waitcnt lgkmcnt(4)
	v_mfma_f32_16x16x128_f8f6f4 v[178:181], v[26:33], v[50:57], v[178:181]
	v_mfma_f32_16x16x128_f8f6f4 v[170:173], v[18:25], v[50:57], v[170:173]
	s_waitcnt lgkmcnt(2)
	v_mfma_f32_16x16x128_f8f6f4 v[158:161], v[26:33], v[42:49], v[158:161]
	v_mfma_f32_16x16x128_f8f6f4 v[154:157], v[18:25], v[42:49], v[154:157]
	s_waitcnt lgkmcnt(0)
	v_mfma_f32_16x16x128_f8f6f4 v[142:145], v[26:33], v[34:41], v[142:145]
	v_mfma_f32_16x16x128_f8f6f4 v[138:141], v[18:25], v[34:41], v[138:141]
	s_setprio 0
	s_setprio 1
	v_mfma_f32_16x16x128_f8f6f4 v[182:185], v[10:17], v[58:65], v[182:185]
	v_mfma_f32_16x16x128_f8f6f4 v[174:177], v[2:9], v[58:65], v[174:177]
	v_mfma_f32_16x16x128_f8f6f4 v[166:169], v[10:17], v[50:57], v[166:169]
	v_mfma_f32_16x16x128_f8f6f4 v[162:165], v[2:9], v[50:57], v[162:165]
	v_mfma_f32_16x16x128_f8f6f4 v[150:153], v[10:17], v[42:49], v[150:153]
	v_mfma_f32_16x16x128_f8f6f4 v[146:149], v[2:9], v[42:49], v[146:149]
	v_mfma_f32_16x16x128_f8f6f4 v[134:137], v[10:17], v[34:41], v[134:137]
	v_mfma_f32_16x16x128_f8f6f4 v[130:133], v[2:9], v[34:41], v[130:133]
	s_setprio 0
	s_barrier
	ds_read_b128 v[58:61], v217 offset:16384
	ds_read_b128 v[62:65], v217 offset:17408
	ds_read_b128 v[50:53], v217 offset:18432
	ds_read_b128 v[54:57], v217 offset:19456
	ds_read_b128 v[42:45], v217 offset:20480
	ds_read_b128 v[46:49], v217 offset:21504
	ds_read_b128 v[34:37], v217 offset:22528
	ds_read_b128 v[38:41], v217 offset:23552
	s_mov_b32 m0, s37
	s_nop 0
	global_load_lds_dwordx4 v210, s[26:27]
	s_nop 0
	s_mov_b32 m0, s38
	s_nop 0
	global_load_lds_dwordx4 v213, s[26:27]
	s_add_u32 s34, s26, 0x20000
	s_addc_u32 s35, s27, 0
	s_mov_b32 m0, s39
	s_nop 0
	global_load_lds_dwordx4 v210, s[34:35]
	s_and_b64 vcc, exec, s[30:31]
	s_mov_b32 m0, s40
	s_nop 0
	global_load_lds_dwordx4 v213, s[34:35]
	s_mov_b32 m0, s36
	s_nop 0
	global_load_lds_dwordx4 v226, s[28:29]
	s_nop 0
	s_mov_b32 m0, s41
	s_nop 0
	global_load_lds_dwordx4 v227, s[28:29]
	s_mov_b64 s[34:35], -1
	s_cbranch_vccz .LBB0_1151
	s_waitcnt vmcnt(8)
	s_mov_b64 s[34:35], 0

.LBB0_1153:
	s_waitcnt lgkmcnt(0)
	v_cndmask_b32_e64 v228, v224, v220, s[4:5]
	v_cndmask_b32_e64 v229, v225, v221, s[4:5]
	s_barrier
	s_setprio 1
	s_waitcnt lgkmcnt(6)
	v_mfma_f32_16x16x128_f8f6f4 v[126:129], v[26:33], v[58:65], v[126:129]
	v_mfma_f32_16x16x128_f8f6f4 v[122:125], v[18:25], v[58:65], v[122:125]
	s_waitcnt lgkmcnt(4)
	v_mfma_f32_16x16x128_f8f6f4 v[110:113], v[26:33], v[50:57], v[110:113]
	v_mfma_f32_16x16x128_f8f6f4 v[106:109], v[18:25], v[50:57], v[106:109]
	s_waitcnt lgkmcnt(2)
	v_mfma_f32_16x16x128_f8f6f4 v[86:89], v[26:33], v[42:49], v[86:89]
	v_mfma_f32_16x16x128_f8f6f4 v[82:85], v[18:25], v[42:49], v[82:85]
	s_waitcnt lgkmcnt(0)
	v_mfma_f32_16x16x128_f8f6f4 v[70:73], v[26:33], v[34:41], v[70:73]
	v_mfma_f32_16x16x128_f8f6f4 v[66:69], v[18:25], v[34:41], v[66:69]
	s_setprio 0
	s_setprio 1
	v_mfma_f32_16x16x128_f8f6f4 v[118:121], v[10:17], v[58:65], v[118:121]
	v_mfma_f32_16x16x128_f8f6f4 v[114:117], v[2:9], v[58:65], v[114:117]
	v_mfma_f32_16x16x128_f8f6f4 v[94:97], v[10:17], v[50:57], v[94:97]
	v_mfma_f32_16x16x128_f8f6f4 v[90:93], v[2:9], v[50:57], v[90:93]
	v_mfma_f32_16x16x128_f8f6f4 v[102:105], v[10:17], v[42:49], v[102:105]
	v_mfma_f32_16x16x128_f8f6f4 v[98:101], v[2:9], v[42:49], v[98:101]
	v_mfma_f32_16x16x128_f8f6f4 v[78:81], v[10:17], v[34:41], v[78:81]
	v_mfma_f32_16x16x128_f8f6f4 v[74:77], v[2:9], v[34:41], v[74:77]
	s_setprio 0
	s_barrier
	v_add_u32_e32 v2, 0x18000, v216
	v_add_u32_e32 v6, 0x1c000, v216
	ds_read_b128 v[26:29], v2
	ds_read_b128 v[30:33], v2 offset:1024
	ds_read_b128 v[18:21], v2 offset:2048
	ds_read_b128 v[22:25], v2 offset:3072
	ds_read_b128 v[10:13], v6
	ds_read_b128 v[14:17], v6 offset:1024
	ds_read_b128 v[2:5], v6 offset:2048
	ds_read_b128 v[6:9], v6 offset:3072
	ds_read_b128 v[58:61], v217 offset:32768
	ds_read_b128 v[62:65], v217 offset:33792
	ds_read_b128 v[50:53], v217 offset:34816
	ds_read_b128 v[54:57], v217 offset:35840
	ds_read_b128 v[42:45], v217 offset:36864
	ds_read_b128 v[46:49], v217 offset:37888
	ds_read_b128 v[34:37], v217 offset:38912
	ds_read_b128 v[38:41], v217 offset:39936
	s_mov_b32 m0, s42
	s_nop 0
	global_load_lds_dwordx4 v228, s[28:29]
	s_and_b64 vcc, exec, s[30:31]
	s_mov_b32 m0, s43
	s_nop 0
	global_load_lds_dwordx4 v229, s[28:29]
	s_mov_b64 s[4:5], -1
	s_cbranch_vccz .LBB0_1155
	s_waitcnt vmcnt(8)
	s_mov_b64 s[4:5], 0

.LBB0_1157:
	v_cndmask_b32_e64 v2, 0, 1, s[20:21]
	v_cmp_ne_u32_e64 s[4:5], 1, v2
	s_andn2_b64 vcc, exec, s[20:21]
	s_cbranch_vccnz .LBB0_1159
	s_mov_b32 m0, s53
	s_nop 0
	global_load_lds_dwordx4 v220, s[12:13]
	s_nop 0
	s_mov_b32 m0, s54
	s_nop 0
	global_load_lds_dwordx4 v221, s[12:13]

.LBB0_1167:
	s_waitcnt vmcnt(7)
	v_mov_b32_e32 v2, v0
	s_and_b64 vcc, exec, s[0:1]
	v_readfirstlane_b32 s12, v2
	s_cbranch_vccnz .LBB0_1197
	v_ashrrev_i32_e32 v1, 31, v2
	v_lshrrev_b32_e32 v1, 26, v1
	v_add_u32_e32 v1, v2, v1
	v_ashrrev_i32_e32 v4, 6, v1
	v_bfe_i32 v1, v2, 27, 1
	v_lshlrev_b32_e32 v3, 4, v2
	v_lshrrev_b32_e32 v1, 22, v1
	v_add_u32_e32 v1, v3, v1
	v_and_b32_e32 v1, 0xfffffc00, v1
	v_sub_u32_e32 v1, v3, v1
	v_lshrrev_b32_e32 v5, 4, v1
	v_bitop3_b32 v5, v5, v1, 32 bitop3:0x6c
	s_waitcnt vmcnt(6)
	v_ashrrev_i32_e32 v6, 31, v5
	v_lshrrev_b32_e32 v6, 26, v6
	v_add_u32_e32 v6, v5, v6
	v_ashrrev_i32_e32 v7, 6, v6
	v_and_b32_e32 v6, 0xc0, v6
	v_sub_u32_e32 v5, v5, v6
	v_lshlrev_b32_e32 v1, 3, v4
	v_lshlrev_b32_e32 v4, 5, v4
	v_ashrrev_i16_sdwa v5, v203, sext(v5) dst_sel:DWORD dst_unused:UNUSED_PAD src0_sel:DWORD src1_sel:BYTE_0
	v_and_b32_e32 v4, 32, v4
	v_bfe_i32 v5, v5, 0, 16
	v_add_u32_e32 v3, 0x2000, v3
	v_add_lshl_u32 v194, v4, v5, 1
	v_ashrrev_i32_e32 v4, 31, v3
	v_lshrrev_b32_e32 v4, 22, v4
	v_add_u32_e32 v4, v3, v4
	v_and_b32_e32 v1, -16, v1
	v_ashrrev_i32_e32 v4, 10, v4
	v_add_u32_e32 v1, v7, v1
	v_mul_i32_i24_e32 v5, 0x400, v4
	v_lshlrev_b32_e32 v6, 1, v1
	v_lshrrev_b32_e32 v8, 2, v1
	v_and_b32_e32 v7, 3, v7
	s_mov_b32 s0, 0x1fffe0
	v_sub_u32_e32 v3, v3, v5
	v_and_b32_e32 v6, 24, v6
	v_and_b32_e32 v8, 4, v8
	v_and_or_b32 v7, v1, s0, v7
	v_lshrrev_b32_e32 v5, 4, v3
	v_or3_b32 v6, v7, v8, v6
	v_bitop3_b32 v3, v5, v3, 32 bitop3:0x6c
	v_lshl_add_u32 v210, v6, 11, v194
	v_ashrrev_i32_e32 v6, 31, v3
	v_lshrrev_b32_e32 v6, 26, v6
	v_lshlrev_b32_e32 v5, 3, v4
	v_add_u32_e32 v6, v3, v6
	v_and_b32_e32 v5, -16, v5
	v_ashrrev_i32_e32 v7, 6, v6
	v_add_u32_e32 v211, v7, v5
	v_and_b32_e32 v5, 0xc0, v6
	v_sub_u32_e32 v3, v3, v5
	v_lshlrev_b32_e32 v4, 5, v4
	v_ashrrev_i16_sdwa v3, v203, sext(v3) dst_sel:DWORD dst_unused:UNUSED_PAD src0_sel:DWORD src1_sel:BYTE_0
	v_and_b32_e32 v7, 3, v7
	v_and_b32_e32 v4, 32, v4
	v_bfe_i32 v3, v3, 0, 16
	v_and_or_b32 v7, v211, s0, v7
	v_readlane_b32 s0, v246, 37
	v_add_lshl_u32 v212, v4, v3, 1
	s_ashr_i32 s11, s12, 6
	v_add_u32_e32 v3, s0, v1
	v_lshl_add_u32 v222, v3, 11, v194
	v_add_u32_e32 v3, s0, v211
	v_readlane_b32 s0, v246, 38
	v_lshl_add_u32 v223, v3, 11, v212
	s_ashr_i32 s10, s12, 8
	v_add_u32_e32 v3, s0, v1
	s_lshl_b32 s4, s11, 10
	v_lshl_add_u32 v224, v3, 11, v194
	v_add_u32_e32 v3, s0, v211
	v_readlane_b32 s0, v243, 34
	v_lshlrev_b32_e32 v5, 1, v211
	v_lshrrev_b32_e32 v6, 2, v211
	v_readlane_b32 s1, v243, 35
	s_add_u32 s0, s6, s0
	v_and_b32_e32 v5, 24, v5
	v_and_b32_e32 v6, 4, v6
	s_addc_u32 s1, s7, s1
	s_add_i32 s34, s4, 0
	v_or3_b32 v5, v7, v6, v5
	s_add_i32 s35, s34, 0x10000
	s_mov_b32 m0, s35
	s_nop 0
	global_load_lds_dwordx4 v210, s[0:1]
	v_lshl_add_u32 v213, v5, 11, v212
	s_add_i32 s36, s34, 0x12000
	s_mov_b32 m0, s36
	s_nop 0
	global_load_lds_dwordx4 v213, s[0:1]
	s_add_u32 s4, s0, 0x40000
	s_addc_u32 s5, s1, 0
	s_add_i32 s37, s34, 0x14000
	s_mov_b32 m0, s37
	s_nop 0
	global_load_lds_dwordx4 v210, s[4:5]
	s_add_i32 s38, s34, 0x16000
	s_mov_b32 m0, s38
	s_nop 0
	global_load_lds_dwordx4 v213, s[4:5]
	s_mov_b32 m0, s34
	s_nop 0
	global_load_lds_dwordx4 v222, s[8:9]
	s_add_i32 s39, s34, 0x2000
	s_mov_b32 m0, s39
	s_nop 0
	global_load_lds_dwordx4 v223, s[8:9]
	s_add_i32 s40, s34, 0x4000
	s_mov_b32 m0, s40
	s_nop 0
	global_load_lds_dwordx4 v224, s[8:9]
	v_lshl_add_u32 v225, v3, 11, v212
	s_add_i32 s41, s34, 0x6000
	s_mov_b32 m0, s41
	s_nop 0
	global_load_lds_dwordx4 v225, s[8:9]
	s_cmp_eq_u32 s10, 1
	s_cselect_b64 s[4:5], -1, 0
	s_cmp_lg_u32 s10, 1
	s_cbranch_scc1 .LBB0_1170
	s_barrier
.LBB0_1170:
	v_lshrrev_b32_e32 v4, 1, v2
	v_and_b32_e32 v4, 24, v4
	v_and_b32_e32 v3, 15, v2
	v_lshlrev_b32_e32 v5, 1, v4
	v_lshlrev_b32_e32 v2, 2, v2
	v_lshl_or_b32 v214, s10, 6, v3
	v_lshl_or_b32 v3, v3, 6, v5
	s_lshl_b32 s10, s10, 13
	v_and_b32_e32 v2, 32, v2
	v_bitop3_b32 v5, v3, s10, v2 bitop3:0xde
	s_lshl_b32 s10, s11, 5
	s_and_b32 s16, s10, 0x60
	s_lshl_b32 s10, s16, 7
	v_bitop3_b32 v2, v3, s10, v2 bitop3:0xde
	s_add_u32 s10, s0, 0x80
	s_waitcnt vmcnt(2)
	s_barrier
	s_addc_u32 s11, s1, 0
	s_add_i32 s42, s34, 0x18000
	s_mov_b32 m0, s42
	s_nop 0
	global_load_lds_dwordx4 v210, s[10:11]
	s_add_i32 s43, s34, 0x1a000
	s_mov_b32 m0, s43
	s_nop 0
	global_load_lds_dwordx4 v213, s[10:11]
	s_add_u32 s10, s8, 0x80
	s_addc_u32 s11, s9, 0
	s_add_i32 s44, s34, 0x8000
	s_mov_b32 m0, s44
	s_nop 0
	global_load_lds_dwordx4 v222, s[10:11]
	s_add_i32 s45, s34, 0xa000
	s_mov_b32 m0, s45
	s_nop 0
	global_load_lds_dwordx4 v223, s[10:11]
	s_add_u32 s14, s0, 0x40080
	s_addc_u32 s15, s1, 0
	s_add_i32 s47, s34, 0x1c000
	s_mov_b32 m0, s47
	s_nop 0
	global_load_lds_dwordx4 v210, s[14:15]
	s_add_i32 s48, s34, 0x1e000
	s_mov_b32 m0, s48
	s_nop 0
	global_load_lds_dwordx4 v213, s[14:15]
	s_waitcnt vmcnt(6)
	s_add_i32 s49, s34, 0xc000
	v_readlane_b32 s14, v243, 32
	s_cmpk_lt_u32 s12, 0x100
	v_readlane_b32 s15, v243, 33
	s_cselect_b64 s[12:13], -1, 0
	s_add_i32 s50, s34, 0xe000
	v_or_b32_e32 v215, s16, v4
	s_mov_b32 s20, 0
	v_add_u32_e32 v216, 0, v2
	v_add_u32_e32 v217, 0, v5
	v_readlane_b32 s53, v243, 20
	s_mov_b32 s54, s14
	v_mov_b32_e32 v218, v222
	v_mov_b32_e32 v219, v223
	v_mov_b32_e32 v220, v224
	v_mov_b32_e32 v221, v225
	s_mov_b64 s[14:15], s[0:1]
	s_barrier
	s_branch .LBB0_1173

.LBB0_1176:
	s_add_u32 s0, s28, 0x80
	s_waitcnt lgkmcnt(0)
	s_addc_u32 s1, s29, 0
	s_add_u32 s26, s24, 0x80
	s_addc_u32 s27, s25, 0
	s_barrier
	s_setprio 1
	s_waitcnt lgkmcnt(7)
	v_mfma_f32_16x16x32_bf16 v[126:129], v[146:149], v[186:189], v[126:129]
	v_mfma_f32_16x16x32_bf16 v[122:125], v[154:157], v[186:189], v[122:125]
	s_waitcnt lgkmcnt(5)
	v_mfma_f32_16x16x32_bf16 v[118:121], v[146:149], v[178:181], v[118:121]
	v_mfma_f32_16x16x32_bf16 v[106:109], v[154:157], v[178:181], v[106:109]
	s_waitcnt lgkmcnt(3)
	v_mfma_f32_16x16x32_bf16 v[94:97], v[146:149], v[170:173], v[94:97]
	v_mfma_f32_16x16x32_bf16 v[90:93], v[154:157], v[170:173], v[90:93]
	s_waitcnt lgkmcnt(1)
	v_mfma_f32_16x16x32_bf16 v[78:81], v[146:149], v[162:165], v[78:81]
	v_mfma_f32_16x16x32_bf16 v[74:77], v[154:157], v[162:165], v[74:77]
	v_mfma_f32_16x16x32_bf16 v[126:129], v[150:153], v[190:193], v[126:129]
	v_mfma_f32_16x16x32_bf16 v[122:125], v[158:161], v[190:193], v[122:125]
	v_mfma_f32_16x16x32_bf16 v[118:121], v[150:153], v[182:185], v[118:121]
	v_mfma_f32_16x16x32_bf16 v[106:109], v[158:161], v[182:185], v[106:109]
	v_mfma_f32_16x16x32_bf16 v[94:97], v[150:153], v[174:177], v[94:97]
	v_mfma_f32_16x16x32_bf16 v[90:93], v[158:161], v[174:177], v[90:93]
	s_waitcnt lgkmcnt(0)
	v_mfma_f32_16x16x32_bf16 v[78:81], v[150:153], v[166:169], v[78:81]
	v_mfma_f32_16x16x32_bf16 v[74:77], v[158:161], v[166:169], v[74:77]
	s_setprio 0
	s_setprio 1
	v_mfma_f32_16x16x32_bf16 v[114:117], v[130:133], v[186:189], v[114:117]
	v_mfma_f32_16x16x32_bf16 v[110:113], v[138:141], v[186:189], v[110:113]
	v_mfma_f32_16x16x32_bf16 v[102:105], v[130:133], v[178:181], v[102:105]
	v_mfma_f32_16x16x32_bf16 v[98:101], v[138:141], v[178:181], v[98:101]
	v_mfma_f32_16x16x32_bf16 v[86:89], v[130:133], v[170:173], v[86:89]
	v_mfma_f32_16x16x32_bf16 v[82:85], v[138:141], v[170:173], v[82:85]
	v_mfma_f32_16x16x32_bf16 v[70:73], v[130:133], v[162:165], v[70:73]
	v_mfma_f32_16x16x32_bf16 v[66:69], v[138:141], v[162:165], v[66:69]
	v_mfma_f32_16x16x32_bf16 v[114:117], v[134:137], v[190:193], v[114:117]
	v_mfma_f32_16x16x32_bf16 v[110:113], v[142:145], v[190:193], v[110:113]
	v_mfma_f32_16x16x32_bf16 v[102:105], v[134:137], v[182:185], v[102:105]
	v_mfma_f32_16x16x32_bf16 v[98:101], v[142:145], v[182:185], v[98:101]
	v_mfma_f32_16x16x32_bf16 v[86:89], v[134:137], v[174:177], v[86:89]
	v_mfma_f32_16x16x32_bf16 v[82:85], v[142:145], v[174:177], v[82:85]
	v_mfma_f32_16x16x32_bf16 v[70:73], v[134:137], v[166:169], v[70:73]
	v_mfma_f32_16x16x32_bf16 v[66:69], v[142:145], v[166:169], v[66:69]
	s_setprio 0
	s_barrier
	ds_read_b128 v[162:165], v217 offset:49152
	ds_read_b128 v[166:169], v217 offset:50176
	ds_read_b128 v[170:173], v217 offset:51200
	ds_read_b128 v[174:177], v217 offset:52224
	ds_read_b128 v[178:181], v217 offset:53248
	ds_read_b128 v[182:185], v217 offset:54272
	ds_read_b128 v[186:189], v217 offset:55296
	ds_read_b128 v[190:193], v217 offset:56320
	s_mov_b32 m0, s42
	s_nop 0
	global_load_lds_dwordx4 v210, s[26:27]
	s_add_u32 s24, s24, 0x40080
	s_mov_b32 m0, s43
	s_nop 0
	global_load_lds_dwordx4 v213, s[26:27]
	s_addc_u32 s25, s25, 0
	s_mov_b32 m0, s47
	s_nop 0
	global_load_lds_dwordx4 v210, s[24:25]
	s_nop 0
	s_mov_b32 m0, s48
	s_nop 0
	global_load_lds_dwordx4 v213, s[24:25]
	s_mov_b32 m0, s44
	s_nop 0
	global_load_lds_dwordx4 v226, s[0:1]
	s_nop 0
	s_mov_b32 m0, s45
	s_nop 0
	global_load_lds_dwordx4 v227, s[0:1]
	s_waitcnt vmcnt(8)
	s_waitcnt lgkmcnt(0)
	s_barrier
	s_setprio 1
	s_waitcnt lgkmcnt(7)
	v_mfma_f32_16x16x32_bf16 v[62:65], v[146:149], v[162:165], v[62:65]
	v_mfma_f32_16x16x32_bf16 v[58:61], v[154:157], v[162:165], v[58:61]
	s_waitcnt lgkmcnt(5)
	v_mfma_f32_16x16x32_bf16 v[46:49], v[146:149], v[170:173], v[46:49]
	v_mfma_f32_16x16x32_bf16 v[42:45], v[154:157], v[170:173], v[42:45]
	s_waitcnt lgkmcnt(3)
	v_mfma_f32_16x16x32_bf16 v[22:25], v[146:149], v[178:181], v[22:25]
	v_mfma_f32_16x16x32_bf16 v[18:21], v[154:157], v[178:181], v[18:21]
	s_waitcnt lgkmcnt(1)
	v_mfma_f32_16x16x32_bf16 v[6:9], v[146:149], v[186:189], v[6:9]
	v_mfma_f32_16x16x32_bf16 v[2:5], v[154:157], v[186:189], v[2:5]
	v_mfma_f32_16x16x32_bf16 v[62:65], v[150:153], v[166:169], v[62:65]
	v_mfma_f32_16x16x32_bf16 v[58:61], v[158:161], v[166:169], v[58:61]
	v_mfma_f32_16x16x32_bf16 v[46:49], v[150:153], v[174:177], v[46:49]
	v_mfma_f32_16x16x32_bf16 v[42:45], v[158:161], v[174:177], v[42:45]
	v_mfma_f32_16x16x32_bf16 v[22:25], v[150:153], v[182:185], v[22:25]
	v_mfma_f32_16x16x32_bf16 v[18:21], v[158:161], v[182:185], v[18:21]
	s_waitcnt lgkmcnt(0)
	v_mfma_f32_16x16x32_bf16 v[6:9], v[150:153], v[190:193], v[6:9]
	v_mfma_f32_16x16x32_bf16 v[2:5], v[158:161], v[190:193], v[2:5]
	s_setprio 0
	s_setprio 1
	v_mfma_f32_16x16x32_bf16 v[54:57], v[130:133], v[162:165], v[54:57]
	v_mfma_f32_16x16x32_bf16 v[50:53], v[138:141], v[162:165], v[50:53]
	v_mfma_f32_16x16x32_bf16 v[30:33], v[130:133], v[170:173], v[30:33]
	v_mfma_f32_16x16x32_bf16 v[26:29], v[138:141], v[170:173], v[26:29]
	v_mfma_f32_16x16x32_bf16 v[38:41], v[130:133], v[178:181], v[38:41]
	v_mfma_f32_16x16x32_bf16 v[34:37], v[138:141], v[178:181], v[34:37]
	v_mfma_f32_16x16x32_bf16 v[14:17], v[130:133], v[186:189], v[14:17]
	v_mfma_f32_16x16x32_bf16 v[10:13], v[138:141], v[186:189], v[10:13]
	v_mfma_f32_16x16x32_bf16 v[54:57], v[134:137], v[166:169], v[54:57]
	v_mfma_f32_16x16x32_bf16 v[50:53], v[142:145], v[166:169], v[50:53]
	v_mfma_f32_16x16x32_bf16 v[30:33], v[134:137], v[174:177], v[30:33]
	v_mfma_f32_16x16x32_bf16 v[26:29], v[142:145], v[174:177], v[26:29]
	v_mfma_f32_16x16x32_bf16 v[38:41], v[134:137], v[182:185], v[38:41]
	v_mfma_f32_16x16x32_bf16 v[34:37], v[142:145], v[182:185], v[34:37]
	v_mfma_f32_16x16x32_bf16 v[14:17], v[134:137], v[190:193], v[14:17]
	v_mfma_f32_16x16x32_bf16 v[10:13], v[142:145], v[190:193], v[10:13]
	s_setprio 0
	s_barrier
	s_add_i32 s56, s56, 2
	s_add_u32 s22, s22, 0x100
	s_addc_u32 s23, s23, 0
	s_cmp_gt_u32 s56, 13
	s_cbranch_scc1 .LBB0_1189
.LBB0_1177:
	v_add_u32_e32 v130, 0x10000, v216
	v_add_u32_e32 v142, 0x14000, v216
	ds_read_b128 v[146:149], v130
	ds_read_b128 v[150:153], v130 offset:1024
	ds_read_b128 v[154:157], v130 offset:2048
	ds_read_b128 v[158:161], v130 offset:3072
	ds_read_b128 v[130:133], v142
	ds_read_b128 v[134:137], v142 offset:1024
	ds_read_b128 v[138:141], v142 offset:2048
	ds_read_b128 v[142:145], v142 offset:3072
	s_add_u32 s28, s8, s22
	s_addc_u32 s29, s9, s23
	s_cmp_eq_u32 s22, 0
	s_cselect_b64 s[0:1], -1, 0
	ds_read_b128 v[186:189], v217
	ds_read_b128 v[190:193], v217 offset:1024
	ds_read_b128 v[178:181], v217 offset:2048
	ds_read_b128 v[182:185], v217 offset:3072
	ds_read_b128 v[170:173], v217 offset:4096
	ds_read_b128 v[174:177], v217 offset:5120
	ds_read_b128 v[162:165], v217 offset:6144
	ds_read_b128 v[166:169], v217 offset:7168
	s_and_b64 s[0:1], s[20:21], s[0:1]
	s_mov_b64 s[24:25], -1
	s_and_b64 vcc, exec, s[0:1]
	s_cbranch_vccnz .LBB0_1179
	s_add_u32 s24, s28, 0x80
	s_addc_u32 s25, s29, 0
	s_mov_b32 m0, s49
	s_nop 0
	global_load_lds_dwordx4 v224, s[24:25]
	s_nop 0
	s_mov_b32 m0, s50
	s_nop 0
	global_load_lds_dwordx4 v225, s[24:25]
	s_waitcnt vmcnt(8)
	s_mov_b64 s[24:25], 0

.LBB0_1181:
	s_xor_b64 s[26:27], s[0:1], -1
	s_add_u32 s28, s28, 0x100
	s_addc_u32 s29, s29, 0
	s_add_u32 s30, s17, s22
	s_addc_u32 s31, s55, s23
	s_cmpk_eq_i32 s22, 0x700
	s_cselect_b64 s[0:1], -1, 0
	s_waitcnt lgkmcnt(0)
	s_and_b64 s[24:25], s[0:1], exec
	v_cndmask_b32_e64 v226, v222, v218, s[0:1]
	s_cselect_b32 s29, s9, s29
	s_cselect_b32 s28, s8, s28
	v_cndmask_b32_e64 v227, v223, v219, s[0:1]
	s_cselect_b32 s25, s15, s31
	s_cselect_b32 s24, s14, s30
	s_barrier
	s_setprio 1
	s_waitcnt lgkmcnt(7)
	v_mfma_f32_16x16x32_bf16 v[126:129], v[146:149], v[186:189], v[126:129]
	v_mfma_f32_16x16x32_bf16 v[122:125], v[154:157], v[186:189], v[122:125]
	s_waitcnt lgkmcnt(5)
	v_mfma_f32_16x16x32_bf16 v[118:121], v[146:149], v[178:181], v[118:121]
	v_mfma_f32_16x16x32_bf16 v[106:109], v[154:157], v[178:181], v[106:109]
	s_waitcnt lgkmcnt(3)
	v_mfma_f32_16x16x32_bf16 v[94:97], v[146:149], v[170:173], v[94:97]
	v_mfma_f32_16x16x32_bf16 v[90:93], v[154:157], v[170:173], v[90:93]
	s_waitcnt lgkmcnt(1)
	v_mfma_f32_16x16x32_bf16 v[78:81], v[146:149], v[162:165], v[78:81]
	v_mfma_f32_16x16x32_bf16 v[74:77], v[154:157], v[162:165], v[74:77]
	v_mfma_f32_16x16x32_bf16 v[126:129], v[150:153], v[190:193], v[126:129]
	v_mfma_f32_16x16x32_bf16 v[122:125], v[158:161], v[190:193], v[122:125]
	v_mfma_f32_16x16x32_bf16 v[118:121], v[150:153], v[182:185], v[118:121]
	v_mfma_f32_16x16x32_bf16 v[106:109], v[158:161], v[182:185], v[106:109]
	v_mfma_f32_16x16x32_bf16 v[94:97], v[150:153], v[174:177], v[94:97]
	v_mfma_f32_16x16x32_bf16 v[90:93], v[158:161], v[174:177], v[90:93]
	s_waitcnt lgkmcnt(0)
	v_mfma_f32_16x16x32_bf16 v[78:81], v[150:153], v[166:169], v[78:81]
	v_mfma_f32_16x16x32_bf16 v[74:77], v[158:161], v[166:169], v[74:77]
	s_setprio 0
	s_setprio 1
	v_mfma_f32_16x16x32_bf16 v[114:117], v[130:133], v[186:189], v[114:117]
	v_mfma_f32_16x16x32_bf16 v[110:113], v[138:141], v[186:189], v[110:113]
	v_mfma_f32_16x16x32_bf16 v[102:105], v[130:133], v[178:181], v[102:105]
	v_mfma_f32_16x16x32_bf16 v[98:101], v[138:141], v[178:181], v[98:101]
	v_mfma_f32_16x16x32_bf16 v[86:89], v[130:133], v[170:173], v[86:89]
	v_mfma_f32_16x16x32_bf16 v[82:85], v[138:141], v[170:173], v[82:85]
	v_mfma_f32_16x16x32_bf16 v[70:73], v[130:133], v[162:165], v[70:73]
	v_mfma_f32_16x16x32_bf16 v[66:69], v[138:141], v[162:165], v[66:69]
	v_mfma_f32_16x16x32_bf16 v[114:117], v[134:137], v[190:193], v[114:117]
	v_mfma_f32_16x16x32_bf16 v[110:113], v[142:145], v[190:193], v[110:113]
	v_mfma_f32_16x16x32_bf16 v[102:105], v[134:137], v[182:185], v[102:105]
	v_mfma_f32_16x16x32_bf16 v[98:101], v[142:145], v[182:185], v[98:101]
	v_mfma_f32_16x16x32_bf16 v[86:89], v[134:137], v[174:177], v[86:89]
	v_mfma_f32_16x16x32_bf16 v[82:85], v[142:145], v[174:177], v[82:85]
	v_mfma_f32_16x16x32_bf16 v[70:73], v[134:137], v[166:169], v[70:73]
	v_mfma_f32_16x16x32_bf16 v[66:69], v[142:145], v[166:169], v[66:69]
	s_setprio 0
	s_barrier
	ds_read_b128 v[186:189], v217 offset:16384
	ds_read_b128 v[190:193], v217 offset:17408
	ds_read_b128 v[178:181], v217 offset:18432
	ds_read_b128 v[182:185], v217 offset:19456
	ds_read_b128 v[170:173], v217 offset:20480
	ds_read_b128 v[174:177], v217 offset:21504
	ds_read_b128 v[162:165], v217 offset:22528
	ds_read_b128 v[166:169], v217 offset:23552
	s_mov_b32 m0, s35
	s_nop 0
	global_load_lds_dwordx4 v210, s[24:25]
	s_nop 0
	s_mov_b32 m0, s36
	s_nop 0
	global_load_lds_dwordx4 v213, s[24:25]
	s_add_u32 s30, s24, 0x40000
	s_addc_u32 s31, s25, 0
	s_mov_b32 m0, s37
	s_nop 0
	global_load_lds_dwordx4 v210, s[30:31]
	s_and_b64 vcc, exec, s[26:27]
	s_mov_b32 m0, s38
	s_nop 0
	global_load_lds_dwordx4 v213, s[30:31]
	s_mov_b32 m0, s34
	s_nop 0
	global_load_lds_dwordx4 v226, s[28:29]
	s_nop 0
	s_mov_b32 m0, s39
	s_nop 0
	global_load_lds_dwordx4 v227, s[28:29]
	s_mov_b64 s[30:31], -1
	s_cbranch_vccz .LBB0_1183
	s_waitcnt vmcnt(8)
	s_mov_b64 s[30:31], 0

.LBB0_1185:
	s_waitcnt lgkmcnt(0)
	v_cndmask_b32_e64 v228, v224, v220, s[0:1]
	v_cndmask_b32_e64 v229, v225, v221, s[0:1]
	s_barrier
	s_setprio 1
	s_waitcnt lgkmcnt(7)
	v_mfma_f32_16x16x32_bf16 v[62:65], v[146:149], v[186:189], v[62:65]
	v_mfma_f32_16x16x32_bf16 v[58:61], v[154:157], v[186:189], v[58:61]
	s_waitcnt lgkmcnt(5)
	v_mfma_f32_16x16x32_bf16 v[46:49], v[146:149], v[178:181], v[46:49]
	v_mfma_f32_16x16x32_bf16 v[42:45], v[154:157], v[178:181], v[42:45]
	s_waitcnt lgkmcnt(3)
	v_mfma_f32_16x16x32_bf16 v[22:25], v[146:149], v[170:173], v[22:25]
	v_mfma_f32_16x16x32_bf16 v[18:21], v[154:157], v[170:173], v[18:21]
	s_waitcnt lgkmcnt(1)
	v_mfma_f32_16x16x32_bf16 v[6:9], v[146:149], v[162:165], v[6:9]
	v_mfma_f32_16x16x32_bf16 v[2:5], v[154:157], v[162:165], v[2:5]
	v_mfma_f32_16x16x32_bf16 v[62:65], v[150:153], v[190:193], v[62:65]
	v_mfma_f32_16x16x32_bf16 v[58:61], v[158:161], v[190:193], v[58:61]
	v_mfma_f32_16x16x32_bf16 v[46:49], v[150:153], v[182:185], v[46:49]
	v_mfma_f32_16x16x32_bf16 v[42:45], v[158:161], v[182:185], v[42:45]
	v_mfma_f32_16x16x32_bf16 v[22:25], v[150:153], v[174:177], v[22:25]
	v_mfma_f32_16x16x32_bf16 v[18:21], v[158:161], v[174:177], v[18:21]
	s_waitcnt lgkmcnt(0)
	v_mfma_f32_16x16x32_bf16 v[6:9], v[150:153], v[166:169], v[6:9]
	v_mfma_f32_16x16x32_bf16 v[2:5], v[158:161], v[166:169], v[2:5]
	s_setprio 0
	s_setprio 1
	v_mfma_f32_16x16x32_bf16 v[54:57], v[130:133], v[186:189], v[54:57]
	v_mfma_f32_16x16x32_bf16 v[50:53], v[138:141], v[186:189], v[50:53]
	v_mfma_f32_16x16x32_bf16 v[30:33], v[130:133], v[178:181], v[30:33]
	v_mfma_f32_16x16x32_bf16 v[26:29], v[138:141], v[178:181], v[26:29]
	v_mfma_f32_16x16x32_bf16 v[38:41], v[130:133], v[170:173], v[38:41]
	v_mfma_f32_16x16x32_bf16 v[34:37], v[138:141], v[170:173], v[34:37]
	v_mfma_f32_16x16x32_bf16 v[14:17], v[130:133], v[162:165], v[14:17]
	v_mfma_f32_16x16x32_bf16 v[10:13], v[138:141], v[162:165], v[10:13]
	v_mfma_f32_16x16x32_bf16 v[54:57], v[134:137], v[190:193], v[54:57]
	v_mfma_f32_16x16x32_bf16 v[50:53], v[142:145], v[190:193], v[50:53]
	v_mfma_f32_16x16x32_bf16 v[30:33], v[134:137], v[182:185], v[30:33]
	v_mfma_f32_16x16x32_bf16 v[26:29], v[142:145], v[182:185], v[26:29]
	v_mfma_f32_16x16x32_bf16 v[38:41], v[134:137], v[174:177], v[38:41]
	v_mfma_f32_16x16x32_bf16 v[34:37], v[142:145], v[174:177], v[34:37]
	v_mfma_f32_16x16x32_bf16 v[14:17], v[134:137], v[166:169], v[14:17]
	v_mfma_f32_16x16x32_bf16 v[10:13], v[142:145], v[166:169], v[10:13]
	s_setprio 0
	s_barrier
	v_add_u32_e32 v130, 0x18000, v216
	v_add_u32_e32 v142, 0x1c000, v216
	ds_read_b128 v[146:149], v130
	ds_read_b128 v[150:153], v130 offset:1024
	ds_read_b128 v[154:157], v130 offset:2048
	ds_read_b128 v[158:161], v130 offset:3072
	ds_read_b128 v[130:133], v142
	ds_read_b128 v[134:137], v142 offset:1024
	ds_read_b128 v[138:141], v142 offset:2048
	ds_read_b128 v[142:145], v142 offset:3072
	ds_read_b128 v[186:189], v217 offset:32768
	ds_read_b128 v[190:193], v217 offset:33792
	ds_read_b128 v[178:181], v217 offset:34816
	ds_read_b128 v[182:185], v217 offset:35840
	ds_read_b128 v[170:173], v217 offset:36864
	ds_read_b128 v[174:177], v217 offset:37888
	ds_read_b128 v[162:165], v217 offset:38912
	ds_read_b128 v[166:169], v217 offset:39936
	s_mov_b32 m0, s40
	s_nop 0
	global_load_lds_dwordx4 v228, s[28:29]
	s_and_b64 vcc, exec, s[26:27]
	s_mov_b32 m0, s41
	s_nop 0
	global_load_lds_dwordx4 v229, s[28:29]
	s_mov_b64 s[0:1], -1
	s_cbranch_vccz .LBB0_1187
	s_waitcnt vmcnt(8)
	s_mov_b64 s[0:1], 0

.LBB0_1189:
	v_cndmask_b32_e64 v130, 0, 1, s[18:19]
	v_cmp_ne_u32_e64 s[0:1], 1, v130
	s_andn2_b64 vcc, exec, s[18:19]
	s_cbranch_vccnz .LBB0_1191
	s_mov_b32 m0, s49
	s_nop 0
	global_load_lds_dwordx4 v220, s[10:11]
	s_nop 0
	s_mov_b32 m0, s50
	s_nop 0
	global_load_lds_dwordx4 v221, s[10:11]

.LBB0_1633:
	s_or_b64 exec, exec, s[0:1]
	v_readlane_b32 s0, v244, 12
	s_waitcnt vmcnt(7)
	v_mov_b32_e32 v2, v0
	s_waitcnt lgkmcnt(0)
	v_mov_b32_e32 v1, s0
	s_barrier
	ds_read_b32 v1, v1
	v_readlane_b32 s1, v243, 0
	v_readlane_b32 s5, v243, 51
	v_readfirstlane_b32 s12, v2
	s_waitcnt lgkmcnt(0)
	v_readfirstlane_b32 s4, v1
	s_add_i32 s0, s4, 7
	s_ashr_i32 s0, s0, 3
	s_mul_i32 s1, s0, s1
	s_add_i32 s52, s1, s5
	s_cmp_lt_i32 s5, s0
	s_cselect_b64 s[0:1], -1, 0
	s_cmp_lt_i32 s52, s4
	s_cselect_b64 s[4:5], -1, 0
	s_and_b64 s[0:1], s[0:1], s[4:5]
	s_andn2_b64 vcc, exec, s[0:1]
	s_cbranch_vccnz .LBB0_1663
	v_bfe_i32 v4, v2, 27, 1
	v_lshlrev_b32_e32 v3, 4, v2
	v_lshrrev_b32_e32 v4, 22, v4
	v_add_u32_e32 v4, v3, v4
	v_and_b32_e32 v4, 0xfffffc00, v4
	v_sub_u32_e32 v4, v3, v4
	v_ashrrev_i32_e32 v1, 31, v2
	v_lshrrev_b32_e32 v5, 4, v4
	v_lshrrev_b32_e32 v1, 26, v1
	v_bitop3_b32 v4, v5, v4, 32 bitop3:0x6c
	v_add_u32_e32 v1, v2, v1
	s_waitcnt vmcnt(6)
	v_ashrrev_i32_e32 v6, 31, v4
	v_ashrrev_i32_e32 v1, 6, v1
	v_lshrrev_b32_e32 v6, 26, v6
	v_lshlrev_b32_e32 v5, 3, v1
	v_add_u32_e32 v6, v4, v6
	v_and_b32_e32 v5, -16, v5
	v_ashrrev_i32_e32 v7, 6, v6
	v_add_u32_e32 v12, v7, v5
	v_and_b32_e32 v5, 0xc0, v6
	v_sub_u32_e32 v4, v4, v5
	v_lshlrev_b32_e32 v1, 5, v1
	v_ashrrev_i16_sdwa v4, v203, sext(v4) dst_sel:DWORD dst_unused:UNUSED_PAD src0_sel:DWORD src1_sel:BYTE_0
	v_and_b32_e32 v1, 32, v1
	v_bfe_i32 v4, v4, 0, 16
	v_add_u32_e32 v3, 0x2000, v3
	v_add_lshl_u32 v1, v1, v4, 1
	v_ashrrev_i32_e32 v4, 31, v3
	v_lshlrev_b32_e32 v5, 1, v12
	v_lshrrev_b32_e32 v6, 2, v12
	v_and_b32_e32 v7, 3, v7
	s_mov_b32 s0, 0x3fffe0
	v_lshrrev_b32_e32 v4, 22, v4
	v_and_b32_e32 v5, 24, v5
	v_and_b32_e32 v6, 4, v6
	v_and_or_b32 v7, v12, s0, v7
	v_add_u32_e32 v4, v3, v4
	v_or3_b32 v5, v7, v6, v5
	v_ashrrev_i32_e32 v4, 10, v4
	v_lshl_add_u32 v210, v5, 10, v1
	v_mul_i32_i24_e32 v5, 0x400, v4
	v_sub_u32_e32 v3, v3, v5
	v_lshrrev_b32_e32 v5, 4, v3
	v_bitop3_b32 v3, v5, v3, 32 bitop3:0x6c
	v_ashrrev_i32_e32 v6, 31, v3
	v_lshrrev_b32_e32 v6, 26, v6
	v_lshlrev_b32_e32 v5, 3, v4
	v_add_u32_e32 v6, v3, v6
	v_and_b32_e32 v5, -16, v5
	v_ashrrev_i32_e32 v7, 6, v6
	v_add_u32_e32 v13, v7, v5
	v_and_b32_e32 v7, 3, v7
	v_and_b32_e32 v5, 0xc0, v6
	v_and_or_b32 v7, v13, s0, v7
	s_ashr_i32 s11, s12, 6
	v_readlane_b32 s0, v244, 22
	s_ashr_i32 s10, s12, 8
	v_sub_u32_e32 v3, v3, v5
	s_lshl_b32 s8, s11, 10
	s_lshl_b32 s0, s0, 25
	v_readlane_b32 s1, v243, 47
	v_lshlrev_b32_e32 v4, 5, v4
	v_ashrrev_i16_sdwa v3, v203, sext(v3) dst_sel:DWORD dst_unused:UNUSED_PAD src0_sel:DWORD src1_sel:BYTE_0
	v_lshlrev_b32_e32 v5, 1, v13
	v_lshrrev_b32_e32 v6, 2, v13
	s_add_u32 s6, s1, s0
	v_readlane_b32 s0, v243, 48
	v_and_b32_e32 v4, 32, v4
	v_bfe_i32 v3, v3, 0, 16
	v_and_b32_e32 v5, 24, v5
	v_and_b32_e32 v6, 4, v6
	s_addc_u32 s7, s0, 0
	v_readlane_b32 s0, v244, 13
	v_or3_b32 v5, v7, v6, v5
	v_add_lshl_u32 v211, v4, v3, 1
	v_mov_b32_e32 v3, s0
	v_lshl_add_u32 v212, v5, 10, v211
	ds_read2_b32 v[4:5], v3 offset1:1
	ds_read2_b32 v[6:7], v3 offset0:2 offset1:3
	ds_read2_b32 v[8:9], v3 offset0:4 offset1:5
	ds_read2_b32 v[10:11], v3 offset0:6 offset1:7
	v_readlane_b32 s0, v244, 17
	v_readlane_b32 s4, v244, 20
	v_lshlrev_b32_e32 v213, 2, v12
	v_lshlrev_b32_e32 v214, 2, v13
	s_waitcnt lgkmcnt(0)
	v_cmp_ge_i32_e32 vcc, s52, v10
	s_add_i32 s30, s8, 0
	s_add_i32 s31, s30, 0x10000
	v_cndmask_b32_e64 v3, 0, 1, vcc
	v_cmp_ge_i32_e32 vcc, s52, v11
	v_lshlrev_b32_e32 v3, 2, v3
	s_add_i32 s34, s30, 0x12000
	v_cndmask_b32_e64 v10, 0, 1, vcc
	v_cmp_ge_i32_e32 vcc, s52, v9
	v_lshlrev_b32_e32 v10, 3, v10
	v_or_b32_e32 v3, v10, v3
	v_cndmask_b32_e64 v9, 0, 1, vcc
	v_cmp_ge_i32_e32 vcc, s52, v8
	v_lshlrev_b32_e32 v9, 1, v9
	s_nop 0
	v_cndmask_b32_e64 v8, 0, 1, vcc
	v_cmp_ge_i32_e32 vcc, s52, v6
	v_or_b32_e32 v8, v8, v9
	v_and_b32_e32 v8, 3, v8
	v_cndmask_b32_e64 v6, 0, 1, vcc
	v_cmp_ge_i32_e32 vcc, s52, v7
	v_lshlrev_b32_e32 v6, 2, v6
	v_or_b32_e32 v3, v8, v3
	v_cndmask_b32_e64 v7, 0, 1, vcc
	v_cmp_ge_i32_e32 vcc, s52, v5
	v_lshlrev_b32_e32 v7, 3, v7
	v_or_b32_e32 v6, v7, v6
	v_cndmask_b32_e64 v5, 0, 1, vcc
	v_cmp_ge_i32_e32 vcc, s52, v4
	v_lshlrev_b32_e32 v5, 1, v5
	v_lshlrev_b32_e32 v3, 4, v3
	v_cndmask_b32_e64 v4, 0, 1, vcc
	v_or_b32_e32 v4, v4, v5
	v_and_b32_e32 v4, 3, v4
	v_or_b32_e32 v4, v4, v6
	v_and_b32_e32 v4, 15, v4
	v_mov_b32_e32 v6, s0
	v_or_b32_e32 v3, v4, v3
	ds_read2_b32 v[4:5], v6 offset1:1
	ds_read2_b32 v[6:7], v6 offset0:2 offset1:3
	v_readlane_b32 s0, v244, 19
	s_waitcnt lgkmcnt(0)
	v_cmp_ge_i32_e32 vcc, s52, v6
	s_nop 1
	v_cndmask_b32_e64 v6, 0, 1, vcc
	v_cmp_ge_i32_e32 vcc, s52, v7
	v_lshlrev_b32_e32 v6, 2, v6
	s_nop 0
	v_cndmask_b32_e64 v7, 0, 1, vcc
	v_cmp_ge_i32_e32 vcc, s52, v5
	v_lshlrev_b32_e32 v7, 3, v7
	v_or_b32_e32 v6, v7, v6
	v_cndmask_b32_e64 v5, 0, 1, vcc
	v_cmp_ge_i32_e32 vcc, s52, v4
	v_lshlrev_b32_e32 v5, 1, v5
	s_nop 0
	v_cndmask_b32_e64 v4, 0, 1, vcc
	v_or_b32_e32 v4, v4, v5
	v_and_b32_e32 v4, 3, v4
	v_or_b32_e32 v6, v4, v6
	v_mov_b32_e32 v4, s0
	ds_read2_b32 v[4:5], v4 offset1:1
	s_waitcnt lgkmcnt(0)
	v_cmp_ge_i32_e32 vcc, s52, v4
	v_mov_b32_e32 v4, s4
	ds_read_b32 v4, v4
	v_cmp_ge_i32_e64 s[0:1], s52, v5
	s_waitcnt lgkmcnt(0)
	v_cmp_ge_i32_e64 s[4:5], s52, v4
	v_lshlrev_b32_e32 v4, 8, v6
	v_or_b32_sdwa v3, v3, v4 dst_sel:DWORD dst_unused:UNUSED_PAD src0_sel:BYTE_0 src1_sel:DWORD
	v_cndmask_b32_e64 v4, 0, 1, s[4:5]
	v_and_b32_e32 v3, 0xfff, v3
	v_addc_co_u32_e64 v4, s[0:1], 0, v4, s[0:1]
	v_bcnt_u32_b32 v3, v3, 0
	v_readlane_b32 s0, v242, 13
	v_addc_co_u32_e32 v3, vcc, v4, v3, vcc
	s_nop 0
	v_add_u32_e32 v4, s0, v213
	v_add_u32_e32 v5, s0, v214
	ds_read_b32 v4, v4
	ds_read_b32 v5, v5
	v_readlane_b32 s0, v244, 21
	v_lshlrev_b32_e32 v194, 21, v3
	s_waitcnt lgkmcnt(1)
	v_add_u32_e32 v226, v4, v1
	s_waitcnt lgkmcnt(0)
	v_add_u32_e32 v223, v5, v211
	v_add_u32_e32 v5, s0, v213
	ds_read_b32 v5, v5
	s_waitcnt lgkmcnt(0)
	v_add_u32_e32 v224, v5, v1
	v_add_u32_e32 v5, s0, v214
	ds_read_b32 v5, v5
	v_readlane_b32 s0, v243, 55
	v_readlane_b32 s1, v243, 56
	s_waitcnt lgkmcnt(0)
	v_add_u32_e32 v225, v5, v211
	v_lshl_add_u64 v[4:5], s[6:7], 0, v[194:195]
	v_lshl_add_u64 v[4:5], v[4:5], 0, s[0:1]
	s_nop 0
	v_readfirstlane_b32 s5, v5
	v_readfirstlane_b32 s4, v4
	s_mov_b32 m0, s31
	s_nop 0
	global_load_lds_dwordx4 v210, s[4:5]
	s_nop 0
	s_mov_b32 m0, s34
	s_nop 0
	global_load_lds_dwordx4 v212, s[4:5]
	s_add_u32 s0, s4, 0x20000
	s_addc_u32 s1, s5, 0
	s_add_i32 s35, s30, 0x14000
	s_mov_b32 m0, s35
	s_nop 0
	global_load_lds_dwordx4 v210, s[0:1]
	s_add_i32 s36, s30, 0x16000
	s_mov_b32 m0, s36
	s_nop 0
	global_load_lds_dwordx4 v212, s[0:1]
	s_mov_b32 m0, s30
	s_nop 0
	global_load_lds_dwordx4 v226, s[2:3]
	s_add_i32 s37, s30, 0x2000
	s_mov_b32 m0, s37
	s_nop 0
	global_load_lds_dwordx4 v223, s[2:3]
	s_add_i32 s38, s30, 0x4000
	s_mov_b32 m0, s38
	s_nop 0
	global_load_lds_dwordx4 v224, s[2:3]
	s_add_i32 s39, s30, 0x6000
	s_mov_b32 m0, s39
	s_nop 0
	global_load_lds_dwordx4 v225, s[2:3]
	s_cmp_eq_u32 s10, 1
	s_cselect_b64 s[8:9], -1, 0
	s_cmp_lg_u32 s10, 1
	s_cbranch_scc1 .LBB0_1636
	s_barrier
.LBB0_1636:
	v_and_b32_e32 v4, 48, v2
	v_lshlrev_b32_e32 v5, 6, v2
	s_movk_i32 s1, 0x3c0
	v_and_or_b32 v4, v5, s1, v4
	v_lshlrev_b32_e32 v5, 2, v2
	s_lshl_b32 s0, s10, 13
	v_and_b32_e32 v5, 32, v5
	v_bitop3_b32 v6, v4, s0, v5 bitop3:0xde
	s_lshl_b32 s0, s11, 5
	s_and_b32 s15, s0, 0x60
	s_lshl_b32 s14, s10, 6
	s_lshl_b32 s0, s15, 7
	v_bitop3_b32 v4, s0, v4, v5 bitop3:0xf6
	s_add_u32 s0, s4, 0x80
	s_waitcnt vmcnt(2)
	s_barrier
	s_addc_u32 s1, s5, 0
	s_add_i32 s40, s30, 0x18000
	s_mov_b32 m0, s40
	s_nop 0
	global_load_lds_dwordx4 v210, s[0:1]
	s_add_i32 s41, s30, 0x1a000
	s_mov_b32 m0, s41
	s_nop 0
	global_load_lds_dwordx4 v212, s[0:1]
	s_add_u32 s10, s2, 0x80
	s_addc_u32 s11, s3, 0
	s_add_i32 s42, s30, 0x8000
	s_mov_b32 m0, s42
	s_nop 0
	global_load_lds_dwordx4 v226, s[10:11]
	s_add_i32 s43, s30, 0xa000
	s_mov_b32 m0, s43
	s_nop 0
	global_load_lds_dwordx4 v223, s[10:11]
	s_add_u32 s0, s4, 0x20080
	s_addc_u32 s1, s5, 0
	s_add_i32 s44, s30, 0x1c000
	s_mov_b32 m0, s44
	s_nop 0
	global_load_lds_dwordx4 v210, s[0:1]
	s_add_i32 s45, s30, 0x1e000
	s_mov_b32 m0, s45
	s_nop 0
	global_load_lds_dwordx4 v212, s[0:1]
	s_waitcnt vmcnt(6)
	s_add_i32 s47, s30, 0xc000
	v_lshrrev_b32_e32 v3, 1, v2
	s_cmpk_lt_u32 s12, 0x100
	v_readlane_b32 s0, v243, 53
	s_cselect_b64 s[12:13], -1, 0
	v_and_or_b32 v215, v2, 31, s14
	s_add_i32 s48, s30, 0xe000
	s_ashr_i32 s49, s18, 3
	v_and_or_b32 v216, v3, 16, s15
	s_mov_b32 s18, 0
	v_add_u32_e32 v217, 0, v4
	v_add_u32_e32 v218, 0, v6
	s_mov_b32 s53, s0
	v_mov_b32_e32 v220, v226
	v_mov_b32_e32 v219, v223
	v_mov_b32_e32 v221, v224
	v_mov_b32_e32 v222, v225
	s_mov_b64 s[16:17], s[4:5]
	s_barrier
	v_readlane_b32 s1, v243, 54
	s_waitcnt vmcnt(0)
	s_branch .LBB0_1639

.LBB0_1642:
	s_add_u32 s4, s24, 0x80
	s_waitcnt lgkmcnt(0)
	s_addc_u32 s5, s25, 0
	s_add_u32 s24, s22, 0x80
	s_addc_u32 s25, s23, 0
	s_barrier
	s_setprio 1
	s_waitcnt lgkmcnt(6)
	v_mfma_f32_16x16x128_f8f6f4 v[190:193], v[26:33], v[58:65], v[190:193]
	v_mfma_f32_16x16x128_f8f6f4 v[186:189], v[18:25], v[58:65], v[186:189]
	s_waitcnt lgkmcnt(4)
	v_mfma_f32_16x16x128_f8f6f4 v[174:177], v[26:33], v[50:57], v[174:177]
	v_mfma_f32_16x16x128_f8f6f4 v[170:173], v[18:25], v[50:57], v[170:173]
	s_waitcnt lgkmcnt(2)
	v_mfma_f32_16x16x128_f8f6f4 v[158:161], v[26:33], v[42:49], v[158:161]
	v_mfma_f32_16x16x128_f8f6f4 v[154:157], v[18:25], v[42:49], v[154:157]
	s_waitcnt lgkmcnt(0)
	v_mfma_f32_16x16x128_f8f6f4 v[142:145], v[26:33], v[34:41], v[142:145]
	v_mfma_f32_16x16x128_f8f6f4 v[138:141], v[18:25], v[34:41], v[138:141]
	s_setprio 0
	s_setprio 1
	v_mfma_f32_16x16x128_f8f6f4 v[182:185], v[10:17], v[58:65], v[182:185]
	v_mfma_f32_16x16x128_f8f6f4 v[178:181], v[2:9], v[58:65], v[178:181]
	v_mfma_f32_16x16x128_f8f6f4 v[166:169], v[10:17], v[50:57], v[166:169]
	v_mfma_f32_16x16x128_f8f6f4 v[162:165], v[2:9], v[50:57], v[162:165]
	v_mfma_f32_16x16x128_f8f6f4 v[150:153], v[10:17], v[42:49], v[150:153]
	v_mfma_f32_16x16x128_f8f6f4 v[146:149], v[2:9], v[42:49], v[146:149]
	v_mfma_f32_16x16x128_f8f6f4 v[134:137], v[10:17], v[34:41], v[134:137]
	v_mfma_f32_16x16x128_f8f6f4 v[130:133], v[2:9], v[34:41], v[130:133]
	s_setprio 0
	s_barrier
	ds_read_b128 v[34:37], v218 offset:49152
	ds_read_b128 v[38:41], v218 offset:50176
	ds_read_b128 v[42:45], v218 offset:51200
	ds_read_b128 v[46:49], v218 offset:52224
	ds_read_b128 v[50:53], v218 offset:53248
	ds_read_b128 v[54:57], v218 offset:54272
	ds_read_b128 v[58:61], v218 offset:55296
	ds_read_b128 v[62:65], v218 offset:56320
	s_mov_b32 m0, s40
	s_nop 0
	global_load_lds_dwordx4 v210, s[24:25]
	s_add_u32 s22, s22, 0x20080
	s_mov_b32 m0, s41
	s_nop 0
	global_load_lds_dwordx4 v212, s[24:25]
	s_addc_u32 s23, s23, 0
	s_mov_b32 m0, s44
	s_nop 0
	global_load_lds_dwordx4 v210, s[22:23]
	s_nop 0
	s_mov_b32 m0, s45
	s_nop 0
	global_load_lds_dwordx4 v212, s[22:23]
	s_mov_b32 m0, s42
	s_nop 0
	global_load_lds_dwordx4 v194, s[4:5]
	s_nop 0
	s_mov_b32 m0, s43
	s_nop 0
	global_load_lds_dwordx4 v227, s[4:5]
	s_waitcnt vmcnt(8)
	s_waitcnt lgkmcnt(0)
	s_barrier
	s_setprio 1
	s_waitcnt lgkmcnt(6)
	v_mfma_f32_16x16x128_f8f6f4 v[126:129], v[26:33], v[34:41], v[126:129]
	v_mfma_f32_16x16x128_f8f6f4 v[122:125], v[18:25], v[34:41], v[122:125]
	s_waitcnt lgkmcnt(4)
	v_mfma_f32_16x16x128_f8f6f4 v[110:113], v[26:33], v[42:49], v[110:113]
	v_mfma_f32_16x16x128_f8f6f4 v[106:109], v[18:25], v[42:49], v[106:109]
	s_waitcnt lgkmcnt(2)
	v_mfma_f32_16x16x128_f8f6f4 v[86:89], v[26:33], v[50:57], v[86:89]
	v_mfma_f32_16x16x128_f8f6f4 v[82:85], v[18:25], v[50:57], v[82:85]
	s_waitcnt lgkmcnt(0)
	v_mfma_f32_16x16x128_f8f6f4 v[70:73], v[26:33], v[58:65], v[70:73]
	v_mfma_f32_16x16x128_f8f6f4 v[66:69], v[18:25], v[58:65], v[66:69]
	s_setprio 0
	s_setprio 1
	v_mfma_f32_16x16x128_f8f6f4 v[118:121], v[10:17], v[34:41], v[118:121]
	v_mfma_f32_16x16x128_f8f6f4 v[114:117], v[2:9], v[34:41], v[114:117]
	v_mfma_f32_16x16x128_f8f6f4 v[102:105], v[10:17], v[42:49], v[102:105]
	v_mfma_f32_16x16x128_f8f6f4 v[90:93], v[2:9], v[42:49], v[90:93]
	v_mfma_f32_16x16x128_f8f6f4 v[98:101], v[10:17], v[50:57], v[98:101]
	v_mfma_f32_16x16x128_f8f6f4 v[94:97], v[2:9], v[50:57], v[94:97]
	v_mfma_f32_16x16x128_f8f6f4 v[78:81], v[10:17], v[58:65], v[78:81]
	v_mfma_f32_16x16x128_f8f6f4 v[74:77], v[2:9], v[58:65], v[74:77]
	s_setprio 0
	s_barrier
	s_add_i32 s55, s55, 2
	s_add_u32 s20, s20, 0x100
	s_addc_u32 s21, s21, 0
	s_cmp_gt_u32 s55, 5
	s_cbranch_scc1 .LBB0_1655
.LBB0_1643:
	v_add_u32_e32 v2, 0x10000, v217
	v_add_u32_e32 v6, 0x14000, v217
	ds_read_b128 v[26:29], v2
	ds_read_b128 v[30:33], v2 offset:1024
	ds_read_b128 v[18:21], v2 offset:2048
	ds_read_b128 v[22:25], v2 offset:3072
	ds_read_b128 v[10:13], v6
	ds_read_b128 v[14:17], v6 offset:1024
	ds_read_b128 v[2:5], v6 offset:2048
	ds_read_b128 v[6:9], v6 offset:3072
	s_add_u32 s24, s2, s20
	s_addc_u32 s25, s3, s21
	s_cmp_eq_u32 s20, 0
	s_cselect_b64 s[4:5], -1, 0
	ds_read_b128 v[58:61], v218
	ds_read_b128 v[62:65], v218 offset:1024
	ds_read_b128 v[50:53], v218 offset:2048
	ds_read_b128 v[54:57], v218 offset:3072
	ds_read_b128 v[42:45], v218 offset:4096
	ds_read_b128 v[46:49], v218 offset:5120
	ds_read_b128 v[34:37], v218 offset:6144
	ds_read_b128 v[38:41], v218 offset:7168
	s_and_b64 s[4:5], s[18:19], s[4:5]
	s_mov_b64 s[22:23], -1
	s_and_b64 vcc, exec, s[4:5]
	s_cbranch_vccnz .LBB0_1645
	s_add_u32 s22, s24, 0x80
	s_addc_u32 s23, s25, 0
	s_mov_b32 m0, s47
	s_nop 0
	global_load_lds_dwordx4 v224, s[22:23]
	s_nop 0
	s_mov_b32 m0, s48
	s_nop 0
	global_load_lds_dwordx4 v225, s[22:23]
	s_waitcnt vmcnt(8)
	s_mov_b64 s[22:23], 0

.LBB0_1647:
	s_xor_b64 s[26:27], s[4:5], -1
	s_add_u32 s24, s24, 0x100
	s_addc_u32 s25, s25, 0
	s_add_u32 s28, s15, s20
	s_addc_u32 s29, s54, s21
	s_cmpk_eq_i32 s20, 0x300
	s_cselect_b64 s[4:5], -1, 0
	s_waitcnt lgkmcnt(0)
	s_and_b64 s[22:23], s[4:5], exec
	v_cndmask_b32_e64 v194, v226, v220, s[4:5]
	s_cselect_b32 s25, s3, s25
	s_cselect_b32 s24, s2, s24
	v_cndmask_b32_e64 v227, v223, v219, s[4:5]
	s_cselect_b32 s23, s17, s29
	s_cselect_b32 s22, s16, s28
	s_barrier
	s_setprio 1
	s_waitcnt lgkmcnt(6)
	v_mfma_f32_16x16x128_f8f6f4 v[190:193], v[26:33], v[58:65], v[190:193]
	v_mfma_f32_16x16x128_f8f6f4 v[186:189], v[18:25], v[58:65], v[186:189]
	s_waitcnt lgkmcnt(4)
	v_mfma_f32_16x16x128_f8f6f4 v[174:177], v[26:33], v[50:57], v[174:177]
	v_mfma_f32_16x16x128_f8f6f4 v[170:173], v[18:25], v[50:57], v[170:173]
	s_waitcnt lgkmcnt(2)
	v_mfma_f32_16x16x128_f8f6f4 v[158:161], v[26:33], v[42:49], v[158:161]
	v_mfma_f32_16x16x128_f8f6f4 v[154:157], v[18:25], v[42:49], v[154:157]
	s_waitcnt lgkmcnt(0)
	v_mfma_f32_16x16x128_f8f6f4 v[142:145], v[26:33], v[34:41], v[142:145]
	v_mfma_f32_16x16x128_f8f6f4 v[138:141], v[18:25], v[34:41], v[138:141]
	s_setprio 0
	s_setprio 1
	v_mfma_f32_16x16x128_f8f6f4 v[182:185], v[10:17], v[58:65], v[182:185]
	v_mfma_f32_16x16x128_f8f6f4 v[178:181], v[2:9], v[58:65], v[178:181]
	v_mfma_f32_16x16x128_f8f6f4 v[166:169], v[10:17], v[50:57], v[166:169]
	v_mfma_f32_16x16x128_f8f6f4 v[162:165], v[2:9], v[50:57], v[162:165]
	v_mfma_f32_16x16x128_f8f6f4 v[150:153], v[10:17], v[42:49], v[150:153]
	v_mfma_f32_16x16x128_f8f6f4 v[146:149], v[2:9], v[42:49], v[146:149]
	v_mfma_f32_16x16x128_f8f6f4 v[134:137], v[10:17], v[34:41], v[134:137]
	v_mfma_f32_16x16x128_f8f6f4 v[130:133], v[2:9], v[34:41], v[130:133]
	s_setprio 0
	s_barrier
	ds_read_b128 v[58:61], v218 offset:16384
	ds_read_b128 v[62:65], v218 offset:17408
	ds_read_b128 v[50:53], v218 offset:18432
	ds_read_b128 v[54:57], v218 offset:19456
	ds_read_b128 v[42:45], v218 offset:20480
	ds_read_b128 v[46:49], v218 offset:21504
	ds_read_b128 v[34:37], v218 offset:22528
	ds_read_b128 v[38:41], v218 offset:23552
	s_mov_b32 m0, s31
	s_nop 0
	global_load_lds_dwordx4 v210, s[22:23]
	s_nop 0
	s_mov_b32 m0, s34
	s_nop 0
	global_load_lds_dwordx4 v212, s[22:23]
	s_add_u32 s28, s22, 0x20000
	s_addc_u32 s29, s23, 0
	s_mov_b32 m0, s35
	s_nop 0
	global_load_lds_dwordx4 v210, s[28:29]
	s_and_b64 vcc, exec, s[26:27]
	s_mov_b32 m0, s36
	s_nop 0
	global_load_lds_dwordx4 v212, s[28:29]
	s_mov_b32 m0, s30
	s_nop 0
	global_load_lds_dwordx4 v194, s[24:25]
	s_nop 0
	s_mov_b32 m0, s37
	s_nop 0
	global_load_lds_dwordx4 v227, s[24:25]
	s_mov_b64 s[28:29], -1
	s_cbranch_vccz .LBB0_1649
	s_waitcnt vmcnt(8)
	s_mov_b64 s[28:29], 0

.LBB0_1651:
	s_waitcnt lgkmcnt(0)
	v_cndmask_b32_e64 v228, v224, v221, s[4:5]
	v_cndmask_b32_e64 v229, v225, v222, s[4:5]
	s_barrier
	s_setprio 1
	s_waitcnt lgkmcnt(6)
	v_mfma_f32_16x16x128_f8f6f4 v[126:129], v[26:33], v[58:65], v[126:129]
	v_mfma_f32_16x16x128_f8f6f4 v[122:125], v[18:25], v[58:65], v[122:125]
	s_waitcnt lgkmcnt(4)
	v_mfma_f32_16x16x128_f8f6f4 v[110:113], v[26:33], v[50:57], v[110:113]
	v_mfma_f32_16x16x128_f8f6f4 v[106:109], v[18:25], v[50:57], v[106:109]
	s_waitcnt lgkmcnt(2)
	v_mfma_f32_16x16x128_f8f6f4 v[86:89], v[26:33], v[42:49], v[86:89]
	v_mfma_f32_16x16x128_f8f6f4 v[82:85], v[18:25], v[42:49], v[82:85]
	s_waitcnt lgkmcnt(0)
	v_mfma_f32_16x16x128_f8f6f4 v[70:73], v[26:33], v[34:41], v[70:73]
	v_mfma_f32_16x16x128_f8f6f4 v[66:69], v[18:25], v[34:41], v[66:69]
	s_setprio 0
	s_setprio 1
	v_mfma_f32_16x16x128_f8f6f4 v[118:121], v[10:17], v[58:65], v[118:121]
	v_mfma_f32_16x16x128_f8f6f4 v[114:117], v[2:9], v[58:65], v[114:117]
	v_mfma_f32_16x16x128_f8f6f4 v[102:105], v[10:17], v[50:57], v[102:105]
	v_mfma_f32_16x16x128_f8f6f4 v[90:93], v[2:9], v[50:57], v[90:93]
	v_mfma_f32_16x16x128_f8f6f4 v[98:101], v[10:17], v[42:49], v[98:101]
	v_mfma_f32_16x16x128_f8f6f4 v[94:97], v[2:9], v[42:49], v[94:97]
	v_mfma_f32_16x16x128_f8f6f4 v[78:81], v[10:17], v[34:41], v[78:81]
	v_mfma_f32_16x16x128_f8f6f4 v[74:77], v[2:9], v[34:41], v[74:77]
	s_setprio 0
	s_barrier
	v_add_u32_e32 v2, 0x18000, v217
	v_add_u32_e32 v6, 0x1c000, v217
	ds_read_b128 v[26:29], v2
	ds_read_b128 v[30:33], v2 offset:1024
	ds_read_b128 v[18:21], v2 offset:2048
	ds_read_b128 v[22:25], v2 offset:3072
	ds_read_b128 v[10:13], v6
	ds_read_b128 v[14:17], v6 offset:1024
	ds_read_b128 v[2:5], v6 offset:2048
	ds_read_b128 v[6:9], v6 offset:3072
	ds_read_b128 v[58:61], v218 offset:32768
	ds_read_b128 v[62:65], v218 offset:33792
	ds_read_b128 v[50:53], v218 offset:34816
	ds_read_b128 v[54:57], v218 offset:35840
	ds_read_b128 v[42:45], v218 offset:36864
	ds_read_b128 v[46:49], v218 offset:37888
	ds_read_b128 v[34:37], v218 offset:38912
	ds_read_b128 v[38:41], v218 offset:39936
	s_mov_b32 m0, s38
	s_nop 0
	global_load_lds_dwordx4 v228, s[24:25]
	s_and_b64 vcc, exec, s[26:27]
	s_mov_b32 m0, s39
	s_nop 0
	global_load_lds_dwordx4 v229, s[24:25]
	s_mov_b64 s[4:5], -1
	s_cbranch_vccz .LBB0_1653
	s_waitcnt vmcnt(8)
	s_mov_b64 s[4:5], 0

.LBB0_1655:
	s_and_b64 vcc, exec, s[0:1]
	s_cbranch_vccnz .LBB0_1657
	s_mov_b32 m0, s47
	s_nop 0
	global_load_lds_dwordx4 v221, s[10:11]
	s_nop 0
	s_mov_b32 m0, s48
	s_nop 0
	global_load_lds_dwordx4 v222, s[10:11]

.LBB0_1788:
	s_or_b64 exec, exec, s[0:1]
	v_readlane_b32 s0, v244, 12
	s_waitcnt vmcnt(7)
	v_mov_b32_e32 v2, v0
	s_waitcnt lgkmcnt(0)
	v_mov_b32_e32 v1, s0
	s_barrier
	ds_read_b32 v1, v1
	v_readlane_b32 s1, v243, 0
	v_readfirstlane_b32 s14, v2
	s_waitcnt lgkmcnt(0)
	v_readfirstlane_b32 s4, v1
	s_add_i32 s0, s4, 7
	s_ashr_i32 s0, s0, 3
	s_mul_i32 s8, s0, s1
	v_readlane_b32 s1, v246, 31
	s_add_i32 s8, s8, s1
	s_cmp_lt_i32 s1, s0
	s_cselect_b64 s[0:1], -1, 0
	s_cmp_lt_i32 s8, s4
	s_cselect_b64 s[4:5], -1, 0
	s_and_b64 s[0:1], s[0:1], s[4:5]
	s_andn2_b64 vcc, exec, s[0:1]
	s_cbranch_vccnz .LBB0_1818
	v_ashrrev_i32_e32 v1, 31, v2
	v_lshrrev_b32_e32 v1, 26, v1
	v_add_u32_e32 v1, v2, v1
	v_ashrrev_i32_e32 v4, 6, v1
	v_bfe_i32 v1, v2, 27, 1
	v_lshlrev_b32_e32 v3, 4, v2
	v_lshrrev_b32_e32 v1, 22, v1
	v_add_u32_e32 v1, v3, v1
	v_and_b32_e32 v1, 0xfffffc00, v1
	v_sub_u32_e32 v1, v3, v1
	v_lshrrev_b32_e32 v5, 4, v1
	v_bitop3_b32 v5, v5, v1, 32 bitop3:0x6c
	s_waitcnt vmcnt(6)
	v_ashrrev_i32_e32 v6, 31, v5
	v_lshrrev_b32_e32 v6, 26, v6
	v_add_u32_e32 v6, v5, v6
	v_ashrrev_i32_e32 v7, 6, v6
	v_and_b32_e32 v6, 0xc0, v6
	v_sub_u32_e32 v5, v5, v6
	v_lshlrev_b32_e32 v1, 3, v4
	v_lshlrev_b32_e32 v4, 5, v4
	v_ashrrev_i16_sdwa v5, v203, sext(v5) dst_sel:DWORD dst_unused:UNUSED_PAD src0_sel:DWORD src1_sel:BYTE_0
	v_and_b32_e32 v4, 32, v4
	v_bfe_i32 v5, v5, 0, 16
	v_add_u32_e32 v3, 0x2000, v3
	v_add_lshl_u32 v210, v4, v5, 1
	v_ashrrev_i32_e32 v4, 31, v3
	v_lshrrev_b32_e32 v4, 22, v4
	v_add_u32_e32 v4, v3, v4
	v_and_b32_e32 v1, -16, v1
	v_ashrrev_i32_e32 v4, 10, v4
	v_add_u32_e32 v1, v7, v1
	v_mul_i32_i24_e32 v5, 0x400, v4
	v_lshlrev_b32_e32 v6, 1, v1
	v_lshrrev_b32_e32 v8, 2, v1
	v_and_b32_e32 v7, 3, v7
	s_mov_b32 s0, 0x3fffe0
	v_sub_u32_e32 v3, v3, v5
	v_and_b32_e32 v6, 24, v6
	v_and_b32_e32 v8, 4, v8
	v_and_or_b32 v7, v1, s0, v7
	v_lshrrev_b32_e32 v5, 4, v3
	v_or3_b32 v6, v7, v8, v6
	v_bitop3_b32 v3, v5, v3, 32 bitop3:0x6c
	v_lshl_add_u32 v211, v6, 10, v210
	v_ashrrev_i32_e32 v6, 31, v3
	v_lshrrev_b32_e32 v6, 26, v6
	v_lshlrev_b32_e32 v5, 3, v4
	v_add_u32_e32 v6, v3, v6
	v_and_b32_e32 v5, -16, v5
	v_ashrrev_i32_e32 v7, 6, v6
	v_add_u32_e32 v212, v7, v5
	v_and_b32_e32 v7, 3, v7
	v_and_b32_e32 v5, 0xc0, v6
	v_and_or_b32 v7, v212, s0, v7
	s_ashr_i32 s11, s14, 6
	v_readlane_b32 s0, v244, 22
	s_ashr_i32 s10, s14, 8
	v_sub_u32_e32 v3, v3, v5
	s_lshl_b32 s9, s11, 10
	s_lshl_b32 s0, s0, 24
	v_readlane_b32 s1, v243, 61
	v_lshlrev_b32_e32 v4, 5, v4
	v_ashrrev_i16_sdwa v3, v203, sext(v3) dst_sel:DWORD dst_unused:UNUSED_PAD src0_sel:DWORD src1_sel:BYTE_0
	v_lshlrev_b32_e32 v5, 1, v212
	v_lshrrev_b32_e32 v6, 2, v212
	s_add_u32 s6, s1, s0
	v_readlane_b32 s0, v243, 62
	v_and_b32_e32 v4, 32, v4
	v_bfe_i32 v3, v3, 0, 16
	v_and_b32_e32 v5, 24, v5
	v_and_b32_e32 v6, 4, v6
	s_addc_u32 s7, s0, 0
	v_readlane_b32 s0, v244, 13
	v_or3_b32 v5, v7, v6, v5
	v_add_lshl_u32 v213, v4, v3, 1
	v_mov_b32_e32 v3, s0
	v_lshl_add_u32 v214, v5, 10, v213
	ds_read2_b32 v[4:5], v3 offset1:1
	ds_read2_b32 v[6:7], v3 offset0:2 offset1:3
	ds_read2_b32 v[8:9], v3 offset0:4 offset1:5
	ds_read2_b32 v[10:11], v3 offset0:6 offset1:7
	v_readlane_b32 s0, v244, 17
	v_readlane_b32 s4, v244, 20
	s_add_i32 s30, s9, 0
	s_add_i32 s31, s30, 0x10000
	s_waitcnt lgkmcnt(0)
	v_cmp_ge_i32_e32 vcc, s8, v10
	s_add_i32 s34, s30, 0x12000
	s_nop 0
	v_cndmask_b32_e64 v3, 0, 1, vcc
	v_cmp_ge_i32_e32 vcc, s8, v11
	v_lshlrev_b32_e32 v3, 2, v3
	s_nop 0
	v_cndmask_b32_e64 v10, 0, 1, vcc
	v_cmp_ge_i32_e32 vcc, s8, v9
	v_lshlrev_b32_e32 v10, 3, v10
	v_or_b32_e32 v3, v10, v3
	v_cndmask_b32_e64 v9, 0, 1, vcc
	v_cmp_ge_i32_e32 vcc, s8, v8
	v_lshlrev_b32_e32 v9, 1, v9
	s_nop 0
	v_cndmask_b32_e64 v8, 0, 1, vcc
	v_cmp_ge_i32_e32 vcc, s8, v6
	v_or_b32_e32 v8, v8, v9
	v_and_b32_e32 v8, 3, v8
	v_cndmask_b32_e64 v6, 0, 1, vcc
	v_cmp_ge_i32_e32 vcc, s8, v7
	v_lshlrev_b32_e32 v6, 2, v6
	v_or_b32_e32 v3, v8, v3
	v_cndmask_b32_e64 v7, 0, 1, vcc
	v_cmp_ge_i32_e32 vcc, s8, v5
	v_lshlrev_b32_e32 v7, 3, v7
	v_or_b32_e32 v6, v7, v6
	v_cndmask_b32_e64 v5, 0, 1, vcc
	v_cmp_ge_i32_e32 vcc, s8, v4
	v_lshlrev_b32_e32 v5, 1, v5
	v_lshlrev_b32_e32 v3, 4, v3
	v_cndmask_b32_e64 v4, 0, 1, vcc
	v_or_b32_e32 v4, v4, v5
	v_and_b32_e32 v4, 3, v4
	v_or_b32_e32 v4, v4, v6
	v_and_b32_e32 v4, 15, v4
	v_mov_b32_e32 v6, s0
	v_or_b32_e32 v3, v4, v3
	ds_read2_b32 v[4:5], v6 offset1:1
	ds_read2_b32 v[6:7], v6 offset0:2 offset1:3
	v_readlane_b32 s0, v244, 19
	s_waitcnt lgkmcnt(0)
	v_cmp_ge_i32_e32 vcc, s8, v6
	s_nop 1
	v_cndmask_b32_e64 v6, 0, 1, vcc
	v_cmp_ge_i32_e32 vcc, s8, v7
	v_lshlrev_b32_e32 v6, 2, v6
	s_nop 0
	v_cndmask_b32_e64 v7, 0, 1, vcc
	v_cmp_ge_i32_e32 vcc, s8, v5
	v_lshlrev_b32_e32 v7, 3, v7
	v_or_b32_e32 v6, v7, v6
	v_cndmask_b32_e64 v5, 0, 1, vcc
	v_cmp_ge_i32_e32 vcc, s8, v4
	v_lshlrev_b32_e32 v5, 1, v5
	s_nop 0
	v_cndmask_b32_e64 v4, 0, 1, vcc
	v_or_b32_e32 v4, v4, v5
	v_and_b32_e32 v4, 3, v4
	v_or_b32_e32 v6, v4, v6
	v_mov_b32_e32 v4, s0
	ds_read2_b32 v[4:5], v4 offset1:1
	s_waitcnt lgkmcnt(0)
	v_cmp_ge_i32_e32 vcc, s8, v4
	v_mov_b32_e32 v4, s4
	ds_read_b32 v4, v4
	v_cmp_ge_i32_e64 s[0:1], s8, v5
	s_waitcnt lgkmcnt(0)
	v_cmp_ge_i32_e64 s[4:5], s8, v4
	v_lshlrev_b32_e32 v4, 8, v6
	v_or_b32_sdwa v3, v3, v4 dst_sel:DWORD dst_unused:UNUSED_PAD src0_sel:BYTE_0 src1_sel:DWORD
	v_cndmask_b32_e64 v4, 0, 1, s[4:5]
	v_and_b32_e32 v3, 0xfff, v3
	v_addc_co_u32_e64 v4, s[0:1], 0, v4, s[0:1]
	v_bcnt_u32_b32 v3, v3, 0
	s_lshl_b32 s0, s8, 8
	v_addc_co_u32_e32 v3, vcc, v4, v3, vcc
	v_add_u32_e32 v4, s0, v1
	v_add_u32_e32 v5, s0, v212
	s_bitset1_b32 s0, 7
	v_lshl_add_u32 v223, v5, 10, v213
	v_add_u32_e32 v5, s0, v1
	v_lshl_add_u32 v224, v5, 10, v210
	v_add_u32_e32 v5, s0, v212
	v_lshlrev_b32_e32 v194, 20, v3
	v_readlane_b32 s0, v243, 25
	v_lshl_add_u32 v225, v5, 10, v213
	v_lshl_add_u32 v226, v4, 10, v210
	v_lshl_add_u64 v[4:5], s[6:7], 0, v[194:195]
	v_readlane_b32 s1, v243, 26
	s_nop 1
	v_lshl_add_u64 v[4:5], v[4:5], 0, s[0:1]
	s_nop 0
	v_readfirstlane_b32 s5, v5
	v_readfirstlane_b32 s4, v4
	s_mov_b32 m0, s31
	s_nop 0
	global_load_lds_dwordx4 v211, s[4:5]
	s_nop 0
	s_mov_b32 m0, s34
	s_nop 0
	global_load_lds_dwordx4 v214, s[4:5]
	s_add_u32 s0, s4, 0x20000
	s_addc_u32 s1, s5, 0
	s_add_i32 s35, s30, 0x14000
	s_mov_b32 m0, s35
	s_nop 0
	global_load_lds_dwordx4 v211, s[0:1]
	s_add_i32 s36, s30, 0x16000
	s_mov_b32 m0, s36
	s_nop 0
	global_load_lds_dwordx4 v214, s[0:1]
	s_add_i32 s37, s30, 0x2000
	v_readlane_b32 s8, v246, 11
	v_readlane_b32 s9, v246, 12
	s_mov_b32 m0, s30
	s_nop 0
	global_load_lds_dwordx4 v226, s[8:9]
	s_add_i32 s38, s30, 0x4000
	s_mov_b32 m0, s37
	s_nop 0
	global_load_lds_dwordx4 v223, s[8:9]
	s_add_i32 s39, s30, 0x6000
	s_mov_b32 m0, s38
	s_nop 0
	global_load_lds_dwordx4 v224, s[8:9]
	s_cmp_eq_u32 s10, 1
	s_mov_b32 m0, s39
	s_nop 0
	global_load_lds_dwordx4 v225, s[8:9]
	s_cselect_b64 s[8:9], -1, 0
	s_cmp_lg_u32 s10, 1
	s_cbranch_scc1 .LBB0_1791
	s_barrier
.LBB0_1791:
	v_and_b32_e32 v3, 15, v2
	v_lshlrev_b32_e32 v5, 6, v3
	v_lshlrev_b32_e32 v3, 2, v3
	v_and_or_b32 v5, v2, 48, v5
	s_lshl_b32 s0, s10, 13
	v_and_b32_e32 v6, 32, v3
	v_bitop3_b32 v7, v5, s0, v6 bitop3:0xde
	s_lshl_b32 s0, s11, 5
	s_and_b32 s15, s0, 0x60
	s_lshl_b32 s0, s15, 7
	v_bitop3_b32 v5, v5, s0, v6 bitop3:0xde
	s_add_u32 s0, s4, 0x80
	s_waitcnt vmcnt(2)
	s_barrier
	s_addc_u32 s1, s5, 0
	s_add_i32 s40, s30, 0x18000
	s_mov_b32 m0, s40
	s_nop 0
	global_load_lds_dwordx4 v211, s[0:1]
	s_add_i32 s41, s30, 0x1a000
	s_mov_b32 m0, s41
	s_nop 0
	global_load_lds_dwordx4 v214, s[0:1]
	v_readlane_b32 s0, v246, 11
	v_readlane_b32 s1, v246, 12
	s_add_u32 s10, s0, 0x80
	s_addc_u32 s11, s1, 0
	s_add_i32 s42, s30, 0x8000
	s_mov_b32 m0, s42
	s_nop 0
	global_load_lds_dwordx4 v226, s[10:11]
	s_add_i32 s43, s30, 0xa000
	s_mov_b32 m0, s43
	s_nop 0
	global_load_lds_dwordx4 v223, s[10:11]
	s_add_u32 s0, s4, 0x20080
	s_addc_u32 s1, s5, 0
	s_add_i32 s44, s30, 0x1c000
	s_mov_b32 m0, s44
	s_nop 0
	global_load_lds_dwordx4 v211, s[0:1]
	s_add_i32 s45, s30, 0x1e000
	s_add_i32 s47, s30, 0xc000
	s_mov_b32 m0, s45
	s_nop 0
	global_load_lds_dwordx4 v214, s[0:1]
	s_cmpk_lt_u32 s14, 0x100
	s_cselect_b64 s[12:13], -1, 0
	s_and_b32 s0, s14, 0xffffff00
	s_add_i32 s0, s0, 0
	v_lshrrev_b32_e32 v4, 1, v2
	s_waitcnt vmcnt(6)
	v_lshlrev_b32_e32 v2, 3, v2
	s_add_i32 s0, s0, 0x20400
	v_and_b32_e32 v4, 16, v4
	v_and_b32_e32 v2, 0x80, v2
	v_add_u32_e32 v215, s0, v3
	v_readlane_b32 s0, v243, 32
	s_add_i32 s48, s30, 0xe000
	s_ashr_i32 s49, s18, 3
	v_or3_b32 v216, v4, v2, s15
	s_mov_b32 s52, 0
	v_add_u32_e32 v217, 0, v5
	v_add_u32_e32 v218, 0, v7
	s_mov_b32 s51, s0
	v_mov_b32_e32 v221, v226
	v_mov_b32_e32 v219, v223
	v_mov_b32_e32 v220, v224
	v_mov_b32_e32 v222, v225
	s_mov_b64 s[16:17], s[4:5]
	s_barrier
	v_readlane_b32 s1, v243, 33
	s_waitcnt vmcnt(0)
	s_branch .LBB0_1794

.LBB0_1797:
	s_add_u32 s4, s24, 0x80
	s_waitcnt lgkmcnt(0)
	s_addc_u32 s5, s25, 0
	s_add_u32 s24, s22, 0x80
	s_addc_u32 s25, s23, 0
	s_barrier
	s_setprio 1
	s_waitcnt lgkmcnt(6)
	v_mfma_f32_16x16x128_f8f6f4 v[190:193], v[26:33], v[58:65], v[190:193]
	v_mfma_f32_16x16x128_f8f6f4 v[186:189], v[18:25], v[58:65], v[186:189]
	s_waitcnt lgkmcnt(4)
	v_mfma_f32_16x16x128_f8f6f4 v[174:177], v[26:33], v[50:57], v[174:177]
	v_mfma_f32_16x16x128_f8f6f4 v[170:173], v[18:25], v[50:57], v[170:173]
	s_waitcnt lgkmcnt(2)
	v_mfma_f32_16x16x128_f8f6f4 v[158:161], v[26:33], v[42:49], v[158:161]
	v_mfma_f32_16x16x128_f8f6f4 v[154:157], v[18:25], v[42:49], v[154:157]
	s_waitcnt lgkmcnt(0)
	v_mfma_f32_16x16x128_f8f6f4 v[142:145], v[26:33], v[34:41], v[142:145]
	v_mfma_f32_16x16x128_f8f6f4 v[138:141], v[18:25], v[34:41], v[138:141]
	s_setprio 0
	s_setprio 1
	v_mfma_f32_16x16x128_f8f6f4 v[182:185], v[10:17], v[58:65], v[182:185]
	v_mfma_f32_16x16x128_f8f6f4 v[178:181], v[2:9], v[58:65], v[178:181]
	v_mfma_f32_16x16x128_f8f6f4 v[166:169], v[10:17], v[50:57], v[166:169]
	v_mfma_f32_16x16x128_f8f6f4 v[162:165], v[2:9], v[50:57], v[162:165]
	v_mfma_f32_16x16x128_f8f6f4 v[150:153], v[10:17], v[42:49], v[150:153]
	v_mfma_f32_16x16x128_f8f6f4 v[146:149], v[2:9], v[42:49], v[146:149]
	v_mfma_f32_16x16x128_f8f6f4 v[134:137], v[10:17], v[34:41], v[134:137]
	v_mfma_f32_16x16x128_f8f6f4 v[130:133], v[2:9], v[34:41], v[130:133]
	s_setprio 0
	s_barrier
	ds_read_b128 v[34:37], v218 offset:49152
	ds_read_b128 v[38:41], v218 offset:50176
	ds_read_b128 v[42:45], v218 offset:51200
	ds_read_b128 v[46:49], v218 offset:52224
	ds_read_b128 v[50:53], v218 offset:53248
	ds_read_b128 v[54:57], v218 offset:54272
	ds_read_b128 v[58:61], v218 offset:55296
	ds_read_b128 v[62:65], v218 offset:56320
	s_mov_b32 m0, s40
	s_nop 0
	global_load_lds_dwordx4 v211, s[24:25]
	s_add_u32 s22, s22, 0x20080
	s_mov_b32 m0, s41
	s_nop 0
	global_load_lds_dwordx4 v214, s[24:25]
	s_addc_u32 s23, s23, 0
	s_mov_b32 m0, s44
	s_nop 0
	global_load_lds_dwordx4 v211, s[22:23]
	s_nop 0
	s_mov_b32 m0, s45
	s_nop 0
	global_load_lds_dwordx4 v214, s[22:23]
	s_mov_b32 m0, s42
	s_nop 0
	global_load_lds_dwordx4 v194, s[4:5]
	s_nop 0
	s_mov_b32 m0, s43
	s_nop 0
	global_load_lds_dwordx4 v227, s[4:5]
	s_waitcnt vmcnt(8)
	s_waitcnt lgkmcnt(0)
	s_barrier
	s_setprio 1
	s_waitcnt lgkmcnt(6)
	v_mfma_f32_16x16x128_f8f6f4 v[126:129], v[26:33], v[34:41], v[126:129]
	v_mfma_f32_16x16x128_f8f6f4 v[122:125], v[18:25], v[34:41], v[122:125]
	s_waitcnt lgkmcnt(4)
	v_mfma_f32_16x16x128_f8f6f4 v[110:113], v[26:33], v[42:49], v[110:113]
	v_mfma_f32_16x16x128_f8f6f4 v[106:109], v[18:25], v[42:49], v[106:109]
	s_waitcnt lgkmcnt(2)
	v_mfma_f32_16x16x128_f8f6f4 v[86:89], v[26:33], v[50:57], v[86:89]
	v_mfma_f32_16x16x128_f8f6f4 v[74:77], v[18:25], v[50:57], v[74:77]
	s_waitcnt lgkmcnt(0)
	v_mfma_f32_16x16x128_f8f6f4 v[70:73], v[26:33], v[58:65], v[70:73]
	v_mfma_f32_16x16x128_f8f6f4 v[66:69], v[18:25], v[58:65], v[66:69]
	s_setprio 0
	s_setprio 1
	v_mfma_f32_16x16x128_f8f6f4 v[118:121], v[10:17], v[34:41], v[118:121]
	v_mfma_f32_16x16x128_f8f6f4 v[114:117], v[2:9], v[34:41], v[114:117]
	v_mfma_f32_16x16x128_f8f6f4 v[94:97], v[10:17], v[42:49], v[94:97]
	v_mfma_f32_16x16x128_f8f6f4 v[90:93], v[2:9], v[42:49], v[90:93]
	v_mfma_f32_16x16x128_f8f6f4 v[102:105], v[10:17], v[50:57], v[102:105]
	v_mfma_f32_16x16x128_f8f6f4 v[98:101], v[2:9], v[50:57], v[98:101]
	v_mfma_f32_16x16x128_f8f6f4 v[82:85], v[10:17], v[58:65], v[82:85]
	v_mfma_f32_16x16x128_f8f6f4 v[78:81], v[2:9], v[58:65], v[78:81]
	s_setprio 0
	s_barrier
	s_add_i32 s54, s54, 2
	s_add_u32 s20, s20, 0x100
	s_addc_u32 s21, s21, 0
	s_cmp_gt_u32 s54, 5
	s_cbranch_scc1 .LBB0_1810
.LBB0_1798:
	v_add_u32_e32 v2, 0x10000, v217
	v_add_u32_e32 v6, 0x14000, v217
	ds_read_b128 v[26:29], v2
	ds_read_b128 v[30:33], v2 offset:1024
	ds_read_b128 v[18:21], v2 offset:2048
	ds_read_b128 v[22:25], v2 offset:3072
	ds_read_b128 v[10:13], v6
	ds_read_b128 v[14:17], v6 offset:1024
	ds_read_b128 v[2:5], v6 offset:2048
	ds_read_b128 v[6:9], v6 offset:3072
	v_readlane_b32 s4, v246, 11
	v_readlane_b32 s5, v246, 12
	s_add_u32 s24, s4, s20
	s_addc_u32 s25, s5, s21
	s_cmp_eq_u32 s20, 0
	s_cselect_b64 s[4:5], -1, 0
	ds_read_b128 v[58:61], v218
	ds_read_b128 v[62:65], v218 offset:1024
	ds_read_b128 v[50:53], v218 offset:2048
	ds_read_b128 v[54:57], v218 offset:3072
	ds_read_b128 v[42:45], v218 offset:4096
	ds_read_b128 v[46:49], v218 offset:5120
	ds_read_b128 v[34:37], v218 offset:6144
	ds_read_b128 v[38:41], v218 offset:7168
	s_and_b64 s[4:5], s[18:19], s[4:5]
	s_mov_b64 s[22:23], -1
	s_and_b64 vcc, exec, s[4:5]
	s_cbranch_vccnz .LBB0_1800
	s_add_u32 s22, s24, 0x80
	s_addc_u32 s23, s25, 0
	s_mov_b32 m0, s47
	s_nop 0
	global_load_lds_dwordx4 v224, s[22:23]
	s_nop 0
	s_mov_b32 m0, s48
	s_nop 0
	global_load_lds_dwordx4 v225, s[22:23]
	s_waitcnt vmcnt(8)
	s_mov_b64 s[22:23], 0

.LBB0_1802:
	s_xor_b64 s[26:27], s[4:5], -1
	s_add_u32 s24, s24, 0x100
	s_addc_u32 s25, s25, 0
	s_add_u32 s28, s15, s20
	s_addc_u32 s29, s53, s21
	s_cmpk_eq_i32 s20, 0x300
	s_cselect_b64 s[4:5], -1, 0
	s_and_b64 s[22:23], s[4:5], exec
	v_readlane_b32 s22, v246, 11
	s_waitcnt lgkmcnt(0)
	v_readlane_b32 s23, v246, 12
	v_cndmask_b32_e64 v194, v226, v221, s[4:5]
	s_cselect_b32 s25, s23, s25
	s_cselect_b32 s24, s22, s24
	v_cndmask_b32_e64 v227, v223, v219, s[4:5]
	s_cselect_b32 s23, s17, s29
	s_cselect_b32 s22, s16, s28
	s_barrier
	s_setprio 1
	s_waitcnt lgkmcnt(6)
	v_mfma_f32_16x16x128_f8f6f4 v[190:193], v[26:33], v[58:65], v[190:193]
	v_mfma_f32_16x16x128_f8f6f4 v[186:189], v[18:25], v[58:65], v[186:189]
	s_waitcnt lgkmcnt(4)
	v_mfma_f32_16x16x128_f8f6f4 v[174:177], v[26:33], v[50:57], v[174:177]
	v_mfma_f32_16x16x128_f8f6f4 v[170:173], v[18:25], v[50:57], v[170:173]
	s_waitcnt lgkmcnt(2)
	v_mfma_f32_16x16x128_f8f6f4 v[158:161], v[26:33], v[42:49], v[158:161]
	v_mfma_f32_16x16x128_f8f6f4 v[154:157], v[18:25], v[42:49], v[154:157]
	s_waitcnt lgkmcnt(0)
	v_mfma_f32_16x16x128_f8f6f4 v[142:145], v[26:33], v[34:41], v[142:145]
	v_mfma_f32_16x16x128_f8f6f4 v[138:141], v[18:25], v[34:41], v[138:141]
	s_setprio 0
	s_setprio 1
	v_mfma_f32_16x16x128_f8f6f4 v[182:185], v[10:17], v[58:65], v[182:185]
	v_mfma_f32_16x16x128_f8f6f4 v[178:181], v[2:9], v[58:65], v[178:181]
	v_mfma_f32_16x16x128_f8f6f4 v[166:169], v[10:17], v[50:57], v[166:169]
	v_mfma_f32_16x16x128_f8f6f4 v[162:165], v[2:9], v[50:57], v[162:165]
	v_mfma_f32_16x16x128_f8f6f4 v[150:153], v[10:17], v[42:49], v[150:153]
	v_mfma_f32_16x16x128_f8f6f4 v[146:149], v[2:9], v[42:49], v[146:149]
	v_mfma_f32_16x16x128_f8f6f4 v[134:137], v[10:17], v[34:41], v[134:137]
	v_mfma_f32_16x16x128_f8f6f4 v[130:133], v[2:9], v[34:41], v[130:133]
	s_setprio 0
	s_barrier
	ds_read_b128 v[58:61], v218 offset:16384
	ds_read_b128 v[62:65], v218 offset:17408
	ds_read_b128 v[50:53], v218 offset:18432
	ds_read_b128 v[54:57], v218 offset:19456
	ds_read_b128 v[42:45], v218 offset:20480
	ds_read_b128 v[46:49], v218 offset:21504
	ds_read_b128 v[34:37], v218 offset:22528
	ds_read_b128 v[38:41], v218 offset:23552
	s_mov_b32 m0, s31
	s_nop 0
	global_load_lds_dwordx4 v211, s[22:23]
	s_nop 0
	s_mov_b32 m0, s34
	s_nop 0
	global_load_lds_dwordx4 v214, s[22:23]
	s_add_u32 s28, s22, 0x20000
	s_addc_u32 s29, s23, 0
	s_mov_b32 m0, s35
	s_nop 0
	global_load_lds_dwordx4 v211, s[28:29]
	s_and_b64 vcc, exec, s[26:27]
	s_mov_b32 m0, s36
	s_nop 0
	global_load_lds_dwordx4 v214, s[28:29]
	s_mov_b32 m0, s30
	s_nop 0
	global_load_lds_dwordx4 v194, s[24:25]
	s_nop 0
	s_mov_b32 m0, s37
	s_nop 0
	global_load_lds_dwordx4 v227, s[24:25]
	s_mov_b64 s[28:29], -1
	s_cbranch_vccz .LBB0_1804
	s_waitcnt vmcnt(8)
	s_mov_b64 s[28:29], 0

.LBB0_1806:
	s_waitcnt lgkmcnt(0)
	v_cndmask_b32_e64 v228, v224, v220, s[4:5]
	v_cndmask_b32_e64 v229, v225, v222, s[4:5]
	s_barrier
	s_setprio 1
	s_waitcnt lgkmcnt(6)
	v_mfma_f32_16x16x128_f8f6f4 v[126:129], v[26:33], v[58:65], v[126:129]
	v_mfma_f32_16x16x128_f8f6f4 v[122:125], v[18:25], v[58:65], v[122:125]
	s_waitcnt lgkmcnt(4)
	v_mfma_f32_16x16x128_f8f6f4 v[110:113], v[26:33], v[50:57], v[110:113]
	v_mfma_f32_16x16x128_f8f6f4 v[106:109], v[18:25], v[50:57], v[106:109]
	s_waitcnt lgkmcnt(2)
	v_mfma_f32_16x16x128_f8f6f4 v[86:89], v[26:33], v[42:49], v[86:89]
	v_mfma_f32_16x16x128_f8f6f4 v[74:77], v[18:25], v[42:49], v[74:77]
	s_waitcnt lgkmcnt(0)
	v_mfma_f32_16x16x128_f8f6f4 v[70:73], v[26:33], v[34:41], v[70:73]
	v_mfma_f32_16x16x128_f8f6f4 v[66:69], v[18:25], v[34:41], v[66:69]
	s_setprio 0
	s_setprio 1
	v_mfma_f32_16x16x128_f8f6f4 v[118:121], v[10:17], v[58:65], v[118:121]
	v_mfma_f32_16x16x128_f8f6f4 v[114:117], v[2:9], v[58:65], v[114:117]
	v_mfma_f32_16x16x128_f8f6f4 v[94:97], v[10:17], v[50:57], v[94:97]
	v_mfma_f32_16x16x128_f8f6f4 v[90:93], v[2:9], v[50:57], v[90:93]
	v_mfma_f32_16x16x128_f8f6f4 v[102:105], v[10:17], v[42:49], v[102:105]
	v_mfma_f32_16x16x128_f8f6f4 v[98:101], v[2:9], v[42:49], v[98:101]
	v_mfma_f32_16x16x128_f8f6f4 v[82:85], v[10:17], v[34:41], v[82:85]
	v_mfma_f32_16x16x128_f8f6f4 v[78:81], v[2:9], v[34:41], v[78:81]
	s_setprio 0
	s_barrier
	v_add_u32_e32 v2, 0x18000, v217
	v_add_u32_e32 v6, 0x1c000, v217
	ds_read_b128 v[26:29], v2
	ds_read_b128 v[30:33], v2 offset:1024
	ds_read_b128 v[18:21], v2 offset:2048
	ds_read_b128 v[22:25], v2 offset:3072
	ds_read_b128 v[10:13], v6
	ds_read_b128 v[14:17], v6 offset:1024
	ds_read_b128 v[2:5], v6 offset:2048
	ds_read_b128 v[6:9], v6 offset:3072
	ds_read_b128 v[58:61], v218 offset:32768
	ds_read_b128 v[62:65], v218 offset:33792
	ds_read_b128 v[50:53], v218 offset:34816
	ds_read_b128 v[54:57], v218 offset:35840
	ds_read_b128 v[42:45], v218 offset:36864
	ds_read_b128 v[46:49], v218 offset:37888
	ds_read_b128 v[34:37], v218 offset:38912
	ds_read_b128 v[38:41], v218 offset:39936
	s_mov_b32 m0, s38
	s_nop 0
	global_load_lds_dwordx4 v228, s[24:25]
	s_and_b64 vcc, exec, s[26:27]
	s_mov_b32 m0, s39
	s_nop 0
	global_load_lds_dwordx4 v229, s[24:25]
	s_mov_b64 s[4:5], -1
	s_cbranch_vccz .LBB0_1808
	s_waitcnt vmcnt(8)
	s_mov_b64 s[4:5], 0

.LBB0_1810:
	s_and_b64 vcc, exec, s[0:1]
	s_cbranch_vccnz .LBB0_1812
	s_mov_b32 m0, s47
	s_nop 0
	global_load_lds_dwordx4 v220, s[10:11]
	s_nop 0
	s_mov_b32 m0, s48
	s_nop 0
	global_load_lds_dwordx4 v222, s[10:11]
